# on top of SLOT transposition: removed the mid-block s_setprio 0/1 flip between the two 16-MFMA groups of every MFMA block
# speedup vs baseline: 1.0190x; 1.0190x over previous
; #define PG8_STAGE(bufoff, gbase, voff) do { _Pragma("unroll") for (int _i = 0; _i < 2; ++_i) \
;         __builtin_amdgcn_global_load_lds((const unsigned*)((const char*)(gbase) + (voff)[_i]), (LAS unsigned*)(lds + (bufoff) + ldsw + _i * 8192), 16, 0, 0); } while (0)
; #define PG8_LDA(dst, b, h) do { _Pragma("unroll") for (int m = 0; m < 4; ++m) _Pragma("unroll") for (int k = 0; k < 2; ++k) dst[m][k] = *(const LAS bf16x8*)(lds + PG8_SA(b, h) + ((aoff ^ (k * 64)) + m * 2048)); } while (0)
; #define PG8_LDB(dst, b, h) do { _Pragma("unroll") for (int n = 0; n < 2; ++n) _Pragma("unroll") for (int k = 0; k < 2; ++k) dst[n][k] = *(const LAS bf16x8*)(lds + PG8_SB(b, h) + ((boff ^ (k * 64)) + n * 2048)); } while (0)
; #define PG8_BAR __builtin_amdgcn_s_barrier()
;     ...
;             const bool last = (t == nt - 2);
;             const char* a1 = cA + (size_t)(t + 1) * kstepA;
;             const char* a2 = last ? nA : cA + (size_t)(t + 2) * kstepA; const char* b2 = last ? nB : cB + (size_t)(t + 2) * kstepB;
;             const char* a3 = a2 + kstepA; const char* b3 = b2 + kstepB;
;             unsigned vs[2][2];
;             if constexpr (GATHER) {
;                 if (last && has_next) {
; #pragma unroll
;                     for (int hh = 0; hh < 2; ++hh)
; #pragma unroll
;                         for (int i = 0; i < 2; ++i) voffN[hh][i] = (unsigned)idxl[(ui + 1) * 256 + hh * HALF + sR[i]] * (unsigned)(K * 2) + (unsigned)sC[i] * 2u;
;                 }
; #pragma unroll
;                 for (int hh = 0; hh < 2; ++hh)
; #pragma unroll
;                     for (int i = 0; i < 2; ++i) vs[hh][i] = last ? voffN[hh][i] : voffA[hh][i];
;             } else {
; #pragma unroll
;                 for (int hh = 0; hh < 2; ++hh)
; #pragma unroll
;                     for (int i = 0; i < 2; ++i) vs[hh][i] = voffA[hh][i];
;             }
;             PG8_LDB(B0, 0, 0); PG8_LDB(B1, 0, 1); PG8_SCHED; PG8_LDA(At, 0, 0); PG8_STAGE(PG8_SA(1, 1), a1, voffA[1]);
;             PG8_WAIT_V(8); PG8_WAIT_L(0); PG8_BAR; if (do0) { PG8_MMA(0, 0, At, B0); PG8_MMA(0, 1, At, B1); } PG8_BAR; PG8_SCHED;
;             PG8_LDA(At, 0, 1); PG8_STAGE(PG8_SB(0, 0), b2, voffB); PG8_STAGE(PG8_SB(0, 1), b2 + hstep, voffB); PG8_STAGE(PG8_SA(0, 0), a2, vs[0]);
;             PG8_WAIT_V(8); PG8_WAIT_L(0); PG8_BAR; if (do1) { PG8_MMA(1, 0, At, B0); PG8_MMA(1, 1, At, B1); } PG8_BAR; PG8_SCHED;
.LBB0_192:
	ds_read_b128 v[158:161], v166
	ds_read_b128 v[180:183], v167
	ds_read_b128 v[184:187], v168
	ds_read_b128 v[188:191], v169
	ds_read_b128 v[192:195], v170
	ds_read_b128 v[200:203], v171
	ds_read_b128 v[204:207], v172
	ds_read_b128 v[208:211], v173
	s_add_u32 s28, s4, 0x80
	s_addc_u32 s29, s5, 0
	s_cmp_eq_u32 s64, 12
	s_cselect_b32 s35, s17, s29
	s_cselect_b32 s34, s60, s28
	s_cselect_b32 s29, s19, s63
	s_cselect_b32 s28, s61, s62
	v_lshl_add_u64 v[162:163], s[4:5], 0, v[152:153]
	s_add_i32 m0, s25, 0xc000
	ds_read_b128 v[212:215], v174
	ds_read_b128 v[216:219], v174 offset:2048
	ds_read_b128 v[220:223], v175
	ds_read_b128 v[224:227], v175 offset:2048
	ds_read_b128 v[228:231], v174 offset:4096
	ds_read_b128 v[232:235], v174 offset:6144
	ds_read_b128 v[236:239], v175 offset:4096
	ds_read_b128 v[240:243], v175 offset:6144
	global_load_lds_dwordx4 v[162:163], off
	v_lshl_add_u64 v[162:163], s[4:5], 0, v[150:151]
	s_add_i32 m0, s25, 0xe000
	s_add_u32 s30, s28, 0x4000
	global_load_lds_dwordx4 v[162:163], off
	s_waitcnt vmcnt(8)
	s_waitcnt lgkmcnt(0)
	s_addc_u32 s31, s29, 0
	s_barrier
	s_setprio 1
	s_waitcnt lgkmcnt(0)
	v_mfma_f32_16x16x32_bf16 v[126:129], v[158:161], v[212:215], v[126:129]
	v_mfma_f32_16x16x32_bf16 v[122:125], v[184:187], v[212:215], v[122:125]
	v_mfma_f32_16x16x32_bf16 v[110:113], v[158:161], v[216:219], v[110:113]
	v_mfma_f32_16x16x32_bf16 v[106:109], v[184:187], v[216:219], v[106:109]
	v_mfma_f32_16x16x32_bf16 v[94:97], v[158:161], v[228:231], v[94:97]
	v_mfma_f32_16x16x32_bf16 v[90:93], v[184:187], v[228:231], v[90:93]
	v_mfma_f32_16x16x32_bf16 v[78:81], v[158:161], v[232:235], v[78:81]
	v_mfma_f32_16x16x32_bf16 v[74:77], v[184:187], v[232:235], v[74:77]
	v_mfma_f32_16x16x32_bf16 v[126:129], v[180:183], v[220:223], v[126:129]
	v_mfma_f32_16x16x32_bf16 v[122:125], v[188:191], v[220:223], v[122:125]
	v_mfma_f32_16x16x32_bf16 v[110:113], v[180:183], v[224:227], v[110:113]
	v_mfma_f32_16x16x32_bf16 v[106:109], v[188:191], v[224:227], v[106:109]
	v_mfma_f32_16x16x32_bf16 v[94:97], v[180:183], v[236:239], v[94:97]
	v_mfma_f32_16x16x32_bf16 v[90:93], v[188:191], v[236:239], v[90:93]
	v_mfma_f32_16x16x32_bf16 v[78:81], v[180:183], v[240:243], v[78:81]
	v_mfma_f32_16x16x32_bf16 v[74:77], v[188:191], v[240:243], v[74:77]
	v_mfma_f32_16x16x32_bf16 v[118:121], v[192:195], v[212:215], v[118:121]
	v_mfma_f32_16x16x32_bf16 v[114:117], v[204:207], v[212:215], v[114:117]
	v_mfma_f32_16x16x32_bf16 v[102:105], v[192:195], v[216:219], v[102:105]
	v_mfma_f32_16x16x32_bf16 v[98:101], v[204:207], v[216:219], v[98:101]
	v_mfma_f32_16x16x32_bf16 v[86:89], v[192:195], v[228:231], v[86:89]
	v_mfma_f32_16x16x32_bf16 v[82:85], v[204:207], v[228:231], v[82:85]
	v_mfma_f32_16x16x32_bf16 v[70:73], v[192:195], v[232:235], v[70:73]
	v_mfma_f32_16x16x32_bf16 v[66:69], v[204:207], v[232:235], v[66:69]
	v_mfma_f32_16x16x32_bf16 v[118:121], v[200:203], v[220:223], v[118:121]
	v_mfma_f32_16x16x32_bf16 v[114:117], v[208:211], v[220:223], v[114:117]
	v_mfma_f32_16x16x32_bf16 v[102:105], v[200:203], v[224:227], v[102:105]
	v_mfma_f32_16x16x32_bf16 v[98:101], v[208:211], v[224:227], v[98:101]
	v_mfma_f32_16x16x32_bf16 v[86:89], v[200:203], v[236:239], v[86:89]
	v_mfma_f32_16x16x32_bf16 v[82:85], v[208:211], v[236:239], v[82:85]
	v_mfma_f32_16x16x32_bf16 v[70:73], v[200:203], v[240:243], v[70:73]
	v_mfma_f32_16x16x32_bf16 v[66:69], v[208:211], v[240:243], v[66:69]
	s_setprio 0
	s_barrier
	s_add_i32 s65, s56, s37
	v_lshl_add_u64 v[162:163], s[28:29], 0, v[130:131]
	s_mov_b32 m0, s65
	ds_read_b128 v[212:215], v174 offset:16384
	ds_read_b128 v[216:219], v174 offset:18432
	ds_read_b128 v[220:223], v175 offset:16384
	ds_read_b128 v[224:227], v175 offset:18432
	ds_read_b128 v[228:231], v174 offset:20480
	ds_read_b128 v[232:235], v174 offset:22528
	ds_read_b128 v[236:239], v175 offset:20480
	ds_read_b128 v[240:243], v175 offset:22528
	global_load_lds_dwordx4 v[162:163], off
	s_add_i32 m0, s65, 0x2000
	s_add_u32 s66, s28, 0x40000
	v_lshl_add_u64 v[162:163], s[28:29], 0, v[132:133]
	s_addc_u32 s67, s29, 0
	s_add_i32 s65, s57, s37
	global_load_lds_dwordx4 v[162:163], off
	v_lshl_add_u64 v[162:163], s[66:67], 0, v[130:131]
	s_mov_b32 m0, s65
	v_lshl_add_u64 v[196:197], s[34:35], 0, v[136:137]
	global_load_lds_dwordx4 v[162:163], off
	v_lshl_add_u64 v[162:163], s[66:67], 0, v[132:133]
	s_add_i32 m0, s65, 0x2000
	s_nop 0
	global_load_lds_dwordx4 v[162:163], off
	v_lshl_add_u64 v[162:163], s[34:35], 0, v[134:135]
	s_mov_b32 m0, s25
	s_nop 0
	global_load_lds_dwordx4 v[162:163], off
	s_mov_b32 m0, s27
	s_nop 0
	global_load_lds_dwordx4 v[196:197], off
	s_waitcnt vmcnt(8)
	s_waitcnt lgkmcnt(0)
	s_barrier
; #define PG8_STAGE(bufoff, gbase, voff) do { _Pragma("unroll") for (int _i = 0; _i < 2; ++_i) \
;         __builtin_amdgcn_global_load_lds((const unsigned*)((const char*)(gbase) + (voff)[_i]), (LAS unsigned*)(lds + (bufoff) + ldsw + _i * 8192), 16, 0, 0); } while (0)
; #define PG8_LDA(dst, b, h) do { _Pragma("unroll") for (int m = 0; m < 4; ++m) _Pragma("unroll") for (int k = 0; k < 2; ++k) dst[m][k] = *(const LAS bf16x8*)(lds + PG8_SA(b, h) + ((aoff ^ (k * 64)) + m * 2048)); } while (0)
; #define PG8_LDB(dst, b, h) do { _Pragma("unroll") for (int n = 0; n < 2; ++n) _Pragma("unroll") for (int k = 0; k < 2; ++k) dst[n][k] = *(const LAS bf16x8*)(lds + PG8_SB(b, h) + ((boff ^ (k * 64)) + n * 2048)); } while (0)
; #define PG8_MMA(ai, bj, At, Bt) do { __builtin_amdgcn_s_setprio(1); _Pragma("unroll") for (int m = 0; m < 4; ++m) _Pragma("unroll") for (int n = 0; n < 2; ++n) _Pragma("unroll") for (int k = 0; k < 2; ++k) \
;         acc[ai][bj][m][n] = __builtin_amdgcn_mfma_f32_16x16x32_bf16(Bt[n][k], At[m][k], acc[ai][bj][m][n], 0, 0, 0); __builtin_amdgcn_s_setprio(0); } while (0)
; #define PG8_WAIT_V(n) asm volatile("s_waitcnt vmcnt(" #n ")" ::: "memory")
; #define PG8_WAIT_L(n) asm volatile("s_waitcnt lgkmcnt(" #n ")" ::: "memory")
; #define PG8_BAR __builtin_amdgcn_s_barrier()
; #define PG8_SCHED __builtin_amdgcn_sched_barrier(0)
;     ...
;             PG8_WAIT_V(8); PG8_WAIT_L(0); PG8_BAR; if (do1) { PG8_MMA(1, 0, At, B0); PG8_MMA(1, 1, At, B1); } PG8_BAR; PG8_SCHED;
;             PG8_LDB(B0, 1, 0); PG8_LDB(B1, 1, 1); PG8_SCHED; PG8_LDA(At, 1, 0); PG8_STAGE(PG8_SA(0, 1), a2, vs[1]);
;             PG8_WAIT_V(8); PG8_WAIT_L(0); PG8_BAR; if (do0) { PG8_MMA(0, 0, At, B0); PG8_MMA(0, 1, At, B1); } PG8_BAR; PG8_SCHED;
	s_setprio 1
	s_waitcnt lgkmcnt(0)
	v_mfma_f32_16x16x32_bf16 v[62:65], v[158:161], v[212:215], v[62:65]
	v_mfma_f32_16x16x32_bf16 v[58:61], v[184:187], v[212:215], v[58:61]
	v_mfma_f32_16x16x32_bf16 v[46:49], v[158:161], v[216:219], v[46:49]
	v_mfma_f32_16x16x32_bf16 v[42:45], v[184:187], v[216:219], v[42:45]
	v_mfma_f32_16x16x32_bf16 v[30:33], v[158:161], v[228:231], v[30:33]
	v_mfma_f32_16x16x32_bf16 v[26:29], v[184:187], v[228:231], v[26:29]
	v_mfma_f32_16x16x32_bf16 v[14:17], v[158:161], v[232:235], v[14:17]
	v_mfma_f32_16x16x32_bf16 v[10:13], v[184:187], v[232:235], v[10:13]
	v_mfma_f32_16x16x32_bf16 v[62:65], v[180:183], v[220:223], v[62:65]
	v_mfma_f32_16x16x32_bf16 v[58:61], v[188:191], v[220:223], v[58:61]
	v_mfma_f32_16x16x32_bf16 v[46:49], v[180:183], v[224:227], v[46:49]
	v_mfma_f32_16x16x32_bf16 v[42:45], v[188:191], v[224:227], v[42:45]
	v_mfma_f32_16x16x32_bf16 v[30:33], v[180:183], v[236:239], v[30:33]
	v_mfma_f32_16x16x32_bf16 v[26:29], v[188:191], v[236:239], v[26:29]
	v_mfma_f32_16x16x32_bf16 v[14:17], v[180:183], v[240:243], v[14:17]
	v_mfma_f32_16x16x32_bf16 v[10:13], v[188:191], v[240:243], v[10:13]
	v_mfma_f32_16x16x32_bf16 v[54:57], v[192:195], v[212:215], v[54:57]
	v_mfma_f32_16x16x32_bf16 v[50:53], v[204:207], v[212:215], v[50:53]
	v_mfma_f32_16x16x32_bf16 v[38:41], v[192:195], v[216:219], v[38:41]
	v_mfma_f32_16x16x32_bf16 v[34:37], v[204:207], v[216:219], v[34:37]
	v_mfma_f32_16x16x32_bf16 v[22:25], v[192:195], v[228:231], v[22:25]
	v_mfma_f32_16x16x32_bf16 v[18:21], v[204:207], v[228:231], v[18:21]
	v_mfma_f32_16x16x32_bf16 v[6:9], v[192:195], v[232:235], v[6:9]
	v_mfma_f32_16x16x32_bf16 v[2:5], v[204:207], v[232:235], v[2:5]
	v_mfma_f32_16x16x32_bf16 v[54:57], v[200:203], v[220:223], v[54:57]
	v_mfma_f32_16x16x32_bf16 v[50:53], v[208:211], v[220:223], v[50:53]
	v_mfma_f32_16x16x32_bf16 v[38:41], v[200:203], v[224:227], v[38:41]
	v_mfma_f32_16x16x32_bf16 v[34:37], v[208:211], v[224:227], v[34:37]
	v_mfma_f32_16x16x32_bf16 v[22:25], v[200:203], v[236:239], v[22:25]
	v_mfma_f32_16x16x32_bf16 v[18:21], v[208:211], v[236:239], v[18:21]
	v_mfma_f32_16x16x32_bf16 v[6:9], v[200:203], v[240:243], v[6:9]
	v_mfma_f32_16x16x32_bf16 v[2:5], v[208:211], v[240:243], v[2:5]
	s_setprio 0
	s_barrier
	s_add_i32 s65, 0, 0x18000
	v_add_u32_e32 v142, s65, v145
	v_add_u32_e32 v180, s65, v165
	s_add_i32 s66, 0, 0x1c000
	ds_read_b128 v[158:161], v142
	ds_read_b128 v[180:183], v180
	ds_read_b128 v[184:187], v176
	ds_read_b128 v[188:191], v177
	v_add_u32_e32 v142, s66, v145
	v_add_u32_e32 v199, s66, v165
	ds_read_b128 v[192:195], v142
	ds_read_b128 v[200:203], v199
	ds_read_b128 v[204:207], v178
	ds_read_b128 v[208:211], v179
	s_mov_b32 m0, s38
	v_lshl_add_u64 v[244:245], s[34:35], 0, v[138:139]
	ds_read_b128 v[212:215], v174 offset:32768
	ds_read_b128 v[216:219], v174 offset:34816
	ds_read_b128 v[220:223], v175 offset:32768
	ds_read_b128 v[224:227], v175 offset:34816
	ds_read_b128 v[228:231], v174 offset:36864
	ds_read_b128 v[232:235], v174 offset:38912
	ds_read_b128 v[236:239], v175 offset:36864
	ds_read_b128 v[240:243], v175 offset:38912
	global_load_lds_dwordx4 v[244:245], off
	v_lshl_add_u64 v[244:245], s[34:35], 0, v[140:141]
	s_mov_b32 m0, s39
	s_nop 0
	global_load_lds_dwordx4 v[244:245], off
	s_waitcnt vmcnt(8)
	s_waitcnt lgkmcnt(0)
	s_barrier
	s_setprio 1
	s_waitcnt lgkmcnt(0)
	v_mfma_f32_16x16x32_bf16 v[126:129], v[158:161], v[212:215], v[126:129]
	v_mfma_f32_16x16x32_bf16 v[122:125], v[184:187], v[212:215], v[122:125]
	v_mfma_f32_16x16x32_bf16 v[110:113], v[158:161], v[216:219], v[110:113]
	v_mfma_f32_16x16x32_bf16 v[106:109], v[184:187], v[216:219], v[106:109]
	v_mfma_f32_16x16x32_bf16 v[94:97], v[158:161], v[228:231], v[94:97]
	v_mfma_f32_16x16x32_bf16 v[90:93], v[184:187], v[228:231], v[90:93]
	v_mfma_f32_16x16x32_bf16 v[78:81], v[158:161], v[232:235], v[78:81]
	v_mfma_f32_16x16x32_bf16 v[74:77], v[184:187], v[232:235], v[74:77]
	v_mfma_f32_16x16x32_bf16 v[126:129], v[180:183], v[220:223], v[126:129]
	v_mfma_f32_16x16x32_bf16 v[122:125], v[188:191], v[220:223], v[122:125]
	v_mfma_f32_16x16x32_bf16 v[110:113], v[180:183], v[224:227], v[110:113]
	v_mfma_f32_16x16x32_bf16 v[106:109], v[188:191], v[224:227], v[106:109]
	v_mfma_f32_16x16x32_bf16 v[94:97], v[180:183], v[236:239], v[94:97]
	v_mfma_f32_16x16x32_bf16 v[90:93], v[188:191], v[236:239], v[90:93]
	v_mfma_f32_16x16x32_bf16 v[78:81], v[180:183], v[240:243], v[78:81]
	v_mfma_f32_16x16x32_bf16 v[74:77], v[188:191], v[240:243], v[74:77]
	v_mfma_f32_16x16x32_bf16 v[118:121], v[192:195], v[212:215], v[118:121]
	v_mfma_f32_16x16x32_bf16 v[114:117], v[204:207], v[212:215], v[114:117]
	v_mfma_f32_16x16x32_bf16 v[102:105], v[192:195], v[216:219], v[102:105]
	v_mfma_f32_16x16x32_bf16 v[98:101], v[204:207], v[216:219], v[98:101]
	v_mfma_f32_16x16x32_bf16 v[86:89], v[192:195], v[228:231], v[86:89]
	v_mfma_f32_16x16x32_bf16 v[82:85], v[204:207], v[228:231], v[82:85]
	v_mfma_f32_16x16x32_bf16 v[70:73], v[192:195], v[232:235], v[70:73]
	v_mfma_f32_16x16x32_bf16 v[66:69], v[204:207], v[232:235], v[66:69]
	v_mfma_f32_16x16x32_bf16 v[118:121], v[200:203], v[220:223], v[118:121]
	v_mfma_f32_16x16x32_bf16 v[114:117], v[208:211], v[220:223], v[114:117]
	v_mfma_f32_16x16x32_bf16 v[102:105], v[200:203], v[224:227], v[102:105]
	v_mfma_f32_16x16x32_bf16 v[98:101], v[208:211], v[224:227], v[98:101]
	v_mfma_f32_16x16x32_bf16 v[86:89], v[200:203], v[236:239], v[86:89]
	v_mfma_f32_16x16x32_bf16 v[82:85], v[208:211], v[236:239], v[82:85]
	v_mfma_f32_16x16x32_bf16 v[70:73], v[200:203], v[240:243], v[70:73]
	v_mfma_f32_16x16x32_bf16 v[66:69], v[208:211], v[240:243], v[66:69]
	s_setprio 0
	s_barrier
; #define PG8_STAGE(bufoff, gbase, voff) do { _Pragma("unroll") for (int _i = 0; _i < 2; ++_i) \
;         __builtin_amdgcn_global_load_lds((const unsigned*)((const char*)(gbase) + (voff)[_i]), (LAS unsigned*)(lds + (bufoff) + ldsw + _i * 8192), 16, 0, 0); } while (0)
; #define PG8_LDA(dst, b, h) do { _Pragma("unroll") for (int m = 0; m < 4; ++m) _Pragma("unroll") for (int k = 0; k < 2; ++k) dst[m][k] = *(const LAS bf16x8*)(lds + PG8_SA(b, h) + ((aoff ^ (k * 64)) + m * 2048)); } while (0)
; #define PG8_MMA(ai, bj, At, Bt) do { __builtin_amdgcn_s_setprio(1); _Pragma("unroll") for (int m = 0; m < 4; ++m) _Pragma("unroll") for (int n = 0; n < 2; ++n) _Pragma("unroll") for (int k = 0; k < 2; ++k) \
;         acc[ai][bj][m][n] = __builtin_amdgcn_mfma_f32_16x16x32_bf16(Bt[n][k], At[m][k], acc[ai][bj][m][n], 0, 0, 0); __builtin_amdgcn_s_setprio(0); } while (0)
; #define PG8_WAIT_V(n) asm volatile("s_waitcnt vmcnt(" #n ")" ::: "memory")
; #define PG8_WAIT_L(n) asm volatile("s_waitcnt lgkmcnt(" #n ")" ::: "memory")
; #define PG8_BAR __builtin_amdgcn_s_barrier()
; #define PG8_SCHED __builtin_amdgcn_sched_barrier(0)
;     ...
;             PG8_LDA(At, 1, 1); PG8_STAGE(PG8_SB(1, 0), b3, voffB); PG8_STAGE(PG8_SB(1, 1), b3 + hstep, voffB); PG8_STAGE(PG8_SA(1, 0), a3, vs[0]);
;             PG8_WAIT_V(8); PG8_WAIT_L(0); PG8_BAR; if (do1) { PG8_MMA(1, 0, At, B0); PG8_MMA(1, 1, At, B1); } PG8_BAR; PG8_SCHED;
;         }
;         if (wr == 0) PG8_BAR;
	s_add_i32 s34, s65, s37
	v_lshl_add_u64 v[244:245], s[30:31], 0, v[130:131]
	s_mov_b32 m0, s34
	ds_read_b128 v[212:215], v174 offset:49152
	ds_read_b128 v[216:219], v174 offset:51200
	ds_read_b128 v[220:223], v175 offset:49152
	ds_read_b128 v[224:227], v175 offset:51200
	ds_read_b128 v[228:231], v174 offset:53248
	ds_read_b128 v[232:235], v174 offset:55296
	ds_read_b128 v[236:239], v175 offset:53248
	ds_read_b128 v[240:243], v175 offset:55296
	global_load_lds_dwordx4 v[244:245], off
	s_add_i32 m0, s34, 0x2000
	s_add_u32 s28, s28, 0x44000
	v_lshl_add_u64 v[244:245], s[30:31], 0, v[132:133]
	s_addc_u32 s29, s29, 0
	s_add_i32 s30, s66, s37
	global_load_lds_dwordx4 v[244:245], off
	v_lshl_add_u64 v[244:245], s[28:29], 0, v[130:131]
	s_mov_b32 m0, s30
	v_lshl_add_u64 v[162:163], v[162:163], 0, s[8:9]
	global_load_lds_dwordx4 v[244:245], off
	v_lshl_add_u64 v[244:245], s[28:29], 0, v[132:133]
	s_add_i32 m0, s30, 0x2000
	s_nop 0
	global_load_lds_dwordx4 v[244:245], off
	s_mov_b32 m0, s51
	s_nop 0
	global_load_lds_dwordx4 v[162:163], off
	v_lshl_add_u64 v[162:163], v[196:197], 0, s[8:9]
	s_mov_b32 m0, s54
	s_nop 0
	global_load_lds_dwordx4 v[162:163], off
	s_waitcnt vmcnt(8)
	s_waitcnt lgkmcnt(0)
	s_barrier
	s_setprio 1
	s_waitcnt lgkmcnt(0)
	v_mfma_f32_16x16x32_bf16 v[62:65], v[158:161], v[212:215], v[62:65]
	v_mfma_f32_16x16x32_bf16 v[58:61], v[184:187], v[212:215], v[58:61]
	v_mfma_f32_16x16x32_bf16 v[46:49], v[158:161], v[216:219], v[46:49]
	v_mfma_f32_16x16x32_bf16 v[42:45], v[184:187], v[216:219], v[42:45]
	v_mfma_f32_16x16x32_bf16 v[30:33], v[158:161], v[228:231], v[30:33]
	v_mfma_f32_16x16x32_bf16 v[26:29], v[184:187], v[228:231], v[26:29]
	v_mfma_f32_16x16x32_bf16 v[14:17], v[158:161], v[232:235], v[14:17]
	v_mfma_f32_16x16x32_bf16 v[10:13], v[184:187], v[232:235], v[10:13]
	v_mfma_f32_16x16x32_bf16 v[62:65], v[180:183], v[220:223], v[62:65]
	v_mfma_f32_16x16x32_bf16 v[58:61], v[188:191], v[220:223], v[58:61]
	v_mfma_f32_16x16x32_bf16 v[46:49], v[180:183], v[224:227], v[46:49]
	v_mfma_f32_16x16x32_bf16 v[42:45], v[188:191], v[224:227], v[42:45]
	v_mfma_f32_16x16x32_bf16 v[30:33], v[180:183], v[236:239], v[30:33]
	v_mfma_f32_16x16x32_bf16 v[26:29], v[188:191], v[236:239], v[26:29]
	v_mfma_f32_16x16x32_bf16 v[14:17], v[180:183], v[240:243], v[14:17]
	v_mfma_f32_16x16x32_bf16 v[10:13], v[188:191], v[240:243], v[10:13]
	v_mfma_f32_16x16x32_bf16 v[54:57], v[192:195], v[212:215], v[54:57]
	v_mfma_f32_16x16x32_bf16 v[50:53], v[204:207], v[212:215], v[50:53]
	v_mfma_f32_16x16x32_bf16 v[38:41], v[192:195], v[216:219], v[38:41]
	v_mfma_f32_16x16x32_bf16 v[34:37], v[204:207], v[216:219], v[34:37]
	v_mfma_f32_16x16x32_bf16 v[22:25], v[192:195], v[228:231], v[22:25]
	v_mfma_f32_16x16x32_bf16 v[18:21], v[204:207], v[228:231], v[18:21]
	v_mfma_f32_16x16x32_bf16 v[6:9], v[192:195], v[232:235], v[6:9]
	v_mfma_f32_16x16x32_bf16 v[2:5], v[204:207], v[232:235], v[2:5]
	v_mfma_f32_16x16x32_bf16 v[54:57], v[200:203], v[220:223], v[54:57]
	v_mfma_f32_16x16x32_bf16 v[50:53], v[208:211], v[220:223], v[50:53]
	v_mfma_f32_16x16x32_bf16 v[38:41], v[200:203], v[224:227], v[38:41]
	v_mfma_f32_16x16x32_bf16 v[34:37], v[208:211], v[224:227], v[34:37]
	v_mfma_f32_16x16x32_bf16 v[22:25], v[200:203], v[236:239], v[22:25]
	v_mfma_f32_16x16x32_bf16 v[18:21], v[208:211], v[236:239], v[18:21]
	v_mfma_f32_16x16x32_bf16 v[6:9], v[200:203], v[240:243], v[6:9]
	v_mfma_f32_16x16x32_bf16 v[2:5], v[208:211], v[240:243], v[2:5]
	s_setprio 0
	s_barrier
	s_add_i32 s64, s64, 2
	s_add_u32 s62, s62, 0x8000
	s_addc_u32 s63, s63, 0
	s_add_u32 s4, s4, 0x100
	s_addc_u32 s5, s5, 0
	s_cmp_gt_u32 s64, 13
	s_cbranch_scc0 .LBB0_192
	s_and_b64 vcc, exec, s[12:13]
	s_cbranch_vccz .LBB0_195
	s_barrier

; #define PG8_STAGE(bufoff, gbase, voff) do { _Pragma("unroll") for (int _i = 0; _i < 2; ++_i) \
;         __builtin_amdgcn_global_load_lds((const unsigned*)((const char*)(gbase) + (voff)[_i]), (LAS unsigned*)(lds + (bufoff) + ldsw + _i * 8192), 16, 0, 0); } while (0)
; #define PG8_LDA(dst, b, h) do { _Pragma("unroll") for (int m = 0; m < 4; ++m) _Pragma("unroll") for (int k = 0; k < 2; ++k) dst[m][k] = *(const LAS bf16x8*)(lds + PG8_SA(b, h) + ((aoff ^ (k * 64)) + m * 2048)); } while (0)
; #define PG8_LDB(dst, b, h) do { _Pragma("unroll") for (int n = 0; n < 2; ++n) _Pragma("unroll") for (int k = 0; k < 2; ++k) dst[n][k] = *(const LAS bf16x8*)(lds + PG8_SB(b, h) + ((boff ^ (k * 64)) + n * 2048)); } while (0)
; #define PG8_BAR __builtin_amdgcn_s_barrier()
;     ...
;             const bool last = (t == nt - 2);
;             const char* a1 = cA + (size_t)(t + 1) * kstepA;
;             const char* a2 = last ? nA : cA + (size_t)(t + 2) * kstepA; const char* b2 = last ? nB : cB + (size_t)(t + 2) * kstepB;
;             const char* a3 = a2 + kstepA; const char* b3 = b2 + kstepB;
;             unsigned vs[2][2];
;             if constexpr (GATHER) {
;                 if (last && has_next) {
; #pragma unroll
;                     for (int hh = 0; hh < 2; ++hh)
; #pragma unroll
;                         for (int i = 0; i < 2; ++i) voffN[hh][i] = (unsigned)idxl[(ui + 1) * 256 + hh * HALF + sR[i]] * (unsigned)(K * 2) + (unsigned)sC[i] * 2u;
;                 }
; #pragma unroll
;                 for (int hh = 0; hh < 2; ++hh)
; #pragma unroll
;                     for (int i = 0; i < 2; ++i) vs[hh][i] = last ? voffN[hh][i] : voffA[hh][i];
;             } else {
; #pragma unroll
;                 for (int hh = 0; hh < 2; ++hh)
; #pragma unroll
;                     for (int i = 0; i < 2; ++i) vs[hh][i] = voffA[hh][i];
;             }
;             PG8_LDB(B0, 0, 0); PG8_LDB(B1, 0, 1); PG8_SCHED; PG8_LDA(At, 0, 0); PG8_STAGE(PG8_SA(1, 1), a1, voffA[1]);
;             PG8_WAIT_V(8); PG8_WAIT_L(0); PG8_BAR; if (do0) { PG8_MMA(0, 0, At, B0); PG8_MMA(0, 1, At, B1); } PG8_BAR; PG8_SCHED;
;             PG8_LDA(At, 0, 1); PG8_STAGE(PG8_SB(0, 0), b2, voffB); PG8_STAGE(PG8_SB(0, 1), b2 + hstep, voffB); PG8_STAGE(PG8_SA(0, 0), a2, vs[0]);
;             PG8_WAIT_V(8); PG8_WAIT_L(0); PG8_BAR; if (do1) { PG8_MMA(1, 0, At, B0); PG8_MMA(1, 1, At, B1); } PG8_BAR; PG8_SCHED;
.LBB0_212:
	ds_read_b128 v[168:171], v153
	ds_read_b128 v[172:175], v154
	ds_read_b128 v[176:179], v155
	ds_read_b128 v[180:183], v156
	ds_read_b128 v[184:187], v157
	ds_read_b128 v[188:191], v158
	ds_read_b128 v[192:195], v159
	ds_read_b128 v[200:203], v160
	s_add_u32 s30, s4, 0x4000
	s_addc_u32 s31, s5, 0
	s_cmp_eq_u32 s64, 12
	s_cselect_b32 s36, s29, s30
	s_cselect_b32 s37, s17, s31
	s_cselect_b32 s34, s61, s62
	s_cselect_b32 s35, s19, s63
	s_add_u32 s30, s36, 0x4000
	s_addc_u32 s31, s37, 0
	v_lshl_add_u64 v[196:197], s[4:5], 0, v[148:149]
	s_add_i32 m0, s27, 0xc000
	ds_read_b128 v[204:207], v161
	ds_read_b128 v[208:211], v161 offset:2048
	ds_read_b128 v[212:215], v162
	ds_read_b128 v[216:219], v162 offset:2048
	ds_read_b128 v[220:223], v161 offset:4096
	ds_read_b128 v[224:227], v161 offset:6144
	ds_read_b128 v[228:231], v162 offset:4096
	ds_read_b128 v[232:235], v162 offset:6144
	global_load_lds_dwordx4 v[196:197], off
	v_lshl_add_u64 v[196:197], s[4:5], 0, v[150:151]
	s_add_i32 m0, s27, 0xe000
	s_nop 0
	global_load_lds_dwordx4 v[196:197], off
	s_waitcnt vmcnt(8)
	s_waitcnt lgkmcnt(0)
	s_barrier
	s_setprio 1
	s_waitcnt lgkmcnt(0)
	v_mfma_f32_16x16x32_bf16 v[126:129], v[168:171], v[204:207], v[126:129]
	v_mfma_f32_16x16x32_bf16 v[122:125], v[176:179], v[204:207], v[122:125]
	v_mfma_f32_16x16x32_bf16 v[110:113], v[168:171], v[208:211], v[110:113]
	v_mfma_f32_16x16x32_bf16 v[106:109], v[176:179], v[208:211], v[106:109]
	v_mfma_f32_16x16x32_bf16 v[94:97], v[168:171], v[220:223], v[94:97]
	v_mfma_f32_16x16x32_bf16 v[90:93], v[176:179], v[220:223], v[90:93]
	v_mfma_f32_16x16x32_bf16 v[78:81], v[168:171], v[224:227], v[78:81]
	v_mfma_f32_16x16x32_bf16 v[74:77], v[176:179], v[224:227], v[74:77]
	v_mfma_f32_16x16x32_bf16 v[126:129], v[172:175], v[212:215], v[126:129]
	v_mfma_f32_16x16x32_bf16 v[122:125], v[180:183], v[212:215], v[122:125]
	v_mfma_f32_16x16x32_bf16 v[110:113], v[172:175], v[216:219], v[110:113]
	v_mfma_f32_16x16x32_bf16 v[106:109], v[180:183], v[216:219], v[106:109]
	v_mfma_f32_16x16x32_bf16 v[94:97], v[172:175], v[228:231], v[94:97]
	v_mfma_f32_16x16x32_bf16 v[90:93], v[180:183], v[228:231], v[90:93]
	v_mfma_f32_16x16x32_bf16 v[78:81], v[172:175], v[232:235], v[78:81]
	v_mfma_f32_16x16x32_bf16 v[74:77], v[180:183], v[232:235], v[74:77]
	v_mfma_f32_16x16x32_bf16 v[118:121], v[184:187], v[204:207], v[118:121]
	v_mfma_f32_16x16x32_bf16 v[114:117], v[192:195], v[204:207], v[114:117]
	v_mfma_f32_16x16x32_bf16 v[102:105], v[184:187], v[208:211], v[102:105]
	v_mfma_f32_16x16x32_bf16 v[98:101], v[192:195], v[208:211], v[98:101]
	v_mfma_f32_16x16x32_bf16 v[86:89], v[184:187], v[220:223], v[86:89]
	v_mfma_f32_16x16x32_bf16 v[82:85], v[192:195], v[220:223], v[82:85]
	v_mfma_f32_16x16x32_bf16 v[70:73], v[184:187], v[224:227], v[70:73]
	v_mfma_f32_16x16x32_bf16 v[66:69], v[192:195], v[224:227], v[66:69]
	v_mfma_f32_16x16x32_bf16 v[118:121], v[188:191], v[212:215], v[118:121]
	v_mfma_f32_16x16x32_bf16 v[114:117], v[200:203], v[212:215], v[114:117]
	v_mfma_f32_16x16x32_bf16 v[102:105], v[188:191], v[216:219], v[102:105]
	v_mfma_f32_16x16x32_bf16 v[98:101], v[200:203], v[216:219], v[98:101]
	v_mfma_f32_16x16x32_bf16 v[86:89], v[188:191], v[228:231], v[86:89]
	v_mfma_f32_16x16x32_bf16 v[82:85], v[200:203], v[228:231], v[82:85]
	v_mfma_f32_16x16x32_bf16 v[70:73], v[188:191], v[232:235], v[70:73]
	v_mfma_f32_16x16x32_bf16 v[66:69], v[200:203], v[232:235], v[66:69]
	s_setprio 0
	s_barrier
	s_add_i32 s65, s58, s39
	v_lshl_add_u64 v[196:197], s[34:35], 0, v[132:133]
	s_mov_b32 m0, s65
	ds_read_b128 v[204:207], v161 offset:16384
	ds_read_b128 v[208:211], v161 offset:18432
	ds_read_b128 v[212:215], v162 offset:16384
	ds_read_b128 v[216:219], v162 offset:18432
	ds_read_b128 v[220:223], v161 offset:20480
	ds_read_b128 v[224:227], v161 offset:22528
	ds_read_b128 v[228:231], v162 offset:20480
	ds_read_b128 v[232:235], v162 offset:22528
	global_load_lds_dwordx4 v[196:197], off
	s_add_i32 m0, s65, 0x2000
	s_add_u32 s66, s34, 0x40000
	v_lshl_add_u64 v[236:237], s[34:35], 0, v[130:131]
	s_addc_u32 s67, s35, 0
	s_add_i32 s65, s59, s39
	global_load_lds_dwordx4 v[236:237], off
	v_lshl_add_u64 v[238:239], s[66:67], 0, v[132:133]
	s_mov_b32 m0, s65
	s_nop 0
	global_load_lds_dwordx4 v[238:239], off
	v_lshl_add_u64 v[238:239], s[66:67], 0, v[130:131]
	s_add_i32 m0, s65, 0x2000
	s_nop 0
	global_load_lds_dwordx4 v[238:239], off
	v_lshl_add_u64 v[238:239], s[36:37], 0, v[134:135]
	s_mov_b32 m0, s27
	s_nop 0
	global_load_lds_dwordx4 v[238:239], off
	v_lshl_add_u64 v[238:239], s[36:37], 0, v[136:137]
	s_mov_b32 m0, s48
	s_nop 0
	global_load_lds_dwordx4 v[238:239], off
	s_waitcnt vmcnt(8)
	s_waitcnt lgkmcnt(0)
	s_barrier
; #define PG8_STAGE(bufoff, gbase, voff) do { _Pragma("unroll") for (int _i = 0; _i < 2; ++_i) \
;         __builtin_amdgcn_global_load_lds((const unsigned*)((const char*)(gbase) + (voff)[_i]), (LAS unsigned*)(lds + (bufoff) + ldsw + _i * 8192), 16, 0, 0); } while (0)
; #define PG8_LDA(dst, b, h) do { _Pragma("unroll") for (int m = 0; m < 4; ++m) _Pragma("unroll") for (int k = 0; k < 2; ++k) dst[m][k] = *(const LAS bf16x8*)(lds + PG8_SA(b, h) + ((aoff ^ (k * 64)) + m * 2048)); } while (0)
; #define PG8_LDB(dst, b, h) do { _Pragma("unroll") for (int n = 0; n < 2; ++n) _Pragma("unroll") for (int k = 0; k < 2; ++k) dst[n][k] = *(const LAS bf16x8*)(lds + PG8_SB(b, h) + ((boff ^ (k * 64)) + n * 2048)); } while (0)
; #define PG8_MMA(ai, bj, At, Bt) do { __builtin_amdgcn_s_setprio(1); _Pragma("unroll") for (int m = 0; m < 4; ++m) _Pragma("unroll") for (int n = 0; n < 2; ++n) _Pragma("unroll") for (int k = 0; k < 2; ++k) \
;         acc[ai][bj][m][n] = __builtin_amdgcn_mfma_f32_16x16x32_bf16(Bt[n][k], At[m][k], acc[ai][bj][m][n], 0, 0, 0); __builtin_amdgcn_s_setprio(0); } while (0)
; #define PG8_WAIT_V(n) asm volatile("s_waitcnt vmcnt(" #n ")" ::: "memory")
; #define PG8_WAIT_L(n) asm volatile("s_waitcnt lgkmcnt(" #n ")" ::: "memory")
; #define PG8_BAR __builtin_amdgcn_s_barrier()
; #define PG8_SCHED __builtin_amdgcn_sched_barrier(0)
;     ...
;             PG8_WAIT_V(8); PG8_WAIT_L(0); PG8_BAR; if (do1) { PG8_MMA(1, 0, At, B0); PG8_MMA(1, 1, At, B1); } PG8_BAR; PG8_SCHED;
;             PG8_LDB(B0, 1, 0); PG8_LDB(B1, 1, 1); PG8_SCHED; PG8_LDA(At, 1, 0); PG8_STAGE(PG8_SA(0, 1), a2, vs[1]);
;             PG8_WAIT_V(8); PG8_WAIT_L(0); PG8_BAR; if (do0) { PG8_MMA(0, 0, At, B0); PG8_MMA(0, 1, At, B1); } PG8_BAR; PG8_SCHED;
	s_setprio 1
	s_waitcnt lgkmcnt(0)
	v_mfma_f32_16x16x32_bf16 v[62:65], v[168:171], v[204:207], v[62:65]
	v_mfma_f32_16x16x32_bf16 v[58:61], v[176:179], v[204:207], v[58:61]
	v_mfma_f32_16x16x32_bf16 v[46:49], v[168:171], v[208:211], v[46:49]
	v_mfma_f32_16x16x32_bf16 v[42:45], v[176:179], v[208:211], v[42:45]
	v_mfma_f32_16x16x32_bf16 v[30:33], v[168:171], v[220:223], v[30:33]
	v_mfma_f32_16x16x32_bf16 v[26:29], v[176:179], v[220:223], v[26:29]
	v_mfma_f32_16x16x32_bf16 v[14:17], v[168:171], v[224:227], v[14:17]
	v_mfma_f32_16x16x32_bf16 v[10:13], v[176:179], v[224:227], v[10:13]
	v_mfma_f32_16x16x32_bf16 v[62:65], v[172:175], v[212:215], v[62:65]
	v_mfma_f32_16x16x32_bf16 v[58:61], v[180:183], v[212:215], v[58:61]
	v_mfma_f32_16x16x32_bf16 v[46:49], v[172:175], v[216:219], v[46:49]
	v_mfma_f32_16x16x32_bf16 v[42:45], v[180:183], v[216:219], v[42:45]
	v_mfma_f32_16x16x32_bf16 v[30:33], v[172:175], v[228:231], v[30:33]
	v_mfma_f32_16x16x32_bf16 v[26:29], v[180:183], v[228:231], v[26:29]
	v_mfma_f32_16x16x32_bf16 v[14:17], v[172:175], v[232:235], v[14:17]
	v_mfma_f32_16x16x32_bf16 v[10:13], v[180:183], v[232:235], v[10:13]
	v_mfma_f32_16x16x32_bf16 v[54:57], v[184:187], v[204:207], v[54:57]
	v_mfma_f32_16x16x32_bf16 v[50:53], v[192:195], v[204:207], v[50:53]
	v_mfma_f32_16x16x32_bf16 v[38:41], v[184:187], v[208:211], v[38:41]
	v_mfma_f32_16x16x32_bf16 v[34:37], v[192:195], v[208:211], v[34:37]
	v_mfma_f32_16x16x32_bf16 v[22:25], v[184:187], v[220:223], v[22:25]
	v_mfma_f32_16x16x32_bf16 v[18:21], v[192:195], v[220:223], v[18:21]
	v_mfma_f32_16x16x32_bf16 v[6:9], v[184:187], v[224:227], v[6:9]
	v_mfma_f32_16x16x32_bf16 v[2:5], v[192:195], v[224:227], v[2:5]
	v_mfma_f32_16x16x32_bf16 v[54:57], v[188:191], v[212:215], v[54:57]
	v_mfma_f32_16x16x32_bf16 v[50:53], v[200:203], v[212:215], v[50:53]
	v_mfma_f32_16x16x32_bf16 v[38:41], v[188:191], v[216:219], v[38:41]
	v_mfma_f32_16x16x32_bf16 v[34:37], v[200:203], v[216:219], v[34:37]
	v_mfma_f32_16x16x32_bf16 v[22:25], v[188:191], v[228:231], v[22:25]
	v_mfma_f32_16x16x32_bf16 v[18:21], v[200:203], v[228:231], v[18:21]
	v_mfma_f32_16x16x32_bf16 v[6:9], v[188:191], v[232:235], v[6:9]
	v_mfma_f32_16x16x32_bf16 v[2:5], v[200:203], v[232:235], v[2:5]
	s_setprio 0
	s_barrier
	s_add_i32 s65, 0, 0x18000
	v_add_u32_e32 v167, s65, v143
	v_add_u32_e32 v172, s65, v152
	s_add_i32 s66, 0, 0x1c000
	ds_read_b128 v[168:171], v167
	ds_read_b128 v[172:175], v172
	ds_read_b128 v[176:179], v163
	ds_read_b128 v[180:183], v164
	v_add_u32_e32 v167, s66, v143
	v_add_u32_e32 v188, s66, v152
	ds_read_b128 v[184:187], v167
	ds_read_b128 v[188:191], v188
	ds_read_b128 v[192:195], v165
	ds_read_b128 v[200:203], v166
	s_mov_b32 m0, s49
	v_lshl_add_u64 v[238:239], s[36:37], 0, v[138:139]
	ds_read_b128 v[204:207], v161 offset:32768
	ds_read_b128 v[208:211], v161 offset:34816
	ds_read_b128 v[212:215], v162 offset:32768
	ds_read_b128 v[216:219], v162 offset:34816
	ds_read_b128 v[220:223], v161 offset:36864
	ds_read_b128 v[224:227], v161 offset:38912
	ds_read_b128 v[228:231], v162 offset:36864
	ds_read_b128 v[232:235], v162 offset:38912
	global_load_lds_dwordx4 v[238:239], off
	v_lshl_add_u64 v[238:239], s[36:37], 0, v[140:141]
	s_mov_b32 m0, s50
	s_nop 0
	global_load_lds_dwordx4 v[238:239], off
	s_waitcnt vmcnt(8)
	s_waitcnt lgkmcnt(0)
	s_barrier
	s_setprio 1
	s_waitcnt lgkmcnt(0)
	v_mfma_f32_16x16x32_bf16 v[126:129], v[168:171], v[204:207], v[126:129]
	v_mfma_f32_16x16x32_bf16 v[122:125], v[176:179], v[204:207], v[122:125]
	v_mfma_f32_16x16x32_bf16 v[110:113], v[168:171], v[208:211], v[110:113]
	v_mfma_f32_16x16x32_bf16 v[106:109], v[176:179], v[208:211], v[106:109]
	v_mfma_f32_16x16x32_bf16 v[94:97], v[168:171], v[220:223], v[94:97]
	v_mfma_f32_16x16x32_bf16 v[90:93], v[176:179], v[220:223], v[90:93]
	v_mfma_f32_16x16x32_bf16 v[78:81], v[168:171], v[224:227], v[78:81]
	v_mfma_f32_16x16x32_bf16 v[74:77], v[176:179], v[224:227], v[74:77]
	v_mfma_f32_16x16x32_bf16 v[126:129], v[172:175], v[212:215], v[126:129]
	v_mfma_f32_16x16x32_bf16 v[122:125], v[180:183], v[212:215], v[122:125]
	v_mfma_f32_16x16x32_bf16 v[110:113], v[172:175], v[216:219], v[110:113]
	v_mfma_f32_16x16x32_bf16 v[106:109], v[180:183], v[216:219], v[106:109]
	v_mfma_f32_16x16x32_bf16 v[94:97], v[172:175], v[228:231], v[94:97]
	v_mfma_f32_16x16x32_bf16 v[90:93], v[180:183], v[228:231], v[90:93]
	v_mfma_f32_16x16x32_bf16 v[78:81], v[172:175], v[232:235], v[78:81]
	v_mfma_f32_16x16x32_bf16 v[74:77], v[180:183], v[232:235], v[74:77]
	v_mfma_f32_16x16x32_bf16 v[118:121], v[184:187], v[204:207], v[118:121]
	v_mfma_f32_16x16x32_bf16 v[114:117], v[192:195], v[204:207], v[114:117]
	v_mfma_f32_16x16x32_bf16 v[102:105], v[184:187], v[208:211], v[102:105]
	v_mfma_f32_16x16x32_bf16 v[98:101], v[192:195], v[208:211], v[98:101]
	v_mfma_f32_16x16x32_bf16 v[86:89], v[184:187], v[220:223], v[86:89]
	v_mfma_f32_16x16x32_bf16 v[82:85], v[192:195], v[220:223], v[82:85]
	v_mfma_f32_16x16x32_bf16 v[70:73], v[184:187], v[224:227], v[70:73]
	v_mfma_f32_16x16x32_bf16 v[66:69], v[192:195], v[224:227], v[66:69]
	v_mfma_f32_16x16x32_bf16 v[118:121], v[188:191], v[212:215], v[118:121]
	v_mfma_f32_16x16x32_bf16 v[114:117], v[200:203], v[212:215], v[114:117]
	v_mfma_f32_16x16x32_bf16 v[102:105], v[188:191], v[216:219], v[102:105]
	v_mfma_f32_16x16x32_bf16 v[98:101], v[200:203], v[216:219], v[98:101]
	v_mfma_f32_16x16x32_bf16 v[86:89], v[188:191], v[228:231], v[86:89]
	v_mfma_f32_16x16x32_bf16 v[82:85], v[200:203], v[228:231], v[82:85]
	v_mfma_f32_16x16x32_bf16 v[70:73], v[188:191], v[232:235], v[70:73]
	v_mfma_f32_16x16x32_bf16 v[66:69], v[200:203], v[232:235], v[66:69]
	s_setprio 0
	s_barrier
; #define PG8_STAGE(bufoff, gbase, voff) do { _Pragma("unroll") for (int _i = 0; _i < 2; ++_i) \
;         __builtin_amdgcn_global_load_lds((const unsigned*)((const char*)(gbase) + (voff)[_i]), (LAS unsigned*)(lds + (bufoff) + ldsw + _i * 8192), 16, 0, 0); } while (0)
; #define PG8_LDA(dst, b, h) do { _Pragma("unroll") for (int m = 0; m < 4; ++m) _Pragma("unroll") for (int k = 0; k < 2; ++k) dst[m][k] = *(const LAS bf16x8*)(lds + PG8_SA(b, h) + ((aoff ^ (k * 64)) + m * 2048)); } while (0)
; #define PG8_MMA(ai, bj, At, Bt) do { __builtin_amdgcn_s_setprio(1); _Pragma("unroll") for (int m = 0; m < 4; ++m) _Pragma("unroll") for (int n = 0; n < 2; ++n) _Pragma("unroll") for (int k = 0; k < 2; ++k) \
;         acc[ai][bj][m][n] = __builtin_amdgcn_mfma_f32_16x16x32_bf16(Bt[n][k], At[m][k], acc[ai][bj][m][n], 0, 0, 0); __builtin_amdgcn_s_setprio(0); } while (0)
; #define PG8_WAIT_V(n) asm volatile("s_waitcnt vmcnt(" #n ")" ::: "memory")
; #define PG8_WAIT_L(n) asm volatile("s_waitcnt lgkmcnt(" #n ")" ::: "memory")
; #define PG8_BAR __builtin_amdgcn_s_barrier()
; #define PG8_SCHED __builtin_amdgcn_sched_barrier(0)
;     ...
;             PG8_LDA(At, 1, 1); PG8_STAGE(PG8_SB(1, 0), b3, voffB); PG8_STAGE(PG8_SB(1, 1), b3 + hstep, voffB); PG8_STAGE(PG8_SA(1, 0), a3, vs[0]);
;             PG8_WAIT_V(8); PG8_WAIT_L(0); PG8_BAR; if (do1) { PG8_MMA(1, 0, At, B0); PG8_MMA(1, 1, At, B1); } PG8_BAR; PG8_SCHED;
;         }
;         if (wr == 0) PG8_BAR;
	s_add_i32 s36, s65, s39
	v_lshl_add_u64 v[196:197], v[196:197], 0, s[12:13]
	s_mov_b32 m0, s36
	ds_read_b128 v[204:207], v161 offset:49152
	ds_read_b128 v[208:211], v161 offset:51200
	ds_read_b128 v[212:215], v162 offset:49152
	ds_read_b128 v[216:219], v162 offset:51200
	ds_read_b128 v[220:223], v161 offset:53248
	ds_read_b128 v[224:227], v161 offset:55296
	ds_read_b128 v[228:231], v162 offset:53248
	ds_read_b128 v[232:235], v162 offset:55296
	global_load_lds_dwordx4 v[196:197], off
	s_add_i32 m0, s36, 0x2000
	s_add_u32 s34, s34, 0x40080
	v_lshl_add_u64 v[196:197], v[236:237], 0, s[12:13]
	s_addc_u32 s35, s35, 0
	s_add_i32 s36, s66, s39
	global_load_lds_dwordx4 v[196:197], off
	v_lshl_add_u64 v[196:197], s[34:35], 0, v[132:133]
	s_mov_b32 m0, s36
	s_nop 0
	global_load_lds_dwordx4 v[196:197], off
	v_lshl_add_u64 v[196:197], s[34:35], 0, v[130:131]
	s_add_i32 m0, s36, 0x2000
	s_nop 0
	global_load_lds_dwordx4 v[196:197], off
	v_lshl_add_u64 v[196:197], s[30:31], 0, v[134:135]
	s_mov_b32 m0, s55
	s_nop 0
	global_load_lds_dwordx4 v[196:197], off
	v_lshl_add_u64 v[196:197], s[30:31], 0, v[136:137]
	s_mov_b32 m0, s56
	s_nop 0
	global_load_lds_dwordx4 v[196:197], off
	s_waitcnt vmcnt(8)
	s_waitcnt lgkmcnt(0)
	s_barrier
	s_setprio 1
	s_waitcnt lgkmcnt(0)
	v_mfma_f32_16x16x32_bf16 v[62:65], v[168:171], v[204:207], v[62:65]
	v_mfma_f32_16x16x32_bf16 v[58:61], v[176:179], v[204:207], v[58:61]
	v_mfma_f32_16x16x32_bf16 v[46:49], v[168:171], v[208:211], v[46:49]
	v_mfma_f32_16x16x32_bf16 v[42:45], v[176:179], v[208:211], v[42:45]
	v_mfma_f32_16x16x32_bf16 v[30:33], v[168:171], v[220:223], v[30:33]
	v_mfma_f32_16x16x32_bf16 v[26:29], v[176:179], v[220:223], v[26:29]
	v_mfma_f32_16x16x32_bf16 v[14:17], v[168:171], v[224:227], v[14:17]
	v_mfma_f32_16x16x32_bf16 v[10:13], v[176:179], v[224:227], v[10:13]
	v_mfma_f32_16x16x32_bf16 v[62:65], v[172:175], v[212:215], v[62:65]
	v_mfma_f32_16x16x32_bf16 v[58:61], v[180:183], v[212:215], v[58:61]
	v_mfma_f32_16x16x32_bf16 v[46:49], v[172:175], v[216:219], v[46:49]
	v_mfma_f32_16x16x32_bf16 v[42:45], v[180:183], v[216:219], v[42:45]
	v_mfma_f32_16x16x32_bf16 v[30:33], v[172:175], v[228:231], v[30:33]
	v_mfma_f32_16x16x32_bf16 v[26:29], v[180:183], v[228:231], v[26:29]
	v_mfma_f32_16x16x32_bf16 v[14:17], v[172:175], v[232:235], v[14:17]
	v_mfma_f32_16x16x32_bf16 v[10:13], v[180:183], v[232:235], v[10:13]
	v_mfma_f32_16x16x32_bf16 v[54:57], v[184:187], v[204:207], v[54:57]
	v_mfma_f32_16x16x32_bf16 v[50:53], v[192:195], v[204:207], v[50:53]
	v_mfma_f32_16x16x32_bf16 v[38:41], v[184:187], v[208:211], v[38:41]
	v_mfma_f32_16x16x32_bf16 v[34:37], v[192:195], v[208:211], v[34:37]
	v_mfma_f32_16x16x32_bf16 v[22:25], v[184:187], v[220:223], v[22:25]
	v_mfma_f32_16x16x32_bf16 v[18:21], v[192:195], v[220:223], v[18:21]
	v_mfma_f32_16x16x32_bf16 v[6:9], v[184:187], v[224:227], v[6:9]
	v_mfma_f32_16x16x32_bf16 v[2:5], v[192:195], v[224:227], v[2:5]
	v_mfma_f32_16x16x32_bf16 v[54:57], v[188:191], v[212:215], v[54:57]
	v_mfma_f32_16x16x32_bf16 v[50:53], v[200:203], v[212:215], v[50:53]
	v_mfma_f32_16x16x32_bf16 v[38:41], v[188:191], v[216:219], v[38:41]
	v_mfma_f32_16x16x32_bf16 v[34:37], v[200:203], v[216:219], v[34:37]
	v_mfma_f32_16x16x32_bf16 v[22:25], v[188:191], v[228:231], v[22:25]
	v_mfma_f32_16x16x32_bf16 v[18:21], v[200:203], v[228:231], v[18:21]
	v_mfma_f32_16x16x32_bf16 v[6:9], v[188:191], v[232:235], v[6:9]
	v_mfma_f32_16x16x32_bf16 v[2:5], v[200:203], v[232:235], v[2:5]
	s_setprio 0
	s_barrier
	s_add_i32 s64, s64, 2
	s_add_u32 s62, s62, 0x100
	s_addc_u32 s63, s63, 0
	s_add_u32 s4, s4, 0x8000
	s_addc_u32 s5, s5, 0
	s_cmp_gt_u32 s64, 13
	s_cbranch_scc0 .LBB0_212
	s_and_b64 vcc, exec, s[14:15]
	s_cbranch_vccz .LBB0_215
	s_barrier

; #define PG8_STAGE(bufoff, gbase, voff) do { _Pragma("unroll") for (int _i = 0; _i < 2; ++_i) \
;         __builtin_amdgcn_global_load_lds((const unsigned*)((const char*)(gbase) + (voff)[_i]), (LAS unsigned*)(lds + (bufoff) + ldsw + _i * 8192), 16, 0, 0); } while (0)
; #define PG8_LDA(dst, b, h) do { _Pragma("unroll") for (int m = 0; m < 4; ++m) _Pragma("unroll") for (int k = 0; k < 2; ++k) dst[m][k] = *(const LAS bf16x8*)(lds + PG8_SA(b, h) + ((aoff ^ (k * 64)) + m * 2048)); } while (0)
; #define PG8_LDB(dst, b, h) do { _Pragma("unroll") for (int n = 0; n < 2; ++n) _Pragma("unroll") for (int k = 0; k < 2; ++k) dst[n][k] = *(const LAS bf16x8*)(lds + PG8_SB(b, h) + ((boff ^ (k * 64)) + n * 2048)); } while (0)
; #define PG8_BAR __builtin_amdgcn_s_barrier()
;     ...
;             const bool last = (t == nt - 2);
;             const char* a1 = cA + (size_t)(t + 1) * kstepA;
;             const char* a2 = last ? nA : cA + (size_t)(t + 2) * kstepA; const char* b2 = last ? nB : cB + (size_t)(t + 2) * kstepB;
;             const char* a3 = a2 + kstepA; const char* b3 = b2 + kstepB;
;             unsigned vs[2][2];
;             if constexpr (GATHER) {
;                 if (last && has_next) {
; #pragma unroll
;                     for (int hh = 0; hh < 2; ++hh)
; #pragma unroll
;                         for (int i = 0; i < 2; ++i) voffN[hh][i] = (unsigned)idxl[(ui + 1) * 256 + hh * HALF + sR[i]] * (unsigned)(K * 2) + (unsigned)sC[i] * 2u;
;                 }
; #pragma unroll
;                 for (int hh = 0; hh < 2; ++hh)
; #pragma unroll
;                     for (int i = 0; i < 2; ++i) vs[hh][i] = last ? voffN[hh][i] : voffA[hh][i];
;             } else {
; #pragma unroll
;                 for (int hh = 0; hh < 2; ++hh)
; #pragma unroll
;                     for (int i = 0; i < 2; ++i) vs[hh][i] = voffA[hh][i];
;             }
;             PG8_LDB(B0, 0, 0); PG8_LDB(B1, 0, 1); PG8_SCHED; PG8_LDA(At, 0, 0); PG8_STAGE(PG8_SA(1, 1), a1, voffA[1]);
;             PG8_WAIT_V(8); PG8_WAIT_L(0); PG8_BAR; if (do0) { PG8_MMA(0, 0, At, B0); PG8_MMA(0, 1, At, B1); } PG8_BAR; PG8_SCHED;
;             PG8_LDA(At, 0, 1); PG8_STAGE(PG8_SB(0, 0), b2, voffB); PG8_STAGE(PG8_SB(0, 1), b2 + hstep, voffB); PG8_STAGE(PG8_SA(0, 0), a2, vs[0]);
;             PG8_WAIT_V(8); PG8_WAIT_L(0); PG8_BAR; if (do1) { PG8_MMA(1, 0, At, B0); PG8_MMA(1, 1, At, B1); } PG8_BAR; PG8_SCHED;
.LBB0_460:
	ds_read_b128 v[130:133], v203
	ds_read_b128 v[134:137], v204
	ds_read_b128 v[138:141], v205
	ds_read_b128 v[142:145], v206
	ds_read_b128 v[168:171], v207
	ds_read_b128 v[172:175], v208
	ds_read_b128 v[176:179], v209
	ds_read_b128 v[180:183], v210
	s_add_u32 s4, s2, 0x80
	s_addc_u32 s5, s3, 0
	s_cmp_eq_u32 s41, 12
	s_cselect_b32 s39, s9, s5
	s_cselect_b32 s38, s12, s4
	s_cselect_b32 s5, s27, s40
	s_cselect_b32 s4, s29, s37
	v_lshl_add_u64 v[196:197], s[2:3], 0, v[162:163]
	s_add_i32 m0, s50, 0xc000
	ds_read_b128 v[184:187], v211
	ds_read_b128 v[188:191], v211 offset:2048
	ds_read_b128 v[192:195], v212
	ds_read_b128 v[220:223], v212 offset:2048
	ds_read_b128 v[224:227], v211 offset:4096
	ds_read_b128 v[228:231], v211 offset:6144
	ds_read_b128 v[232:235], v212 offset:4096
	ds_read_b128 v[236:239], v212 offset:6144
	global_load_lds_dwordx4 v[196:197], off
	v_lshl_add_u64 v[196:197], s[2:3], 0, v[160:161]
	s_add_i32 m0, s50, 0xe000
	s_add_u32 s6, s4, 0x4000
	global_load_lds_dwordx4 v[196:197], off
	s_waitcnt vmcnt(8)
	s_waitcnt lgkmcnt(0)
	s_addc_u32 s7, s5, 0
	s_barrier
	s_setprio 1
	s_waitcnt lgkmcnt(0)
	v_mfma_f32_16x16x32_bf16 v[126:129], v[130:133], v[184:187], v[126:129]
	v_mfma_f32_16x16x32_bf16 v[58:61], v[138:141], v[184:187], v[58:61]
	v_mfma_f32_16x16x32_bf16 v[122:125], v[130:133], v[188:191], v[122:125]
	v_mfma_f32_16x16x32_bf16 v[118:121], v[138:141], v[188:191], v[118:121]
	v_mfma_f32_16x16x32_bf16 v[114:117], v[130:133], v[224:227], v[114:117]
	v_mfma_f32_16x16x32_bf16 v[110:113], v[138:141], v[224:227], v[110:113]
	v_mfma_f32_16x16x32_bf16 v[106:109], v[130:133], v[228:231], v[106:109]
	v_mfma_f32_16x16x32_bf16 v[102:105], v[138:141], v[228:231], v[102:105]
	v_mfma_f32_16x16x32_bf16 v[126:129], v[134:137], v[192:195], v[126:129]
	v_mfma_f32_16x16x32_bf16 v[58:61], v[142:145], v[192:195], v[58:61]
	v_mfma_f32_16x16x32_bf16 v[122:125], v[134:137], v[220:223], v[122:125]
	v_mfma_f32_16x16x32_bf16 v[118:121], v[142:145], v[220:223], v[118:121]
	v_mfma_f32_16x16x32_bf16 v[114:117], v[134:137], v[232:235], v[114:117]
	v_mfma_f32_16x16x32_bf16 v[110:113], v[142:145], v[232:235], v[110:113]
	v_mfma_f32_16x16x32_bf16 v[106:109], v[134:137], v[236:239], v[106:109]
	v_mfma_f32_16x16x32_bf16 v[102:105], v[142:145], v[236:239], v[102:105]
	v_mfma_f32_16x16x32_bf16 v[66:69], v[168:171], v[184:187], v[66:69]
	v_mfma_f32_16x16x32_bf16 v[50:53], v[176:179], v[184:187], v[50:53]
	v_mfma_f32_16x16x32_bf16 v[54:57], v[168:171], v[188:191], v[54:57]
	v_mfma_f32_16x16x32_bf16 v[42:45], v[176:179], v[188:191], v[42:45]
	v_mfma_f32_16x16x32_bf16 v[46:49], v[168:171], v[224:227], v[46:49]
	v_mfma_f32_16x16x32_bf16 v[34:37], v[176:179], v[224:227], v[34:37]
	v_mfma_f32_16x16x32_bf16 v[98:101], v[168:171], v[228:231], v[98:101]
	v_mfma_f32_16x16x32_bf16 v[38:41], v[176:179], v[228:231], v[38:41]
	v_mfma_f32_16x16x32_bf16 v[66:69], v[172:175], v[192:195], v[66:69]
	v_mfma_f32_16x16x32_bf16 v[50:53], v[180:183], v[192:195], v[50:53]
	v_mfma_f32_16x16x32_bf16 v[54:57], v[172:175], v[220:223], v[54:57]
	v_mfma_f32_16x16x32_bf16 v[42:45], v[180:183], v[220:223], v[42:45]
	v_mfma_f32_16x16x32_bf16 v[46:49], v[172:175], v[232:235], v[46:49]
	v_mfma_f32_16x16x32_bf16 v[34:37], v[180:183], v[232:235], v[34:37]
	v_mfma_f32_16x16x32_bf16 v[98:101], v[172:175], v[236:239], v[98:101]
	v_mfma_f32_16x16x32_bf16 v[38:41], v[180:183], v[236:239], v[38:41]
	s_setprio 0
	s_barrier
	s_add_i32 s42, s65, s49
	v_lshl_add_u64 v[196:197], s[4:5], 0, v[146:147]
	s_mov_b32 m0, s42
	ds_read_b128 v[184:187], v211 offset:16384
	ds_read_b128 v[188:191], v211 offset:18432
	ds_read_b128 v[192:195], v212 offset:16384
	ds_read_b128 v[220:223], v212 offset:18432
	ds_read_b128 v[224:227], v211 offset:20480
	ds_read_b128 v[228:231], v211 offset:22528
	ds_read_b128 v[232:235], v212 offset:20480
	ds_read_b128 v[236:239], v212 offset:22528
	global_load_lds_dwordx4 v[196:197], off
	s_add_i32 m0, s42, 0x2000
	s_add_u32 s42, s4, 0x40000
	v_lshl_add_u64 v[196:197], s[4:5], 0, v[148:149]
	s_addc_u32 s43, s5, 0
	s_add_i32 s74, s66, s49
	global_load_lds_dwordx4 v[196:197], off
	v_lshl_add_u64 v[196:197], s[42:43], 0, v[146:147]
	s_mov_b32 m0, s74
	v_lshl_add_u64 v[240:241], s[38:39], 0, v[152:153]
	global_load_lds_dwordx4 v[196:197], off
	v_lshl_add_u64 v[196:197], s[42:43], 0, v[148:149]
	s_add_i32 m0, s74, 0x2000
	s_nop 0
	global_load_lds_dwordx4 v[196:197], off
	v_lshl_add_u64 v[196:197], s[38:39], 0, v[150:151]
	s_mov_b32 m0, s50
	s_nop 0
	global_load_lds_dwordx4 v[196:197], off
	s_mov_b32 m0, s51
	s_nop 0
	global_load_lds_dwordx4 v[240:241], off
	s_waitcnt vmcnt(8)
	s_waitcnt lgkmcnt(0)
	s_barrier
; #define PG8_STAGE(bufoff, gbase, voff) do { _Pragma("unroll") for (int _i = 0; _i < 2; ++_i) \
;         __builtin_amdgcn_global_load_lds((const unsigned*)((const char*)(gbase) + (voff)[_i]), (LAS unsigned*)(lds + (bufoff) + ldsw + _i * 8192), 16, 0, 0); } while (0)
; #define PG8_LDA(dst, b, h) do { _Pragma("unroll") for (int m = 0; m < 4; ++m) _Pragma("unroll") for (int k = 0; k < 2; ++k) dst[m][k] = *(const LAS bf16x8*)(lds + PG8_SA(b, h) + ((aoff ^ (k * 64)) + m * 2048)); } while (0)
; #define PG8_LDB(dst, b, h) do { _Pragma("unroll") for (int n = 0; n < 2; ++n) _Pragma("unroll") for (int k = 0; k < 2; ++k) dst[n][k] = *(const LAS bf16x8*)(lds + PG8_SB(b, h) + ((boff ^ (k * 64)) + n * 2048)); } while (0)
; #define PG8_MMA(ai, bj, At, Bt) do { __builtin_amdgcn_s_setprio(1); _Pragma("unroll") for (int m = 0; m < 4; ++m) _Pragma("unroll") for (int n = 0; n < 2; ++n) _Pragma("unroll") for (int k = 0; k < 2; ++k) \
;         acc[ai][bj][m][n] = __builtin_amdgcn_mfma_f32_16x16x32_bf16(Bt[n][k], At[m][k], acc[ai][bj][m][n], 0, 0, 0); __builtin_amdgcn_s_setprio(0); } while (0)
; #define PG8_WAIT_V(n) asm volatile("s_waitcnt vmcnt(" #n ")" ::: "memory")
; #define PG8_WAIT_L(n) asm volatile("s_waitcnt lgkmcnt(" #n ")" ::: "memory")
; #define PG8_BAR __builtin_amdgcn_s_barrier()
; #define PG8_SCHED __builtin_amdgcn_sched_barrier(0)
;     ...
;             PG8_WAIT_V(8); PG8_WAIT_L(0); PG8_BAR; if (do1) { PG8_MMA(1, 0, At, B0); PG8_MMA(1, 1, At, B1); } PG8_BAR; PG8_SCHED;
;             PG8_LDB(B0, 1, 0); PG8_LDB(B1, 1, 1); PG8_SCHED; PG8_LDA(At, 1, 0); PG8_STAGE(PG8_SA(0, 1), a2, vs[1]);
;             PG8_WAIT_V(8); PG8_WAIT_L(0); PG8_BAR; if (do0) { PG8_MMA(0, 0, At, B0); PG8_MMA(0, 1, At, B1); } PG8_BAR; PG8_SCHED;
	s_setprio 1
	s_waitcnt lgkmcnt(0)
	v_mfma_f32_16x16x32_bf16 v[94:97], v[130:133], v[184:187], v[94:97]
	v_mfma_f32_16x16x32_bf16 v[26:29], v[138:141], v[184:187], v[26:29]
	v_mfma_f32_16x16x32_bf16 v[90:93], v[130:133], v[188:191], v[90:93]
	v_mfma_f32_16x16x32_bf16 v[86:89], v[138:141], v[188:191], v[86:89]
	v_mfma_f32_16x16x32_bf16 v[82:85], v[130:133], v[224:227], v[82:85]
	v_mfma_f32_16x16x32_bf16 v[78:81], v[138:141], v[224:227], v[78:81]
	v_mfma_f32_16x16x32_bf16 v[74:77], v[130:133], v[228:231], v[74:77]
	v_mfma_f32_16x16x32_bf16 v[70:73], v[138:141], v[228:231], v[70:73]
	v_mfma_f32_16x16x32_bf16 v[94:97], v[134:137], v[192:195], v[94:97]
	v_mfma_f32_16x16x32_bf16 v[26:29], v[142:145], v[192:195], v[26:29]
	v_mfma_f32_16x16x32_bf16 v[90:93], v[134:137], v[220:223], v[90:93]
	v_mfma_f32_16x16x32_bf16 v[86:89], v[142:145], v[220:223], v[86:89]
	v_mfma_f32_16x16x32_bf16 v[82:85], v[134:137], v[232:235], v[82:85]
	v_mfma_f32_16x16x32_bf16 v[78:81], v[142:145], v[232:235], v[78:81]
	v_mfma_f32_16x16x32_bf16 v[74:77], v[134:137], v[236:239], v[74:77]
	v_mfma_f32_16x16x32_bf16 v[70:73], v[142:145], v[236:239], v[70:73]
	v_mfma_f32_16x16x32_bf16 v[30:33], v[168:171], v[184:187], v[30:33]
	v_mfma_f32_16x16x32_bf16 v[18:21], v[176:179], v[184:187], v[18:21]
	v_mfma_f32_16x16x32_bf16 v[22:25], v[168:171], v[188:191], v[22:25]
	v_mfma_f32_16x16x32_bf16 v[10:13], v[176:179], v[188:191], v[10:13]
	v_mfma_f32_16x16x32_bf16 v[14:17], v[168:171], v[224:227], v[14:17]
	v_mfma_f32_16x16x32_bf16 v[2:5], v[176:179], v[224:227], v[2:5]
	v_mfma_f32_16x16x32_bf16 v[62:65], v[168:171], v[228:231], v[62:65]
	v_mfma_f32_16x16x32_bf16 v[6:9], v[176:179], v[228:231], v[6:9]
	v_mfma_f32_16x16x32_bf16 v[30:33], v[172:175], v[192:195], v[30:33]
	v_mfma_f32_16x16x32_bf16 v[18:21], v[180:183], v[192:195], v[18:21]
	v_mfma_f32_16x16x32_bf16 v[22:25], v[172:175], v[220:223], v[22:25]
	v_mfma_f32_16x16x32_bf16 v[10:13], v[180:183], v[220:223], v[10:13]
	v_mfma_f32_16x16x32_bf16 v[14:17], v[172:175], v[232:235], v[14:17]
	v_mfma_f32_16x16x32_bf16 v[2:5], v[180:183], v[232:235], v[2:5]
	v_mfma_f32_16x16x32_bf16 v[62:65], v[172:175], v[236:239], v[62:65]
	v_mfma_f32_16x16x32_bf16 v[6:9], v[180:183], v[236:239], v[6:9]
	s_setprio 0
	s_barrier
	s_add_i32 s42, 0, 0x18000
	s_add_i32 s43, 0, 0x1c000
	v_add_u32_e32 v130, s42, v201
	v_add_u32_e32 v134, s42, v202
	v_add_u32_e32 v158, s43, v201
	v_add_u32_e32 v172, s43, v202
	ds_read_b128 v[130:133], v130
	ds_read_b128 v[134:137], v134
	ds_read_b128 v[138:141], v213
	ds_read_b128 v[142:145], v214
	ds_read_b128 v[168:171], v158
	ds_read_b128 v[172:175], v172
	ds_read_b128 v[176:179], v215
	ds_read_b128 v[180:183], v216
	s_mov_b32 m0, s52
	v_lshl_add_u64 v[242:243], s[38:39], 0, v[154:155]
	ds_read_b128 v[184:187], v211 offset:32768
	ds_read_b128 v[188:191], v211 offset:34816
	ds_read_b128 v[192:195], v212 offset:32768
	ds_read_b128 v[220:223], v212 offset:34816
	ds_read_b128 v[224:227], v211 offset:36864
	ds_read_b128 v[228:231], v211 offset:38912
	ds_read_b128 v[232:235], v212 offset:36864
	ds_read_b128 v[236:239], v212 offset:38912
	global_load_lds_dwordx4 v[242:243], off
	v_lshl_add_u64 v[242:243], s[38:39], 0, v[156:157]
	s_mov_b32 m0, s53
	s_nop 0
	global_load_lds_dwordx4 v[242:243], off
	s_waitcnt vmcnt(8)
	s_waitcnt lgkmcnt(0)
	s_barrier
	s_setprio 1
	s_waitcnt lgkmcnt(0)
	v_mfma_f32_16x16x32_bf16 v[126:129], v[130:133], v[184:187], v[126:129]
	v_mfma_f32_16x16x32_bf16 v[58:61], v[138:141], v[184:187], v[58:61]
	v_mfma_f32_16x16x32_bf16 v[122:125], v[130:133], v[188:191], v[122:125]
	v_mfma_f32_16x16x32_bf16 v[118:121], v[138:141], v[188:191], v[118:121]
	v_mfma_f32_16x16x32_bf16 v[114:117], v[130:133], v[224:227], v[114:117]
	v_mfma_f32_16x16x32_bf16 v[110:113], v[138:141], v[224:227], v[110:113]
	v_mfma_f32_16x16x32_bf16 v[106:109], v[130:133], v[228:231], v[106:109]
	v_mfma_f32_16x16x32_bf16 v[102:105], v[138:141], v[228:231], v[102:105]
	v_mfma_f32_16x16x32_bf16 v[126:129], v[134:137], v[192:195], v[126:129]
	v_mfma_f32_16x16x32_bf16 v[58:61], v[142:145], v[192:195], v[58:61]
	v_mfma_f32_16x16x32_bf16 v[122:125], v[134:137], v[220:223], v[122:125]
	v_mfma_f32_16x16x32_bf16 v[118:121], v[142:145], v[220:223], v[118:121]
	v_mfma_f32_16x16x32_bf16 v[114:117], v[134:137], v[232:235], v[114:117]
	v_mfma_f32_16x16x32_bf16 v[110:113], v[142:145], v[232:235], v[110:113]
	v_mfma_f32_16x16x32_bf16 v[106:109], v[134:137], v[236:239], v[106:109]
	v_mfma_f32_16x16x32_bf16 v[102:105], v[142:145], v[236:239], v[102:105]
	v_mfma_f32_16x16x32_bf16 v[66:69], v[168:171], v[184:187], v[66:69]
	v_mfma_f32_16x16x32_bf16 v[50:53], v[176:179], v[184:187], v[50:53]
	v_mfma_f32_16x16x32_bf16 v[54:57], v[168:171], v[188:191], v[54:57]
	v_mfma_f32_16x16x32_bf16 v[42:45], v[176:179], v[188:191], v[42:45]
	v_mfma_f32_16x16x32_bf16 v[46:49], v[168:171], v[224:227], v[46:49]
	v_mfma_f32_16x16x32_bf16 v[34:37], v[176:179], v[224:227], v[34:37]
	v_mfma_f32_16x16x32_bf16 v[98:101], v[168:171], v[228:231], v[98:101]
	v_mfma_f32_16x16x32_bf16 v[38:41], v[176:179], v[228:231], v[38:41]
	v_mfma_f32_16x16x32_bf16 v[66:69], v[172:175], v[192:195], v[66:69]
	v_mfma_f32_16x16x32_bf16 v[50:53], v[180:183], v[192:195], v[50:53]
	v_mfma_f32_16x16x32_bf16 v[54:57], v[172:175], v[220:223], v[54:57]
	v_mfma_f32_16x16x32_bf16 v[42:45], v[180:183], v[220:223], v[42:45]
	v_mfma_f32_16x16x32_bf16 v[46:49], v[172:175], v[232:235], v[46:49]
	v_mfma_f32_16x16x32_bf16 v[34:37], v[180:183], v[232:235], v[34:37]
	v_mfma_f32_16x16x32_bf16 v[98:101], v[172:175], v[236:239], v[98:101]
	v_mfma_f32_16x16x32_bf16 v[38:41], v[180:183], v[236:239], v[38:41]
	s_setprio 0
	s_barrier
; #define PG8_STAGE(bufoff, gbase, voff) do { _Pragma("unroll") for (int _i = 0; _i < 2; ++_i) \
;         __builtin_amdgcn_global_load_lds((const unsigned*)((const char*)(gbase) + (voff)[_i]), (LAS unsigned*)(lds + (bufoff) + ldsw + _i * 8192), 16, 0, 0); } while (0)
; #define PG8_LDA(dst, b, h) do { _Pragma("unroll") for (int m = 0; m < 4; ++m) _Pragma("unroll") for (int k = 0; k < 2; ++k) dst[m][k] = *(const LAS bf16x8*)(lds + PG8_SA(b, h) + ((aoff ^ (k * 64)) + m * 2048)); } while (0)
; #define PG8_MMA(ai, bj, At, Bt) do { __builtin_amdgcn_s_setprio(1); _Pragma("unroll") for (int m = 0; m < 4; ++m) _Pragma("unroll") for (int n = 0; n < 2; ++n) _Pragma("unroll") for (int k = 0; k < 2; ++k) \
;         acc[ai][bj][m][n] = __builtin_amdgcn_mfma_f32_16x16x32_bf16(Bt[n][k], At[m][k], acc[ai][bj][m][n], 0, 0, 0); __builtin_amdgcn_s_setprio(0); } while (0)
; #define PG8_WAIT_V(n) asm volatile("s_waitcnt vmcnt(" #n ")" ::: "memory")
; #define PG8_WAIT_L(n) asm volatile("s_waitcnt lgkmcnt(" #n ")" ::: "memory")
; #define PG8_BAR __builtin_amdgcn_s_barrier()
; #define PG8_SCHED __builtin_amdgcn_sched_barrier(0)
;     ...
;             PG8_LDA(At, 1, 1); PG8_STAGE(PG8_SB(1, 0), b3, voffB); PG8_STAGE(PG8_SB(1, 1), b3 + hstep, voffB); PG8_STAGE(PG8_SA(1, 0), a3, vs[0]);
;             PG8_WAIT_V(8); PG8_WAIT_L(0); PG8_BAR; if (do1) { PG8_MMA(1, 0, At, B0); PG8_MMA(1, 1, At, B1); } PG8_BAR; PG8_SCHED;
;         }
;         if (wr == 0) PG8_BAR;
	s_add_i32 s38, s42, s49
	v_lshl_add_u64 v[242:243], s[6:7], 0, v[146:147]
	s_mov_b32 m0, s38
	ds_read_b128 v[184:187], v211 offset:49152
	ds_read_b128 v[188:191], v211 offset:51200
	ds_read_b128 v[192:195], v212 offset:49152
	ds_read_b128 v[220:223], v212 offset:51200
	ds_read_b128 v[224:227], v211 offset:53248
	ds_read_b128 v[228:231], v211 offset:55296
	ds_read_b128 v[232:235], v212 offset:53248
	ds_read_b128 v[236:239], v212 offset:55296
	global_load_lds_dwordx4 v[242:243], off
	s_add_i32 m0, s38, 0x2000
	s_add_u32 s4, s4, 0x44000
	v_lshl_add_u64 v[242:243], s[6:7], 0, v[148:149]
	s_addc_u32 s5, s5, 0
	s_add_i32 s6, s43, s49
	global_load_lds_dwordx4 v[242:243], off
	v_lshl_add_u64 v[242:243], s[4:5], 0, v[146:147]
	s_mov_b32 m0, s6
	v_lshl_add_u64 v[196:197], v[196:197], 0, s[92:93]
	global_load_lds_dwordx4 v[242:243], off
	v_lshl_add_u64 v[242:243], s[4:5], 0, v[148:149]
	s_add_i32 m0, s6, 0x2000
	s_nop 0
	global_load_lds_dwordx4 v[242:243], off
	s_mov_b32 m0, s55
	s_nop 0
	global_load_lds_dwordx4 v[196:197], off
	v_lshl_add_u64 v[196:197], v[240:241], 0, s[92:93]
	s_mov_b32 m0, s56
	s_nop 0
	global_load_lds_dwordx4 v[196:197], off
	s_waitcnt vmcnt(8)
	s_waitcnt lgkmcnt(0)
	s_barrier
	s_setprio 1
	s_waitcnt lgkmcnt(0)
	v_mfma_f32_16x16x32_bf16 v[94:97], v[130:133], v[184:187], v[94:97]
	v_mfma_f32_16x16x32_bf16 v[26:29], v[138:141], v[184:187], v[26:29]
	v_mfma_f32_16x16x32_bf16 v[90:93], v[130:133], v[188:191], v[90:93]
	v_mfma_f32_16x16x32_bf16 v[86:89], v[138:141], v[188:191], v[86:89]
	v_mfma_f32_16x16x32_bf16 v[82:85], v[130:133], v[224:227], v[82:85]
	v_mfma_f32_16x16x32_bf16 v[78:81], v[138:141], v[224:227], v[78:81]
	v_mfma_f32_16x16x32_bf16 v[74:77], v[130:133], v[228:231], v[74:77]
	v_mfma_f32_16x16x32_bf16 v[70:73], v[138:141], v[228:231], v[70:73]
	v_mfma_f32_16x16x32_bf16 v[94:97], v[134:137], v[192:195], v[94:97]
	v_mfma_f32_16x16x32_bf16 v[26:29], v[142:145], v[192:195], v[26:29]
	v_mfma_f32_16x16x32_bf16 v[90:93], v[134:137], v[220:223], v[90:93]
	v_mfma_f32_16x16x32_bf16 v[86:89], v[142:145], v[220:223], v[86:89]
	v_mfma_f32_16x16x32_bf16 v[82:85], v[134:137], v[232:235], v[82:85]
	v_mfma_f32_16x16x32_bf16 v[78:81], v[142:145], v[232:235], v[78:81]
	v_mfma_f32_16x16x32_bf16 v[74:77], v[134:137], v[236:239], v[74:77]
	v_mfma_f32_16x16x32_bf16 v[70:73], v[142:145], v[236:239], v[70:73]
	v_mfma_f32_16x16x32_bf16 v[30:33], v[168:171], v[184:187], v[30:33]
	v_mfma_f32_16x16x32_bf16 v[18:21], v[176:179], v[184:187], v[18:21]
	v_mfma_f32_16x16x32_bf16 v[22:25], v[168:171], v[188:191], v[22:25]
	v_mfma_f32_16x16x32_bf16 v[10:13], v[176:179], v[188:191], v[10:13]
	v_mfma_f32_16x16x32_bf16 v[14:17], v[168:171], v[224:227], v[14:17]
	v_mfma_f32_16x16x32_bf16 v[2:5], v[176:179], v[224:227], v[2:5]
	v_mfma_f32_16x16x32_bf16 v[62:65], v[168:171], v[228:231], v[62:65]
	v_mfma_f32_16x16x32_bf16 v[6:9], v[176:179], v[228:231], v[6:9]
	v_mfma_f32_16x16x32_bf16 v[30:33], v[172:175], v[192:195], v[30:33]
	v_mfma_f32_16x16x32_bf16 v[18:21], v[180:183], v[192:195], v[18:21]
	v_mfma_f32_16x16x32_bf16 v[22:25], v[172:175], v[220:223], v[22:25]
	v_mfma_f32_16x16x32_bf16 v[10:13], v[180:183], v[220:223], v[10:13]
	v_mfma_f32_16x16x32_bf16 v[14:17], v[172:175], v[232:235], v[14:17]
	v_mfma_f32_16x16x32_bf16 v[2:5], v[180:183], v[232:235], v[2:5]
	v_mfma_f32_16x16x32_bf16 v[62:65], v[172:175], v[236:239], v[62:65]
	v_mfma_f32_16x16x32_bf16 v[6:9], v[180:183], v[236:239], v[6:9]
	s_setprio 0
	s_barrier
	s_add_i32 s41, s41, 2
	s_add_u32 s37, s37, 0x8000
	s_addc_u32 s40, s40, 0
	s_add_u32 s2, s2, 0x100
	s_addc_u32 s3, s3, 0
	s_cmp_gt_u32 s41, 13
	s_cbranch_scc0 .LBB0_460
	s_and_b64 vcc, exec, s[24:25]
	s_cbranch_vccz .LBB0_463
	s_barrier

; #define PG8_STAGE(bufoff, gbase, voff) do { _Pragma("unroll") for (int _i = 0; _i < 2; ++_i) \
;         __builtin_amdgcn_global_load_lds((const unsigned*)((const char*)(gbase) + (voff)[_i]), (LAS unsigned*)(lds + (bufoff) + ldsw + _i * 8192), 16, 0, 0); } while (0)
; #define PG8_LDA(dst, b, h) do { _Pragma("unroll") for (int m = 0; m < 4; ++m) _Pragma("unroll") for (int k = 0; k < 2; ++k) dst[m][k] = *(const LAS bf16x8*)(lds + PG8_SA(b, h) + ((aoff ^ (k * 64)) + m * 2048)); } while (0)
; #define PG8_LDB(dst, b, h) do { _Pragma("unroll") for (int n = 0; n < 2; ++n) _Pragma("unroll") for (int k = 0; k < 2; ++k) dst[n][k] = *(const LAS bf16x8*)(lds + PG8_SB(b, h) + ((boff ^ (k * 64)) + n * 2048)); } while (0)
; #define PG8_BAR __builtin_amdgcn_s_barrier()
;     ...
;             const bool last = (t == nt - 2);
;             const char* a1 = cA + (size_t)(t + 1) * kstepA;
;             const char* a2 = last ? nA : cA + (size_t)(t + 2) * kstepA; const char* b2 = last ? nB : cB + (size_t)(t + 2) * kstepB;
;             const char* a3 = a2 + kstepA; const char* b3 = b2 + kstepB;
;             unsigned vs[2][2];
;             if constexpr (GATHER) {
;                 if (last && has_next) {
; #pragma unroll
;                     for (int hh = 0; hh < 2; ++hh)
; #pragma unroll
;                         for (int i = 0; i < 2; ++i) voffN[hh][i] = (unsigned)idxl[(ui + 1) * 256 + hh * HALF + sR[i]] * (unsigned)(K * 2) + (unsigned)sC[i] * 2u;
;                 }
; #pragma unroll
;                 for (int hh = 0; hh < 2; ++hh)
; #pragma unroll
;                     for (int i = 0; i < 2; ++i) vs[hh][i] = last ? voffN[hh][i] : voffA[hh][i];
;             } else {
; #pragma unroll
;                 for (int hh = 0; hh < 2; ++hh)
; #pragma unroll
;                     for (int i = 0; i < 2; ++i) vs[hh][i] = voffA[hh][i];
;             }
;             PG8_LDB(B0, 0, 0); PG8_LDB(B1, 0, 1); PG8_SCHED; PG8_LDA(At, 0, 0); PG8_STAGE(PG8_SA(1, 1), a1, voffA[1]);
;             PG8_WAIT_V(8); PG8_WAIT_L(0); PG8_BAR; if (do0) { PG8_MMA(0, 0, At, B0); PG8_MMA(0, 1, At, B1); } PG8_BAR; PG8_SCHED;
;             PG8_LDA(At, 0, 1); PG8_STAGE(PG8_SB(0, 0), b2, voffB); PG8_STAGE(PG8_SB(0, 1), b2 + hstep, voffB); PG8_STAGE(PG8_SA(0, 0), a2, vs[0]);
;             PG8_WAIT_V(8); PG8_WAIT_L(0); PG8_BAR; if (do1) { PG8_MMA(1, 0, At, B0); PG8_MMA(1, 1, At, B1); } PG8_BAR; PG8_SCHED;
.LBB0_557:
	ds_read_b128 v[130:133], v199
	ds_read_b128 v[134:137], v200
	ds_read_b128 v[138:141], v201
	ds_read_b128 v[142:145], v202
	ds_read_b128 v[164:167], v203
	ds_read_b128 v[168:171], v204
	ds_read_b128 v[172:175], v205
	ds_read_b128 v[176:179], v206
	s_add_u32 s2, s0, 0x80
	s_addc_u32 s3, s1, 0
	s_cmp_eq_u32 s41, 12
	s_cselect_b32 s39, s7, s3
	s_cselect_b32 s38, s8, s2
	s_cselect_b32 s3, s25, s40
	s_cselect_b32 s2, s27, s37
	v_lshl_add_u64 v[192:193], s[0:1], 0, v[162:163]
	s_add_i32 m0, s50, 0xc000
	ds_read_b128 v[180:183], v207
	ds_read_b128 v[184:187], v207 offset:2048
	ds_read_b128 v[188:191], v208
	ds_read_b128 v[216:219], v208 offset:2048
	ds_read_b128 v[220:223], v207 offset:4096
	ds_read_b128 v[224:227], v207 offset:6144
	ds_read_b128 v[228:231], v208 offset:4096
	ds_read_b128 v[232:235], v208 offset:6144
	global_load_lds_dwordx4 v[192:193], off
	v_lshl_add_u64 v[192:193], s[0:1], 0, v[160:161]
	s_add_i32 m0, s50, 0xe000
	s_add_u32 s4, s2, 0x4000
	global_load_lds_dwordx4 v[192:193], off
	s_waitcnt vmcnt(8)
	s_waitcnt lgkmcnt(0)
	s_addc_u32 s5, s3, 0
	s_barrier
	s_setprio 1
	s_waitcnt lgkmcnt(0)
	v_mfma_f32_16x16x32_bf16 v[126:129], v[130:133], v[180:183], v[126:129]
	v_mfma_f32_16x16x32_bf16 v[58:61], v[138:141], v[180:183], v[58:61]
	v_mfma_f32_16x16x32_bf16 v[122:125], v[130:133], v[184:187], v[122:125]
	v_mfma_f32_16x16x32_bf16 v[118:121], v[138:141], v[184:187], v[118:121]
	v_mfma_f32_16x16x32_bf16 v[114:117], v[130:133], v[220:223], v[114:117]
	v_mfma_f32_16x16x32_bf16 v[110:113], v[138:141], v[220:223], v[110:113]
	v_mfma_f32_16x16x32_bf16 v[106:109], v[130:133], v[224:227], v[106:109]
	v_mfma_f32_16x16x32_bf16 v[102:105], v[138:141], v[224:227], v[102:105]
	v_mfma_f32_16x16x32_bf16 v[126:129], v[134:137], v[188:191], v[126:129]
	v_mfma_f32_16x16x32_bf16 v[58:61], v[142:145], v[188:191], v[58:61]
	v_mfma_f32_16x16x32_bf16 v[122:125], v[134:137], v[216:219], v[122:125]
	v_mfma_f32_16x16x32_bf16 v[118:121], v[142:145], v[216:219], v[118:121]
	v_mfma_f32_16x16x32_bf16 v[114:117], v[134:137], v[228:231], v[114:117]
	v_mfma_f32_16x16x32_bf16 v[110:113], v[142:145], v[228:231], v[110:113]
	v_mfma_f32_16x16x32_bf16 v[106:109], v[134:137], v[232:235], v[106:109]
	v_mfma_f32_16x16x32_bf16 v[102:105], v[142:145], v[232:235], v[102:105]
	v_mfma_f32_16x16x32_bf16 v[66:69], v[164:167], v[180:183], v[66:69]
	v_mfma_f32_16x16x32_bf16 v[50:53], v[172:175], v[180:183], v[50:53]
	v_mfma_f32_16x16x32_bf16 v[54:57], v[164:167], v[184:187], v[54:57]
	v_mfma_f32_16x16x32_bf16 v[42:45], v[172:175], v[184:187], v[42:45]
	v_mfma_f32_16x16x32_bf16 v[46:49], v[164:167], v[220:223], v[46:49]
	v_mfma_f32_16x16x32_bf16 v[34:37], v[172:175], v[220:223], v[34:37]
	v_mfma_f32_16x16x32_bf16 v[98:101], v[164:167], v[224:227], v[98:101]
	v_mfma_f32_16x16x32_bf16 v[38:41], v[172:175], v[224:227], v[38:41]
	v_mfma_f32_16x16x32_bf16 v[66:69], v[168:171], v[188:191], v[66:69]
	v_mfma_f32_16x16x32_bf16 v[50:53], v[176:179], v[188:191], v[50:53]
	v_mfma_f32_16x16x32_bf16 v[54:57], v[168:171], v[216:219], v[54:57]
	v_mfma_f32_16x16x32_bf16 v[42:45], v[176:179], v[216:219], v[42:45]
	v_mfma_f32_16x16x32_bf16 v[46:49], v[168:171], v[228:231], v[46:49]
	v_mfma_f32_16x16x32_bf16 v[34:37], v[176:179], v[228:231], v[34:37]
	v_mfma_f32_16x16x32_bf16 v[98:101], v[168:171], v[232:235], v[98:101]
	v_mfma_f32_16x16x32_bf16 v[38:41], v[176:179], v[232:235], v[38:41]
	s_setprio 0
	s_barrier
	s_add_i32 s42, s63, s49
	v_lshl_add_u64 v[192:193], s[2:3], 0, v[146:147]
	s_mov_b32 m0, s42
	ds_read_b128 v[180:183], v207 offset:16384
	ds_read_b128 v[184:187], v207 offset:18432
	ds_read_b128 v[188:191], v208 offset:16384
	ds_read_b128 v[216:219], v208 offset:18432
	ds_read_b128 v[220:223], v207 offset:20480
	ds_read_b128 v[224:227], v207 offset:22528
	ds_read_b128 v[228:231], v208 offset:20480
	ds_read_b128 v[232:235], v208 offset:22528
	global_load_lds_dwordx4 v[192:193], off
	s_add_i32 m0, s42, 0x2000
	s_add_u32 s42, s2, 0x40000
	v_lshl_add_u64 v[192:193], s[2:3], 0, v[148:149]
	s_addc_u32 s43, s3, 0
	s_add_i32 s73, s64, s49
	global_load_lds_dwordx4 v[192:193], off
	v_lshl_add_u64 v[192:193], s[42:43], 0, v[146:147]
	s_mov_b32 m0, s73
	v_lshl_add_u64 v[236:237], s[38:39], 0, v[152:153]
	global_load_lds_dwordx4 v[192:193], off
	v_lshl_add_u64 v[192:193], s[42:43], 0, v[148:149]
	s_add_i32 m0, s73, 0x2000
	s_nop 0
	global_load_lds_dwordx4 v[192:193], off
	v_lshl_add_u64 v[192:193], s[38:39], 0, v[150:151]
	s_mov_b32 m0, s50
	s_nop 0
	global_load_lds_dwordx4 v[192:193], off
	s_mov_b32 m0, s51
	s_nop 0
	global_load_lds_dwordx4 v[236:237], off
	s_waitcnt vmcnt(8)
	s_waitcnt lgkmcnt(0)
	s_barrier
; #define PG8_STAGE(bufoff, gbase, voff) do { _Pragma("unroll") for (int _i = 0; _i < 2; ++_i) \
;         __builtin_amdgcn_global_load_lds((const unsigned*)((const char*)(gbase) + (voff)[_i]), (LAS unsigned*)(lds + (bufoff) + ldsw + _i * 8192), 16, 0, 0); } while (0)
; #define PG8_LDA(dst, b, h) do { _Pragma("unroll") for (int m = 0; m < 4; ++m) _Pragma("unroll") for (int k = 0; k < 2; ++k) dst[m][k] = *(const LAS bf16x8*)(lds + PG8_SA(b, h) + ((aoff ^ (k * 64)) + m * 2048)); } while (0)
; #define PG8_LDB(dst, b, h) do { _Pragma("unroll") for (int n = 0; n < 2; ++n) _Pragma("unroll") for (int k = 0; k < 2; ++k) dst[n][k] = *(const LAS bf16x8*)(lds + PG8_SB(b, h) + ((boff ^ (k * 64)) + n * 2048)); } while (0)
; #define PG8_MMA(ai, bj, At, Bt) do { __builtin_amdgcn_s_setprio(1); _Pragma("unroll") for (int m = 0; m < 4; ++m) _Pragma("unroll") for (int n = 0; n < 2; ++n) _Pragma("unroll") for (int k = 0; k < 2; ++k) \
;         acc[ai][bj][m][n] = __builtin_amdgcn_mfma_f32_16x16x32_bf16(Bt[n][k], At[m][k], acc[ai][bj][m][n], 0, 0, 0); __builtin_amdgcn_s_setprio(0); } while (0)
; #define PG8_WAIT_V(n) asm volatile("s_waitcnt vmcnt(" #n ")" ::: "memory")
; #define PG8_WAIT_L(n) asm volatile("s_waitcnt lgkmcnt(" #n ")" ::: "memory")
; #define PG8_BAR __builtin_amdgcn_s_barrier()
; #define PG8_SCHED __builtin_amdgcn_sched_barrier(0)
;     ...
;             PG8_WAIT_V(8); PG8_WAIT_L(0); PG8_BAR; if (do1) { PG8_MMA(1, 0, At, B0); PG8_MMA(1, 1, At, B1); } PG8_BAR; PG8_SCHED;
;             PG8_LDB(B0, 1, 0); PG8_LDB(B1, 1, 1); PG8_SCHED; PG8_LDA(At, 1, 0); PG8_STAGE(PG8_SA(0, 1), a2, vs[1]);
;             PG8_WAIT_V(8); PG8_WAIT_L(0); PG8_BAR; if (do0) { PG8_MMA(0, 0, At, B0); PG8_MMA(0, 1, At, B1); } PG8_BAR; PG8_SCHED;
	s_setprio 1
	s_waitcnt lgkmcnt(0)
	v_mfma_f32_16x16x32_bf16 v[94:97], v[130:133], v[180:183], v[94:97]
	v_mfma_f32_16x16x32_bf16 v[26:29], v[138:141], v[180:183], v[26:29]
	v_mfma_f32_16x16x32_bf16 v[90:93], v[130:133], v[184:187], v[90:93]
	v_mfma_f32_16x16x32_bf16 v[86:89], v[138:141], v[184:187], v[86:89]
	v_mfma_f32_16x16x32_bf16 v[82:85], v[130:133], v[220:223], v[82:85]
	v_mfma_f32_16x16x32_bf16 v[78:81], v[138:141], v[220:223], v[78:81]
	v_mfma_f32_16x16x32_bf16 v[74:77], v[130:133], v[224:227], v[74:77]
	v_mfma_f32_16x16x32_bf16 v[70:73], v[138:141], v[224:227], v[70:73]
	v_mfma_f32_16x16x32_bf16 v[94:97], v[134:137], v[188:191], v[94:97]
	v_mfma_f32_16x16x32_bf16 v[26:29], v[142:145], v[188:191], v[26:29]
	v_mfma_f32_16x16x32_bf16 v[90:93], v[134:137], v[216:219], v[90:93]
	v_mfma_f32_16x16x32_bf16 v[86:89], v[142:145], v[216:219], v[86:89]
	v_mfma_f32_16x16x32_bf16 v[82:85], v[134:137], v[228:231], v[82:85]
	v_mfma_f32_16x16x32_bf16 v[78:81], v[142:145], v[228:231], v[78:81]
	v_mfma_f32_16x16x32_bf16 v[74:77], v[134:137], v[232:235], v[74:77]
	v_mfma_f32_16x16x32_bf16 v[70:73], v[142:145], v[232:235], v[70:73]
	v_mfma_f32_16x16x32_bf16 v[30:33], v[164:167], v[180:183], v[30:33]
	v_mfma_f32_16x16x32_bf16 v[18:21], v[172:175], v[180:183], v[18:21]
	v_mfma_f32_16x16x32_bf16 v[22:25], v[164:167], v[184:187], v[22:25]
	v_mfma_f32_16x16x32_bf16 v[10:13], v[172:175], v[184:187], v[10:13]
	v_mfma_f32_16x16x32_bf16 v[14:17], v[164:167], v[220:223], v[14:17]
	v_mfma_f32_16x16x32_bf16 v[2:5], v[172:175], v[220:223], v[2:5]
	v_mfma_f32_16x16x32_bf16 v[62:65], v[164:167], v[224:227], v[62:65]
	v_mfma_f32_16x16x32_bf16 v[6:9], v[172:175], v[224:227], v[6:9]
	v_mfma_f32_16x16x32_bf16 v[30:33], v[168:171], v[188:191], v[30:33]
	v_mfma_f32_16x16x32_bf16 v[18:21], v[176:179], v[188:191], v[18:21]
	v_mfma_f32_16x16x32_bf16 v[22:25], v[168:171], v[216:219], v[22:25]
	v_mfma_f32_16x16x32_bf16 v[10:13], v[176:179], v[216:219], v[10:13]
	v_mfma_f32_16x16x32_bf16 v[14:17], v[168:171], v[228:231], v[14:17]
	v_mfma_f32_16x16x32_bf16 v[2:5], v[176:179], v[228:231], v[2:5]
	v_mfma_f32_16x16x32_bf16 v[62:65], v[168:171], v[232:235], v[62:65]
	v_mfma_f32_16x16x32_bf16 v[6:9], v[176:179], v[232:235], v[6:9]
	s_setprio 0
	s_barrier
	s_add_i32 s42, 0, 0x18000
	s_add_i32 s43, 0, 0x1c000
	v_add_u32_e32 v130, s42, v196
	v_add_u32_e32 v134, s42, v197
	v_add_u32_e32 v158, s43, v196
	v_add_u32_e32 v168, s43, v197
	ds_read_b128 v[130:133], v130
	ds_read_b128 v[134:137], v134
	ds_read_b128 v[138:141], v209
	ds_read_b128 v[142:145], v210
	ds_read_b128 v[164:167], v158
	ds_read_b128 v[168:171], v168
	ds_read_b128 v[172:175], v211
	ds_read_b128 v[176:179], v212
	s_mov_b32 m0, s52
	v_lshl_add_u64 v[238:239], s[38:39], 0, v[154:155]
	ds_read_b128 v[180:183], v207 offset:32768
	ds_read_b128 v[184:187], v207 offset:34816
	ds_read_b128 v[188:191], v208 offset:32768
	ds_read_b128 v[216:219], v208 offset:34816
	ds_read_b128 v[220:223], v207 offset:36864
	ds_read_b128 v[224:227], v207 offset:38912
	ds_read_b128 v[228:231], v208 offset:36864
	ds_read_b128 v[232:235], v208 offset:38912
	global_load_lds_dwordx4 v[238:239], off
	v_lshl_add_u64 v[238:239], s[38:39], 0, v[156:157]
	s_mov_b32 m0, s53
	s_nop 0
	global_load_lds_dwordx4 v[238:239], off
	s_waitcnt vmcnt(8)
	s_waitcnt lgkmcnt(0)
	s_barrier
	s_setprio 1
	s_waitcnt lgkmcnt(0)
	v_mfma_f32_16x16x32_bf16 v[126:129], v[130:133], v[180:183], v[126:129]
	v_mfma_f32_16x16x32_bf16 v[58:61], v[138:141], v[180:183], v[58:61]
	v_mfma_f32_16x16x32_bf16 v[122:125], v[130:133], v[184:187], v[122:125]
	v_mfma_f32_16x16x32_bf16 v[118:121], v[138:141], v[184:187], v[118:121]
	v_mfma_f32_16x16x32_bf16 v[114:117], v[130:133], v[220:223], v[114:117]
	v_mfma_f32_16x16x32_bf16 v[110:113], v[138:141], v[220:223], v[110:113]
	v_mfma_f32_16x16x32_bf16 v[106:109], v[130:133], v[224:227], v[106:109]
	v_mfma_f32_16x16x32_bf16 v[102:105], v[138:141], v[224:227], v[102:105]
	v_mfma_f32_16x16x32_bf16 v[126:129], v[134:137], v[188:191], v[126:129]
	v_mfma_f32_16x16x32_bf16 v[58:61], v[142:145], v[188:191], v[58:61]
	v_mfma_f32_16x16x32_bf16 v[122:125], v[134:137], v[216:219], v[122:125]
	v_mfma_f32_16x16x32_bf16 v[118:121], v[142:145], v[216:219], v[118:121]
	v_mfma_f32_16x16x32_bf16 v[114:117], v[134:137], v[228:231], v[114:117]
	v_mfma_f32_16x16x32_bf16 v[110:113], v[142:145], v[228:231], v[110:113]
	v_mfma_f32_16x16x32_bf16 v[106:109], v[134:137], v[232:235], v[106:109]
	v_mfma_f32_16x16x32_bf16 v[102:105], v[142:145], v[232:235], v[102:105]
	v_mfma_f32_16x16x32_bf16 v[66:69], v[164:167], v[180:183], v[66:69]
	v_mfma_f32_16x16x32_bf16 v[50:53], v[172:175], v[180:183], v[50:53]
	v_mfma_f32_16x16x32_bf16 v[54:57], v[164:167], v[184:187], v[54:57]
	v_mfma_f32_16x16x32_bf16 v[42:45], v[172:175], v[184:187], v[42:45]
	v_mfma_f32_16x16x32_bf16 v[46:49], v[164:167], v[220:223], v[46:49]
	v_mfma_f32_16x16x32_bf16 v[34:37], v[172:175], v[220:223], v[34:37]
	v_mfma_f32_16x16x32_bf16 v[98:101], v[164:167], v[224:227], v[98:101]
	v_mfma_f32_16x16x32_bf16 v[38:41], v[172:175], v[224:227], v[38:41]
	v_mfma_f32_16x16x32_bf16 v[66:69], v[168:171], v[188:191], v[66:69]
	v_mfma_f32_16x16x32_bf16 v[50:53], v[176:179], v[188:191], v[50:53]
	v_mfma_f32_16x16x32_bf16 v[54:57], v[168:171], v[216:219], v[54:57]
	v_mfma_f32_16x16x32_bf16 v[42:45], v[176:179], v[216:219], v[42:45]
	v_mfma_f32_16x16x32_bf16 v[46:49], v[168:171], v[228:231], v[46:49]
	v_mfma_f32_16x16x32_bf16 v[34:37], v[176:179], v[228:231], v[34:37]
	v_mfma_f32_16x16x32_bf16 v[98:101], v[168:171], v[232:235], v[98:101]
	v_mfma_f32_16x16x32_bf16 v[38:41], v[176:179], v[232:235], v[38:41]
	s_setprio 0
	s_barrier
; #define PG8_STAGE(bufoff, gbase, voff) do { _Pragma("unroll") for (int _i = 0; _i < 2; ++_i) \
;         __builtin_amdgcn_global_load_lds((const unsigned*)((const char*)(gbase) + (voff)[_i]), (LAS unsigned*)(lds + (bufoff) + ldsw + _i * 8192), 16, 0, 0); } while (0)
; #define PG8_LDA(dst, b, h) do { _Pragma("unroll") for (int m = 0; m < 4; ++m) _Pragma("unroll") for (int k = 0; k < 2; ++k) dst[m][k] = *(const LAS bf16x8*)(lds + PG8_SA(b, h) + ((aoff ^ (k * 64)) + m * 2048)); } while (0)
; #define PG8_MMA(ai, bj, At, Bt) do { __builtin_amdgcn_s_setprio(1); _Pragma("unroll") for (int m = 0; m < 4; ++m) _Pragma("unroll") for (int n = 0; n < 2; ++n) _Pragma("unroll") for (int k = 0; k < 2; ++k) \
;         acc[ai][bj][m][n] = __builtin_amdgcn_mfma_f32_16x16x32_bf16(Bt[n][k], At[m][k], acc[ai][bj][m][n], 0, 0, 0); __builtin_amdgcn_s_setprio(0); } while (0)
; #define PG8_WAIT_V(n) asm volatile("s_waitcnt vmcnt(" #n ")" ::: "memory")
; #define PG8_WAIT_L(n) asm volatile("s_waitcnt lgkmcnt(" #n ")" ::: "memory")
; #define PG8_BAR __builtin_amdgcn_s_barrier()
; #define PG8_SCHED __builtin_amdgcn_sched_barrier(0)
;     ...
;             PG8_LDA(At, 1, 1); PG8_STAGE(PG8_SB(1, 0), b3, voffB); PG8_STAGE(PG8_SB(1, 1), b3 + hstep, voffB); PG8_STAGE(PG8_SA(1, 0), a3, vs[0]);
;             PG8_WAIT_V(8); PG8_WAIT_L(0); PG8_BAR; if (do1) { PG8_MMA(1, 0, At, B0); PG8_MMA(1, 1, At, B1); } PG8_BAR; PG8_SCHED;
;         }
;         if (wr == 0) PG8_BAR;
	s_add_i32 s38, s42, s49
	v_lshl_add_u64 v[238:239], s[4:5], 0, v[146:147]
	s_mov_b32 m0, s38
	ds_read_b128 v[180:183], v207 offset:49152
	ds_read_b128 v[184:187], v207 offset:51200
	ds_read_b128 v[188:191], v208 offset:49152
	ds_read_b128 v[216:219], v208 offset:51200
	ds_read_b128 v[220:223], v207 offset:53248
	ds_read_b128 v[224:227], v207 offset:55296
	ds_read_b128 v[228:231], v208 offset:53248
	ds_read_b128 v[232:235], v208 offset:55296
	global_load_lds_dwordx4 v[238:239], off
	s_add_i32 m0, s38, 0x2000
	s_add_u32 s2, s2, 0x44000
	v_lshl_add_u64 v[238:239], s[4:5], 0, v[148:149]
	s_addc_u32 s3, s3, 0
	s_add_i32 s4, s43, s49
	global_load_lds_dwordx4 v[238:239], off
	v_lshl_add_u64 v[238:239], s[2:3], 0, v[146:147]
	s_mov_b32 m0, s4
	v_lshl_add_u64 v[192:193], v[192:193], 0, s[92:93]
	global_load_lds_dwordx4 v[238:239], off
	v_lshl_add_u64 v[238:239], s[2:3], 0, v[148:149]
	s_add_i32 m0, s4, 0x2000
	s_nop 0
	global_load_lds_dwordx4 v[238:239], off
	s_mov_b32 m0, s55
	s_nop 0
	global_load_lds_dwordx4 v[192:193], off
	v_lshl_add_u64 v[192:193], v[236:237], 0, s[92:93]
	s_mov_b32 m0, s56
	s_nop 0
	global_load_lds_dwordx4 v[192:193], off
	s_waitcnt vmcnt(8)
	s_waitcnt lgkmcnt(0)
	s_barrier
	s_setprio 1
	s_waitcnt lgkmcnt(0)
	v_mfma_f32_16x16x32_bf16 v[94:97], v[130:133], v[180:183], v[94:97]
	v_mfma_f32_16x16x32_bf16 v[26:29], v[138:141], v[180:183], v[26:29]
	v_mfma_f32_16x16x32_bf16 v[90:93], v[130:133], v[184:187], v[90:93]
	v_mfma_f32_16x16x32_bf16 v[86:89], v[138:141], v[184:187], v[86:89]
	v_mfma_f32_16x16x32_bf16 v[82:85], v[130:133], v[220:223], v[82:85]
	v_mfma_f32_16x16x32_bf16 v[78:81], v[138:141], v[220:223], v[78:81]
	v_mfma_f32_16x16x32_bf16 v[74:77], v[130:133], v[224:227], v[74:77]
	v_mfma_f32_16x16x32_bf16 v[70:73], v[138:141], v[224:227], v[70:73]
	v_mfma_f32_16x16x32_bf16 v[94:97], v[134:137], v[188:191], v[94:97]
	v_mfma_f32_16x16x32_bf16 v[26:29], v[142:145], v[188:191], v[26:29]
	v_mfma_f32_16x16x32_bf16 v[90:93], v[134:137], v[216:219], v[90:93]
	v_mfma_f32_16x16x32_bf16 v[86:89], v[142:145], v[216:219], v[86:89]
	v_mfma_f32_16x16x32_bf16 v[82:85], v[134:137], v[228:231], v[82:85]
	v_mfma_f32_16x16x32_bf16 v[78:81], v[142:145], v[228:231], v[78:81]
	v_mfma_f32_16x16x32_bf16 v[74:77], v[134:137], v[232:235], v[74:77]
	v_mfma_f32_16x16x32_bf16 v[70:73], v[142:145], v[232:235], v[70:73]
	v_mfma_f32_16x16x32_bf16 v[30:33], v[164:167], v[180:183], v[30:33]
	v_mfma_f32_16x16x32_bf16 v[18:21], v[172:175], v[180:183], v[18:21]
	v_mfma_f32_16x16x32_bf16 v[22:25], v[164:167], v[184:187], v[22:25]
	v_mfma_f32_16x16x32_bf16 v[10:13], v[172:175], v[184:187], v[10:13]
	v_mfma_f32_16x16x32_bf16 v[14:17], v[164:167], v[220:223], v[14:17]
	v_mfma_f32_16x16x32_bf16 v[2:5], v[172:175], v[220:223], v[2:5]
	v_mfma_f32_16x16x32_bf16 v[62:65], v[164:167], v[224:227], v[62:65]
	v_mfma_f32_16x16x32_bf16 v[6:9], v[172:175], v[224:227], v[6:9]
	v_mfma_f32_16x16x32_bf16 v[30:33], v[168:171], v[188:191], v[30:33]
	v_mfma_f32_16x16x32_bf16 v[18:21], v[176:179], v[188:191], v[18:21]
	v_mfma_f32_16x16x32_bf16 v[22:25], v[168:171], v[216:219], v[22:25]
	v_mfma_f32_16x16x32_bf16 v[10:13], v[176:179], v[216:219], v[10:13]
	v_mfma_f32_16x16x32_bf16 v[14:17], v[168:171], v[228:231], v[14:17]
	v_mfma_f32_16x16x32_bf16 v[2:5], v[176:179], v[228:231], v[2:5]
	v_mfma_f32_16x16x32_bf16 v[62:65], v[168:171], v[232:235], v[62:65]
	v_mfma_f32_16x16x32_bf16 v[6:9], v[176:179], v[232:235], v[6:9]
	s_setprio 0
	s_barrier
	s_add_i32 s41, s41, 2
	s_add_u32 s37, s37, 0x8000
	s_addc_u32 s40, s40, 0
	s_add_u32 s0, s0, 0x100
	s_addc_u32 s1, s1, 0
	s_cmp_gt_u32 s41, 13
	s_cbranch_scc0 .LBB0_557
	s_and_b64 vcc, exec, s[80:81]
	s_cbranch_vccz .LBB0_560
	s_barrier

; #define PG8_STAGE(bufoff, gbase, voff) do { _Pragma("unroll") for (int _i = 0; _i < 2; ++_i) \
;         __builtin_amdgcn_global_load_lds((const unsigned*)((const char*)(gbase) + (voff)[_i]), (LAS unsigned*)(lds + (bufoff) + ldsw + _i * 8192), 16, 0, 0); } while (0)
; #define PG8_LDA(dst, b, h) do { _Pragma("unroll") for (int m = 0; m < 4; ++m) _Pragma("unroll") for (int k = 0; k < 2; ++k) dst[m][k] = *(const LAS bf16x8*)(lds + PG8_SA(b, h) + ((aoff ^ (k * 64)) + m * 2048)); } while (0)
; #define PG8_LDB(dst, b, h) do { _Pragma("unroll") for (int n = 0; n < 2; ++n) _Pragma("unroll") for (int k = 0; k < 2; ++k) dst[n][k] = *(const LAS bf16x8*)(lds + PG8_SB(b, h) + ((boff ^ (k * 64)) + n * 2048)); } while (0)
; #define PG8_BAR __builtin_amdgcn_s_barrier()
;     ...
;             const bool last = (t == nt - 2);
;             const char* a1 = cA + (size_t)(t + 1) * kstepA;
;             const char* a2 = last ? nA : cA + (size_t)(t + 2) * kstepA; const char* b2 = last ? nB : cB + (size_t)(t + 2) * kstepB;
;             const char* a3 = a2 + kstepA; const char* b3 = b2 + kstepB;
;             unsigned vs[2][2];
;             if constexpr (GATHER) {
;                 if (last && has_next) {
; #pragma unroll
;                     for (int hh = 0; hh < 2; ++hh)
; #pragma unroll
;                         for (int i = 0; i < 2; ++i) voffN[hh][i] = (unsigned)idxl[(ui + 1) * 256 + hh * HALF + sR[i]] * (unsigned)(K * 2) + (unsigned)sC[i] * 2u;
;                 }
; #pragma unroll
;                 for (int hh = 0; hh < 2; ++hh)
; #pragma unroll
;                     for (int i = 0; i < 2; ++i) vs[hh][i] = last ? voffN[hh][i] : voffA[hh][i];
;             } else {
; #pragma unroll
;                 for (int hh = 0; hh < 2; ++hh)
; #pragma unroll
;                     for (int i = 0; i < 2; ++i) vs[hh][i] = voffA[hh][i];
;             }
;             PG8_LDB(B0, 0, 0); PG8_LDB(B1, 0, 1); PG8_SCHED; PG8_LDA(At, 0, 0); PG8_STAGE(PG8_SA(1, 1), a1, voffA[1]);
;             PG8_WAIT_V(8); PG8_WAIT_L(0); PG8_BAR; if (do0) { PG8_MMA(0, 0, At, B0); PG8_MMA(0, 1, At, B1); } PG8_BAR; PG8_SCHED;
;             PG8_LDA(At, 0, 1); PG8_STAGE(PG8_SB(0, 0), b2, voffB); PG8_STAGE(PG8_SB(0, 1), b2 + hstep, voffB); PG8_STAGE(PG8_SA(0, 0), a2, vs[0]);
;             PG8_WAIT_V(8); PG8_WAIT_L(0); PG8_BAR; if (do1) { PG8_MMA(1, 0, At, B0); PG8_MMA(1, 1, At, B1); } PG8_BAR; PG8_SCHED;
.LBB0_1008:
	v_add_u32_e32 v2, s54, v226
	v_add_u32_e32 v134, s54, v227
	ds_read_b128 v[150:153], v2
	ds_read_b128 v[154:157], v134
	v_add_u32_e32 v2, s55, v226
	v_add_u32_e32 v134, s55, v227
	ds_read_b128 v[158:161], v2
	ds_read_b128 v[162:165], v134
	v_add_u32_e32 v2, s56, v226
	v_add_u32_e32 v138, s56, v227
	ds_read_b128 v[134:137], v2
	ds_read_b128 v[138:141], v138
	v_add_u32_e32 v2, s57, v226
	v_add_u32_e32 v146, s57, v227
	ds_read_b128 v[142:145], v2
	ds_read_b128 v[146:149], v146
	v_lshl_add_u64 v[224:225], v[222:223], 0, s[28:29]
	s_add_i32 m0, s23, 0xc000
	s_waitcnt lgkmcnt(0)
	ds_read_b128 v[190:193], v228
	ds_read_b128 v[178:181], v228 offset:2048
	ds_read_b128 v[194:197], v229
	ds_read_b128 v[182:185], v229 offset:2048
	ds_read_b128 v[174:177], v228 offset:4096
	ds_read_b128 v[166:169], v228 offset:6144
	ds_read_b128 v[186:189], v229 offset:4096
	ds_read_b128 v[170:173], v229 offset:6144
	global_load_lds_dwordx4 v[224:225], off
	v_lshl_add_u64 v[224:225], v[220:221], 0, s[28:29]
	s_add_i32 m0, s23, 0xe000
	v_cndmask_b32_e64 v2, 0, 1, s[26:27]
	global_load_lds_dwordx4 v[224:225], off
	s_waitcnt vmcnt(8)
	s_waitcnt lgkmcnt(0)
	v_cmp_ne_u32_e64 s[8:9], 1, v2
	s_andn2_b64 vcc, exec, s[26:27]
	s_barrier
	s_cbranch_vccnz .LBB0_1010
	s_setprio 1
	s_waitcnt lgkmcnt(0)
	v_mfma_f32_16x16x32_bf16 v[130:133], v[150:153], v[190:193], v[130:133]
	v_mfma_f32_16x16x32_bf16 v[126:129], v[158:161], v[190:193], v[126:129]
	v_mfma_f32_16x16x32_bf16 v[114:117], v[150:153], v[178:181], v[114:117]
	v_mfma_f32_16x16x32_bf16 v[110:113], v[158:161], v[178:181], v[110:113]
	v_mfma_f32_16x16x32_bf16 v[98:101], v[150:153], v[174:177], v[98:101]
	v_mfma_f32_16x16x32_bf16 v[94:97], v[158:161], v[174:177], v[94:97]
	v_mfma_f32_16x16x32_bf16 v[82:85], v[150:153], v[166:169], v[82:85]
	v_mfma_f32_16x16x32_bf16 v[78:81], v[158:161], v[166:169], v[78:81]
	v_mfma_f32_16x16x32_bf16 v[130:133], v[154:157], v[194:197], v[130:133]
	v_mfma_f32_16x16x32_bf16 v[126:129], v[162:165], v[194:197], v[126:129]
	v_mfma_f32_16x16x32_bf16 v[114:117], v[154:157], v[182:185], v[114:117]
	v_mfma_f32_16x16x32_bf16 v[110:113], v[162:165], v[182:185], v[110:113]
	v_mfma_f32_16x16x32_bf16 v[98:101], v[154:157], v[186:189], v[98:101]
	v_mfma_f32_16x16x32_bf16 v[94:97], v[162:165], v[186:189], v[94:97]
	v_mfma_f32_16x16x32_bf16 v[82:85], v[154:157], v[170:173], v[82:85]
	v_mfma_f32_16x16x32_bf16 v[78:81], v[162:165], v[170:173], v[78:81]
	v_mfma_f32_16x16x32_bf16 v[122:125], v[134:137], v[190:193], v[122:125]
	v_mfma_f32_16x16x32_bf16 v[118:121], v[142:145], v[190:193], v[118:121]
	v_mfma_f32_16x16x32_bf16 v[106:109], v[134:137], v[178:181], v[106:109]
	v_mfma_f32_16x16x32_bf16 v[102:105], v[142:145], v[178:181], v[102:105]
	v_mfma_f32_16x16x32_bf16 v[90:93], v[134:137], v[174:177], v[90:93]
	v_mfma_f32_16x16x32_bf16 v[86:89], v[142:145], v[174:177], v[86:89]
	v_mfma_f32_16x16x32_bf16 v[74:77], v[134:137], v[166:169], v[74:77]
	v_mfma_f32_16x16x32_bf16 v[70:73], v[142:145], v[166:169], v[70:73]
	v_mfma_f32_16x16x32_bf16 v[122:125], v[138:141], v[194:197], v[122:125]
	v_mfma_f32_16x16x32_bf16 v[118:121], v[146:149], v[194:197], v[118:121]
	v_mfma_f32_16x16x32_bf16 v[106:109], v[138:141], v[182:185], v[106:109]
	v_mfma_f32_16x16x32_bf16 v[102:105], v[146:149], v[182:185], v[102:105]
	v_mfma_f32_16x16x32_bf16 v[90:93], v[138:141], v[186:189], v[90:93]
	v_mfma_f32_16x16x32_bf16 v[86:89], v[146:149], v[186:189], v[86:89]
	v_mfma_f32_16x16x32_bf16 v[74:77], v[138:141], v[170:173], v[74:77]
	v_mfma_f32_16x16x32_bf16 v[70:73], v[146:149], v[170:173], v[70:73]
	s_setprio 0
.LBB0_1010:
	s_add_u32 s10, s90, s28
	s_addc_u32 s11, s91, s29
	s_add_u32 s30, s10, 0x4213700
	s_addc_u32 s31, s11, 0
	s_and_b64 s[10:11], s[6:7], exec
	v_cndmask_b32_e64 v2, v218, v4, s[6:7]
	v_cndmask_b32_e64 v224, v219, v5, s[6:7]
	s_cselect_b32 s35, s83, s31
	s_cselect_b32 s34, s82, s30
	s_cselect_b32 s31, s21, s64
	s_cselect_b32 s30, s20, s19
	s_barrier
	s_mov_b32 m0, s37
	v_lshl_add_u64 v[232:233], s[30:31], 0, v[202:203]
	s_add_u32 s10, s30, 0x40000
	s_waitcnt lgkmcnt(0)
	ds_read_b128 v[190:193], v228 offset:16384
	ds_read_b128 v[178:181], v228 offset:18432
	ds_read_b128 v[194:197], v229 offset:16384
	ds_read_b128 v[182:185], v229 offset:18432
	ds_read_b128 v[174:177], v228 offset:20480
	ds_read_b128 v[166:169], v228 offset:22528
	ds_read_b128 v[186:189], v229 offset:20480
	ds_read_b128 v[170:173], v229 offset:22528
	global_load_lds_dwordx4 v[232:233], off
	v_lshl_add_u64 v[232:233], s[30:31], 0, v[204:205]
	s_mov_b32 m0, s38
	s_addc_u32 s11, s31, 0
	global_load_lds_dwordx4 v[232:233], off
	v_lshl_add_u64 v[232:233], s[10:11], 0, v[202:203]
	s_mov_b32 m0, s39
	v_cndmask_b32_e64 v213, 0, 1, s[24:25]
	global_load_lds_dwordx4 v[232:233], off
	v_lshl_add_u64 v[232:233], s[10:11], 0, v[204:205]
	s_mov_b32 m0, s40
	v_cmp_ne_u32_e64 s[10:11], 1, v213
	global_load_lds_dwordx4 v[232:233], off
	s_mov_b32 m0, s23
	s_andn2_b64 vcc, exec, s[24:25]
	global_load_lds_dwordx4 v2, s[34:35]
	s_mov_b32 m0, s41
	s_nop 0
	global_load_lds_dwordx4 v224, s[34:35]
	s_waitcnt vmcnt(8)
	s_waitcnt lgkmcnt(0)
	s_barrier
	s_cbranch_vccnz .LBB0_1012
; #define PG8_STAGE(bufoff, gbase, voff) do { _Pragma("unroll") for (int _i = 0; _i < 2; ++_i) \
;         __builtin_amdgcn_global_load_lds((const unsigned*)((const char*)(gbase) + (voff)[_i]), (LAS unsigned*)(lds + (bufoff) + ldsw + _i * 8192), 16, 0, 0); } while (0)
; #define PG8_LDA(dst, b, h) do { _Pragma("unroll") for (int m = 0; m < 4; ++m) _Pragma("unroll") for (int k = 0; k < 2; ++k) dst[m][k] = *(const LAS bf16x8*)(lds + PG8_SA(b, h) + ((aoff ^ (k * 64)) + m * 2048)); } while (0)
; #define PG8_LDB(dst, b, h) do { _Pragma("unroll") for (int n = 0; n < 2; ++n) _Pragma("unroll") for (int k = 0; k < 2; ++k) dst[n][k] = *(const LAS bf16x8*)(lds + PG8_SB(b, h) + ((boff ^ (k * 64)) + n * 2048)); } while (0)
; #define PG8_MMA(ai, bj, At, Bt) do { __builtin_amdgcn_s_setprio(1); _Pragma("unroll") for (int m = 0; m < 4; ++m) _Pragma("unroll") for (int n = 0; n < 2; ++n) _Pragma("unroll") for (int k = 0; k < 2; ++k) \
;         acc[ai][bj][m][n] = __builtin_amdgcn_mfma_f32_16x16x32_bf16(Bt[n][k], At[m][k], acc[ai][bj][m][n], 0, 0, 0); __builtin_amdgcn_s_setprio(0); } while (0)
; #define PG8_WAIT_V(n) asm volatile("s_waitcnt vmcnt(" #n ")" ::: "memory")
; #define PG8_WAIT_L(n) asm volatile("s_waitcnt lgkmcnt(" #n ")" ::: "memory")
; #define PG8_BAR __builtin_amdgcn_s_barrier()
; #define PG8_SCHED __builtin_amdgcn_sched_barrier(0)
;     ...
;             PG8_WAIT_V(8); PG8_WAIT_L(0); PG8_BAR; if (do1) { PG8_MMA(1, 0, At, B0); PG8_MMA(1, 1, At, B1); } PG8_BAR; PG8_SCHED;
;             PG8_LDB(B0, 1, 0); PG8_LDB(B1, 1, 1); PG8_SCHED; PG8_LDA(At, 1, 0); PG8_STAGE(PG8_SA(0, 1), a2, vs[1]);
;             PG8_WAIT_V(8); PG8_WAIT_L(0); PG8_BAR; if (do0) { PG8_MMA(0, 0, At, B0); PG8_MMA(0, 1, At, B1); } PG8_BAR; PG8_SCHED;
	s_setprio 1
	s_waitcnt lgkmcnt(0)
	v_mfma_f32_16x16x32_bf16 v[66:69], v[150:153], v[190:193], v[66:69]
	v_mfma_f32_16x16x32_bf16 v[62:65], v[158:161], v[190:193], v[62:65]
	v_mfma_f32_16x16x32_bf16 v[50:53], v[150:153], v[178:181], v[50:53]
	v_mfma_f32_16x16x32_bf16 v[46:49], v[158:161], v[178:181], v[46:49]
	v_mfma_f32_16x16x32_bf16 v[34:37], v[150:153], v[174:177], v[34:37]
	v_mfma_f32_16x16x32_bf16 v[30:33], v[158:161], v[174:177], v[30:33]
	v_mfma_f32_16x16x32_bf16 v[18:21], v[150:153], v[166:169], v[18:21]
	v_mfma_f32_16x16x32_bf16 v[14:17], v[158:161], v[166:169], v[14:17]
	v_mfma_f32_16x16x32_bf16 v[66:69], v[154:157], v[194:197], v[66:69]
	v_mfma_f32_16x16x32_bf16 v[62:65], v[162:165], v[194:197], v[62:65]
	v_mfma_f32_16x16x32_bf16 v[50:53], v[154:157], v[182:185], v[50:53]
	v_mfma_f32_16x16x32_bf16 v[46:49], v[162:165], v[182:185], v[46:49]
	v_mfma_f32_16x16x32_bf16 v[34:37], v[154:157], v[186:189], v[34:37]
	v_mfma_f32_16x16x32_bf16 v[30:33], v[162:165], v[186:189], v[30:33]
	v_mfma_f32_16x16x32_bf16 v[18:21], v[154:157], v[170:173], v[18:21]
	v_mfma_f32_16x16x32_bf16 v[14:17], v[162:165], v[170:173], v[14:17]
	v_mfma_f32_16x16x32_bf16 v[58:61], v[134:137], v[190:193], v[58:61]
	v_mfma_f32_16x16x32_bf16 v[54:57], v[142:145], v[190:193], v[54:57]
	v_mfma_f32_16x16x32_bf16 v[42:45], v[134:137], v[178:181], v[42:45]
	v_mfma_f32_16x16x32_bf16 v[38:41], v[142:145], v[178:181], v[38:41]
	v_mfma_f32_16x16x32_bf16 v[26:29], v[134:137], v[174:177], v[26:29]
	v_mfma_f32_16x16x32_bf16 v[22:25], v[142:145], v[174:177], v[22:25]
	v_mfma_f32_16x16x32_bf16 v[10:13], v[134:137], v[166:169], v[10:13]
	v_mfma_f32_16x16x32_bf16 v[6:9], v[142:145], v[166:169], v[6:9]
	v_mfma_f32_16x16x32_bf16 v[58:61], v[138:141], v[194:197], v[58:61]
	v_mfma_f32_16x16x32_bf16 v[54:57], v[146:149], v[194:197], v[54:57]
	v_mfma_f32_16x16x32_bf16 v[42:45], v[138:141], v[182:185], v[42:45]
	v_mfma_f32_16x16x32_bf16 v[38:41], v[146:149], v[182:185], v[38:41]
	v_mfma_f32_16x16x32_bf16 v[26:29], v[138:141], v[186:189], v[26:29]
	v_mfma_f32_16x16x32_bf16 v[22:25], v[146:149], v[186:189], v[22:25]
	v_mfma_f32_16x16x32_bf16 v[10:13], v[138:141], v[170:173], v[10:13]
	v_mfma_f32_16x16x32_bf16 v[6:9], v[146:149], v[170:173], v[6:9]
	s_setprio 0
.LBB0_1012:
	v_cndmask_b32_e64 v213, v214, v215, s[6:7]
	v_cndmask_b32_e64 v225, v216, v217, s[6:7]
	s_barrier
	s_add_i32 s6, 0, 0x18000
	v_add_u32_e32 v134, s6, v226
	v_add_u32_e32 v135, s6, v227
	ds_read_b128 v[150:153], v134
	ds_read_b128 v[154:157], v135
	v_add_u32_e32 v134, s58, v226
	s_add_i32 s6, 0, 0x1c000
	v_add_u32_e32 v135, s58, v227
	ds_read_b128 v[158:161], v134
	ds_read_b128 v[162:165], v135
	v_add_u32_e32 v134, s6, v226
	v_add_u32_e32 v138, s6, v227
	v_add_u32_e32 v142, s59, v226
	v_add_u32_e32 v146, s59, v227
	ds_read_b128 v[134:137], v134
	ds_read_b128 v[138:141], v138
	ds_read_b128 v[142:145], v142
	ds_read_b128 v[146:149], v146
	s_mov_b32 m0, s42
	s_waitcnt lgkmcnt(0)
	ds_read_b128 v[190:193], v228 offset:32768
	ds_read_b128 v[178:181], v228 offset:34816
	ds_read_b128 v[194:197], v229 offset:32768
	ds_read_b128 v[182:185], v229 offset:34816
	ds_read_b128 v[174:177], v228 offset:36864
	ds_read_b128 v[166:169], v228 offset:38912
	ds_read_b128 v[186:189], v229 offset:36864
	ds_read_b128 v[170:173], v229 offset:38912
	global_load_lds_dwordx4 v213, s[34:35]
	s_mov_b32 m0, s43
	s_and_b64 vcc, exec, s[8:9]
	global_load_lds_dwordx4 v225, s[34:35]
	s_waitcnt vmcnt(8)
	s_waitcnt lgkmcnt(0)
	s_barrier
	s_cbranch_vccnz .LBB0_1014
	s_setprio 1
	s_waitcnt lgkmcnt(0)
	v_mfma_f32_16x16x32_bf16 v[130:133], v[150:153], v[190:193], v[130:133]
	v_mfma_f32_16x16x32_bf16 v[126:129], v[158:161], v[190:193], v[126:129]
	v_mfma_f32_16x16x32_bf16 v[114:117], v[150:153], v[178:181], v[114:117]
	v_mfma_f32_16x16x32_bf16 v[110:113], v[158:161], v[178:181], v[110:113]
	v_mfma_f32_16x16x32_bf16 v[98:101], v[150:153], v[174:177], v[98:101]
	v_mfma_f32_16x16x32_bf16 v[94:97], v[158:161], v[174:177], v[94:97]
	v_mfma_f32_16x16x32_bf16 v[82:85], v[150:153], v[166:169], v[82:85]
	v_mfma_f32_16x16x32_bf16 v[78:81], v[158:161], v[166:169], v[78:81]
	v_mfma_f32_16x16x32_bf16 v[130:133], v[154:157], v[194:197], v[130:133]
	v_mfma_f32_16x16x32_bf16 v[126:129], v[162:165], v[194:197], v[126:129]
	v_mfma_f32_16x16x32_bf16 v[114:117], v[154:157], v[182:185], v[114:117]
	v_mfma_f32_16x16x32_bf16 v[110:113], v[162:165], v[182:185], v[110:113]
	v_mfma_f32_16x16x32_bf16 v[98:101], v[154:157], v[186:189], v[98:101]
	v_mfma_f32_16x16x32_bf16 v[94:97], v[162:165], v[186:189], v[94:97]
	v_mfma_f32_16x16x32_bf16 v[82:85], v[154:157], v[170:173], v[82:85]
	v_mfma_f32_16x16x32_bf16 v[78:81], v[162:165], v[170:173], v[78:81]
	v_mfma_f32_16x16x32_bf16 v[122:125], v[134:137], v[190:193], v[122:125]
	v_mfma_f32_16x16x32_bf16 v[118:121], v[142:145], v[190:193], v[118:121]
	v_mfma_f32_16x16x32_bf16 v[106:109], v[134:137], v[178:181], v[106:109]
	v_mfma_f32_16x16x32_bf16 v[102:105], v[142:145], v[178:181], v[102:105]
	v_mfma_f32_16x16x32_bf16 v[90:93], v[134:137], v[174:177], v[90:93]
	v_mfma_f32_16x16x32_bf16 v[86:89], v[142:145], v[174:177], v[86:89]
	v_mfma_f32_16x16x32_bf16 v[74:77], v[134:137], v[166:169], v[74:77]
	v_mfma_f32_16x16x32_bf16 v[70:73], v[142:145], v[166:169], v[70:73]
	v_mfma_f32_16x16x32_bf16 v[122:125], v[138:141], v[194:197], v[122:125]
	v_mfma_f32_16x16x32_bf16 v[118:121], v[146:149], v[194:197], v[118:121]
	v_mfma_f32_16x16x32_bf16 v[106:109], v[138:141], v[182:185], v[106:109]
	v_mfma_f32_16x16x32_bf16 v[102:105], v[146:149], v[182:185], v[102:105]
	v_mfma_f32_16x16x32_bf16 v[90:93], v[138:141], v[186:189], v[90:93]
	v_mfma_f32_16x16x32_bf16 v[86:89], v[146:149], v[186:189], v[86:89]
	v_mfma_f32_16x16x32_bf16 v[74:77], v[138:141], v[170:173], v[74:77]
	v_mfma_f32_16x16x32_bf16 v[70:73], v[146:149], v[170:173], v[70:73]
	s_setprio 0
; #define PG8_STAGE(bufoff, gbase, voff) do { _Pragma("unroll") for (int _i = 0; _i < 2; ++_i) \
;         __builtin_amdgcn_global_load_lds((const unsigned*)((const char*)(gbase) + (voff)[_i]), (LAS unsigned*)(lds + (bufoff) + ldsw + _i * 8192), 16, 0, 0); } while (0)
; #define PG8_LDA(dst, b, h) do { _Pragma("unroll") for (int m = 0; m < 4; ++m) _Pragma("unroll") for (int k = 0; k < 2; ++k) dst[m][k] = *(const LAS bf16x8*)(lds + PG8_SA(b, h) + ((aoff ^ (k * 64)) + m * 2048)); } while (0)
; #define PG8_MMA(ai, bj, At, Bt) do { __builtin_amdgcn_s_setprio(1); _Pragma("unroll") for (int m = 0; m < 4; ++m) _Pragma("unroll") for (int n = 0; n < 2; ++n) _Pragma("unroll") for (int k = 0; k < 2; ++k) \
;         acc[ai][bj][m][n] = __builtin_amdgcn_mfma_f32_16x16x32_bf16(Bt[n][k], At[m][k], acc[ai][bj][m][n], 0, 0, 0); __builtin_amdgcn_s_setprio(0); } while (0)
; #define PG8_WAIT_V(n) asm volatile("s_waitcnt vmcnt(" #n ")" ::: "memory")
; #define PG8_WAIT_L(n) asm volatile("s_waitcnt lgkmcnt(" #n ")" ::: "memory")
; #define PG8_BAR __builtin_amdgcn_s_barrier()
; #define PG8_SCHED __builtin_amdgcn_sched_barrier(0)
;     ...
;             PG8_LDA(At, 1, 1); PG8_STAGE(PG8_SB(1, 0), b3, voffB); PG8_STAGE(PG8_SB(1, 1), b3 + hstep, voffB); PG8_STAGE(PG8_SA(1, 0), a3, vs[0]);
;             PG8_WAIT_V(8); PG8_WAIT_L(0); PG8_BAR; if (do1) { PG8_MMA(1, 0, At, B0); PG8_MMA(1, 1, At, B1); } PG8_BAR; PG8_SCHED;
.LBB0_1014:
	v_mov_b32_e32 v225, v3
	s_add_u32 s6, s30, 0x4000
	v_lshl_add_u64 v[232:233], s[34:35], 0, v[2:3]
	v_lshl_add_u64 v[224:225], s[34:35], 0, v[224:225]
	s_addc_u32 s7, s31, 0
	s_barrier
	s_mov_b32 m0, s47
	v_lshl_add_u64 v[234:235], s[6:7], 0, v[202:203]
	s_waitcnt lgkmcnt(0)
	ds_read_b128 v[190:193], v228 offset:49152
	ds_read_b128 v[178:181], v228 offset:51200
	ds_read_b128 v[194:197], v229 offset:49152
	ds_read_b128 v[182:185], v229 offset:51200
	ds_read_b128 v[174:177], v228 offset:53248
	ds_read_b128 v[166:169], v228 offset:55296
	ds_read_b128 v[186:189], v229 offset:53248
	ds_read_b128 v[170:173], v229 offset:55296
	global_load_lds_dwordx4 v[234:235], off
	v_lshl_add_u64 v[234:235], s[6:7], 0, v[204:205]
	s_add_u32 s6, s30, 0x44000
	s_mov_b32 m0, s48
	s_addc_u32 s7, s31, 0
	global_load_lds_dwordx4 v[234:235], off
	v_lshl_add_u64 v[234:235], s[6:7], 0, v[202:203]
	s_mov_b32 m0, s51
	v_lshl_add_u64 v[232:233], v[232:233], 0, s[16:17]
	global_load_lds_dwordx4 v[234:235], off
	v_lshl_add_u64 v[234:235], s[6:7], 0, v[204:205]
	s_mov_b32 m0, s52
	v_lshl_add_u64 v[224:225], v[224:225], 0, s[16:17]
	global_load_lds_dwordx4 v[234:235], off
	s_mov_b32 m0, s49
	s_and_b64 vcc, exec, s[10:11]
	global_load_lds_dwordx4 v[232:233], off
	s_mov_b32 m0, s50
	s_nop 0
	global_load_lds_dwordx4 v[224:225], off
	s_waitcnt vmcnt(8)
	s_waitcnt lgkmcnt(0)
	s_barrier
	s_cbranch_vccnz .LBB0_1005
	s_setprio 1
	s_waitcnt lgkmcnt(0)
	v_mfma_f32_16x16x32_bf16 v[66:69], v[150:153], v[190:193], v[66:69]
	v_mfma_f32_16x16x32_bf16 v[62:65], v[158:161], v[190:193], v[62:65]
	v_mfma_f32_16x16x32_bf16 v[50:53], v[150:153], v[178:181], v[50:53]
	v_mfma_f32_16x16x32_bf16 v[46:49], v[158:161], v[178:181], v[46:49]
	v_mfma_f32_16x16x32_bf16 v[34:37], v[150:153], v[174:177], v[34:37]
	v_mfma_f32_16x16x32_bf16 v[30:33], v[158:161], v[174:177], v[30:33]
	v_mfma_f32_16x16x32_bf16 v[18:21], v[150:153], v[166:169], v[18:21]
	v_mfma_f32_16x16x32_bf16 v[14:17], v[158:161], v[166:169], v[14:17]
	v_mfma_f32_16x16x32_bf16 v[66:69], v[154:157], v[194:197], v[66:69]
	v_mfma_f32_16x16x32_bf16 v[62:65], v[162:165], v[194:197], v[62:65]
	v_mfma_f32_16x16x32_bf16 v[50:53], v[154:157], v[182:185], v[50:53]
	v_mfma_f32_16x16x32_bf16 v[46:49], v[162:165], v[182:185], v[46:49]
	v_mfma_f32_16x16x32_bf16 v[34:37], v[154:157], v[186:189], v[34:37]
	v_mfma_f32_16x16x32_bf16 v[30:33], v[162:165], v[186:189], v[30:33]
	v_mfma_f32_16x16x32_bf16 v[18:21], v[154:157], v[170:173], v[18:21]
	v_mfma_f32_16x16x32_bf16 v[14:17], v[162:165], v[170:173], v[14:17]
	v_mfma_f32_16x16x32_bf16 v[58:61], v[134:137], v[190:193], v[58:61]
	v_mfma_f32_16x16x32_bf16 v[54:57], v[142:145], v[190:193], v[54:57]
	v_mfma_f32_16x16x32_bf16 v[42:45], v[134:137], v[178:181], v[42:45]
	v_mfma_f32_16x16x32_bf16 v[38:41], v[142:145], v[178:181], v[38:41]
	v_mfma_f32_16x16x32_bf16 v[26:29], v[134:137], v[174:177], v[26:29]
	v_mfma_f32_16x16x32_bf16 v[22:25], v[142:145], v[174:177], v[22:25]
	v_mfma_f32_16x16x32_bf16 v[10:13], v[134:137], v[166:169], v[10:13]
	v_mfma_f32_16x16x32_bf16 v[6:9], v[142:145], v[166:169], v[6:9]
	v_mfma_f32_16x16x32_bf16 v[58:61], v[138:141], v[194:197], v[58:61]
	v_mfma_f32_16x16x32_bf16 v[54:57], v[146:149], v[194:197], v[54:57]
	v_mfma_f32_16x16x32_bf16 v[42:45], v[138:141], v[182:185], v[42:45]
	v_mfma_f32_16x16x32_bf16 v[38:41], v[146:149], v[182:185], v[38:41]
	v_mfma_f32_16x16x32_bf16 v[26:29], v[138:141], v[186:189], v[26:29]
	v_mfma_f32_16x16x32_bf16 v[22:25], v[146:149], v[186:189], v[22:25]
	v_mfma_f32_16x16x32_bf16 v[10:13], v[138:141], v[170:173], v[10:13]
	v_mfma_f32_16x16x32_bf16 v[6:9], v[146:149], v[170:173], v[6:9]
	s_setprio 0
	s_branch .LBB0_1005

; #define PG8_STAGE(bufoff, gbase, voff) do { _Pragma("unroll") for (int _i = 0; _i < 2; ++_i) \
;         __builtin_amdgcn_global_load_lds((const unsigned*)((const char*)(gbase) + (voff)[_i]), (LAS unsigned*)(lds + (bufoff) + ldsw + _i * 8192), 16, 0, 0); } while (0)
; #define PG8_LDA(dst, b, h) do { _Pragma("unroll") for (int m = 0; m < 4; ++m) _Pragma("unroll") for (int k = 0; k < 2; ++k) dst[m][k] = *(const LAS bf16x8*)(lds + PG8_SA(b, h) + ((aoff ^ (k * 64)) + m * 2048)); } while (0)
; #define PG8_LDB(dst, b, h) do { _Pragma("unroll") for (int n = 0; n < 2; ++n) _Pragma("unroll") for (int k = 0; k < 2; ++k) dst[n][k] = *(const LAS bf16x8*)(lds + PG8_SB(b, h) + ((boff ^ (k * 64)) + n * 2048)); } while (0)
; #define PG8_BAR __builtin_amdgcn_s_barrier()
;     ...
;             const bool last = (t == nt - 2);
;             const char* a1 = cA + (size_t)(t + 1) * kstepA;
;             const char* a2 = last ? nA : cA + (size_t)(t + 2) * kstepA; const char* b2 = last ? nB : cB + (size_t)(t + 2) * kstepB;
;             const char* a3 = a2 + kstepA; const char* b3 = b2 + kstepB;
;             unsigned vs[2][2];
;             if constexpr (GATHER) {
;                 if (last && has_next) {
; #pragma unroll
;                     for (int hh = 0; hh < 2; ++hh)
; #pragma unroll
;                         for (int i = 0; i < 2; ++i) voffN[hh][i] = (unsigned)idxl[(ui + 1) * 256 + hh * HALF + sR[i]] * (unsigned)(K * 2) + (unsigned)sC[i] * 2u;
;                 }
; #pragma unroll
;                 for (int hh = 0; hh < 2; ++hh)
; #pragma unroll
;                     for (int i = 0; i < 2; ++i) vs[hh][i] = last ? voffN[hh][i] : voffA[hh][i];
;             } else {
; #pragma unroll
;                 for (int hh = 0; hh < 2; ++hh)
; #pragma unroll
;                     for (int i = 0; i < 2; ++i) vs[hh][i] = voffA[hh][i];
;             }
;             PG8_LDB(B0, 0, 0); PG8_LDB(B1, 0, 1); PG8_SCHED; PG8_LDA(At, 0, 0); PG8_STAGE(PG8_SA(1, 1), a1, voffA[1]);
;             PG8_WAIT_V(8); PG8_WAIT_L(0); PG8_BAR; if (do0) { PG8_MMA(0, 0, At, B0); PG8_MMA(0, 1, At, B1); } PG8_BAR; PG8_SCHED;
;             PG8_LDA(At, 0, 1); PG8_STAGE(PG8_SB(0, 0), b2, voffB); PG8_STAGE(PG8_SB(0, 1), b2 + hstep, voffB); PG8_STAGE(PG8_SA(0, 0), a2, vs[0]);
;             PG8_WAIT_V(8); PG8_WAIT_L(0); PG8_BAR; if (do1) { PG8_MMA(1, 0, At, B0); PG8_MMA(1, 1, At, B1); } PG8_BAR; PG8_SCHED;
.LBB0_1100:
	ds_read_b128 v[150:153], v218
	ds_read_b128 v[154:157], v219
	ds_read_b128 v[158:161], v220
	ds_read_b128 v[162:165], v221
	ds_read_b128 v[134:137], v222
	ds_read_b128 v[138:141], v223
	ds_read_b128 v[142:145], v224
	ds_read_b128 v[146:149], v225
	v_lshl_add_u64 v[4:5], s[22:23], 0, v[212:213]
	s_add_i32 m0, s28, 0xc000
	s_waitcnt lgkmcnt(0)
	ds_read_b128 v[190:193], v226
	ds_read_b128 v[178:181], v226 offset:2048
	ds_read_b128 v[194:197], v227
	ds_read_b128 v[182:185], v227 offset:2048
	ds_read_b128 v[174:177], v226 offset:4096
	ds_read_b128 v[166:169], v226 offset:6144
	ds_read_b128 v[186:189], v227 offset:4096
	ds_read_b128 v[170:173], v227 offset:6144
	global_load_lds_dwordx4 v[4:5], off
	v_lshl_add_u64 v[4:5], s[22:23], 0, v[214:215]
	s_add_i32 m0, s28, 0xe000
	v_cmp_ne_u32_e64 s[6:7], 1, v228
	global_load_lds_dwordx4 v[4:5], off
	s_waitcnt vmcnt(8)
	s_waitcnt lgkmcnt(0)
	s_andn2_b64 vcc, exec, s[20:21]
	s_barrier
	s_cbranch_vccnz .LBB0_1102
	s_setprio 1
	s_waitcnt lgkmcnt(0)
	v_mfma_f32_16x16x32_bf16 v[66:69], v[150:153], v[190:193], v[66:69]
	v_mfma_f32_16x16x32_bf16 v[62:65], v[158:161], v[190:193], v[62:65]
	v_mfma_f32_16x16x32_bf16 v[50:53], v[150:153], v[178:181], v[50:53]
	v_mfma_f32_16x16x32_bf16 v[46:49], v[158:161], v[178:181], v[46:49]
	v_mfma_f32_16x16x32_bf16 v[34:37], v[150:153], v[174:177], v[34:37]
	v_mfma_f32_16x16x32_bf16 v[30:33], v[158:161], v[174:177], v[30:33]
	v_mfma_f32_16x16x32_bf16 v[18:21], v[150:153], v[166:169], v[18:21]
	v_mfma_f32_16x16x32_bf16 v[14:17], v[158:161], v[166:169], v[14:17]
	v_mfma_f32_16x16x32_bf16 v[66:69], v[154:157], v[194:197], v[66:69]
	v_mfma_f32_16x16x32_bf16 v[62:65], v[162:165], v[194:197], v[62:65]
	v_mfma_f32_16x16x32_bf16 v[50:53], v[154:157], v[182:185], v[50:53]
	v_mfma_f32_16x16x32_bf16 v[46:49], v[162:165], v[182:185], v[46:49]
	v_mfma_f32_16x16x32_bf16 v[34:37], v[154:157], v[186:189], v[34:37]
	v_mfma_f32_16x16x32_bf16 v[30:33], v[162:165], v[186:189], v[30:33]
	v_mfma_f32_16x16x32_bf16 v[18:21], v[154:157], v[170:173], v[18:21]
	v_mfma_f32_16x16x32_bf16 v[14:17], v[162:165], v[170:173], v[14:17]
	v_mfma_f32_16x16x32_bf16 v[58:61], v[134:137], v[190:193], v[58:61]
	v_mfma_f32_16x16x32_bf16 v[54:57], v[142:145], v[190:193], v[54:57]
	v_mfma_f32_16x16x32_bf16 v[42:45], v[134:137], v[178:181], v[42:45]
	v_mfma_f32_16x16x32_bf16 v[38:41], v[142:145], v[178:181], v[38:41]
	v_mfma_f32_16x16x32_bf16 v[26:29], v[134:137], v[174:177], v[26:29]
	v_mfma_f32_16x16x32_bf16 v[22:25], v[142:145], v[174:177], v[22:25]
	v_mfma_f32_16x16x32_bf16 v[10:13], v[134:137], v[166:169], v[10:13]
	v_mfma_f32_16x16x32_bf16 v[4:7], v[142:145], v[166:169], v[6:9]
	v_mfma_f32_16x16x32_bf16 v[58:61], v[138:141], v[194:197], v[58:61]
	v_mfma_f32_16x16x32_bf16 v[54:57], v[146:149], v[194:197], v[54:57]
	v_mfma_f32_16x16x32_bf16 v[42:45], v[138:141], v[182:185], v[42:45]
	v_mfma_f32_16x16x32_bf16 v[38:41], v[146:149], v[182:185], v[38:41]
	v_mfma_f32_16x16x32_bf16 v[26:29], v[138:141], v[186:189], v[26:29]
	v_mfma_f32_16x16x32_bf16 v[22:25], v[146:149], v[186:189], v[22:25]
	v_mfma_f32_16x16x32_bf16 v[10:13], v[138:141], v[170:173], v[10:13]
	v_mfma_f32_16x16x32_bf16 v[6:9], v[146:149], v[170:173], v[4:7]
	s_setprio 0
.LBB0_1102:
	s_add_u32 s8, s22, 0x4000
	s_addc_u32 s9, s23, 0
	s_cmp_eq_u32 s61, s59
	s_cselect_b32 s27, s15, s9
	s_cselect_b32 s26, s14, s8
	s_cselect_b32 s25, s17, s63
	s_cselect_b32 s24, s16, s62
	s_barrier
	s_mov_b32 m0, s29
	v_lshl_add_u64 v[4:5], s[24:25], 0, v[208:209]
	s_add_u32 s8, s24, 0xb0000
	s_waitcnt lgkmcnt(0)
	ds_read_b128 v[190:193], v226 offset:16384
	ds_read_b128 v[178:181], v226 offset:18432
	ds_read_b128 v[194:197], v227 offset:16384
	ds_read_b128 v[182:185], v227 offset:18432
	ds_read_b128 v[174:177], v226 offset:20480
	ds_read_b128 v[166:169], v226 offset:22528
	ds_read_b128 v[186:189], v227 offset:20480
	ds_read_b128 v[170:173], v227 offset:22528
	global_load_lds_dwordx4 v[4:5], off
	v_lshl_add_u64 v[4:5], s[24:25], 0, v[210:211]
	s_mov_b32 m0, s30
	s_addc_u32 s9, s25, 0
	global_load_lds_dwordx4 v[4:5], off
	v_lshl_add_u64 v[4:5], s[8:9], 0, v[208:209]
	s_mov_b32 m0, s31
	v_cndmask_b32_e64 v3, 0, 1, s[18:19]
	global_load_lds_dwordx4 v[4:5], off
	v_lshl_add_u64 v[4:5], s[8:9], 0, v[210:211]
	s_mov_b32 m0, s34
	v_cmp_ne_u32_e64 s[8:9], 1, v3
	global_load_lds_dwordx4 v[4:5], off
	v_lshl_add_u64 v[4:5], s[26:27], 0, v[200:201]
	s_mov_b32 m0, s28
	s_andn2_b64 vcc, exec, s[18:19]
	global_load_lds_dwordx4 v[4:5], off
	v_lshl_add_u64 v[4:5], s[26:27], 0, v[202:203]
	s_mov_b32 m0, s35
	s_nop 0
	global_load_lds_dwordx4 v[4:5], off
	s_waitcnt vmcnt(8)
	s_waitcnt lgkmcnt(0)
	s_barrier
	s_cbranch_vccnz .LBB0_1104
	s_setprio 1
	s_waitcnt lgkmcnt(0)
	v_mfma_f32_16x16x32_bf16 v[130:133], v[150:153], v[190:193], v[130:133]
	v_mfma_f32_16x16x32_bf16 v[126:129], v[158:161], v[190:193], v[126:129]
	v_mfma_f32_16x16x32_bf16 v[114:117], v[150:153], v[178:181], v[114:117]
	v_mfma_f32_16x16x32_bf16 v[110:113], v[158:161], v[178:181], v[110:113]
	v_mfma_f32_16x16x32_bf16 v[98:101], v[150:153], v[174:177], v[98:101]
	v_mfma_f32_16x16x32_bf16 v[94:97], v[158:161], v[174:177], v[94:97]
	v_mfma_f32_16x16x32_bf16 v[82:85], v[150:153], v[166:169], v[82:85]
	v_mfma_f32_16x16x32_bf16 v[78:81], v[158:161], v[166:169], v[78:81]
	v_mfma_f32_16x16x32_bf16 v[130:133], v[154:157], v[194:197], v[130:133]
	v_mfma_f32_16x16x32_bf16 v[126:129], v[162:165], v[194:197], v[126:129]
	v_mfma_f32_16x16x32_bf16 v[114:117], v[154:157], v[182:185], v[114:117]
	v_mfma_f32_16x16x32_bf16 v[110:113], v[162:165], v[182:185], v[110:113]
	v_mfma_f32_16x16x32_bf16 v[98:101], v[154:157], v[186:189], v[98:101]
	v_mfma_f32_16x16x32_bf16 v[94:97], v[162:165], v[186:189], v[94:97]
	v_mfma_f32_16x16x32_bf16 v[82:85], v[154:157], v[170:173], v[82:85]
	v_mfma_f32_16x16x32_bf16 v[78:81], v[162:165], v[170:173], v[78:81]
	v_mfma_f32_16x16x32_bf16 v[122:125], v[134:137], v[190:193], v[122:125]
	v_mfma_f32_16x16x32_bf16 v[118:121], v[142:145], v[190:193], v[118:121]
	v_mfma_f32_16x16x32_bf16 v[106:109], v[134:137], v[178:181], v[106:109]
	v_mfma_f32_16x16x32_bf16 v[102:105], v[142:145], v[178:181], v[102:105]
	v_mfma_f32_16x16x32_bf16 v[90:93], v[134:137], v[174:177], v[90:93]
	v_mfma_f32_16x16x32_bf16 v[86:89], v[142:145], v[174:177], v[86:89]
	v_mfma_f32_16x16x32_bf16 v[74:77], v[134:137], v[166:169], v[74:77]
	v_mfma_f32_16x16x32_bf16 v[70:73], v[142:145], v[166:169], v[70:73]
	v_mfma_f32_16x16x32_bf16 v[122:125], v[138:141], v[194:197], v[122:125]
	v_mfma_f32_16x16x32_bf16 v[118:121], v[146:149], v[194:197], v[118:121]
	v_mfma_f32_16x16x32_bf16 v[106:109], v[138:141], v[182:185], v[106:109]
	v_mfma_f32_16x16x32_bf16 v[102:105], v[146:149], v[182:185], v[102:105]
	v_mfma_f32_16x16x32_bf16 v[90:93], v[138:141], v[186:189], v[90:93]
	v_mfma_f32_16x16x32_bf16 v[86:89], v[146:149], v[186:189], v[86:89]
	v_mfma_f32_16x16x32_bf16 v[74:77], v[138:141], v[170:173], v[74:77]
	v_mfma_f32_16x16x32_bf16 v[70:73], v[146:149], v[170:173], v[70:73]
	s_setprio 0
; #define PG8_STAGE(bufoff, gbase, voff) do { _Pragma("unroll") for (int _i = 0; _i < 2; ++_i) \
;         __builtin_amdgcn_global_load_lds((const unsigned*)((const char*)(gbase) + (voff)[_i]), (LAS unsigned*)(lds + (bufoff) + ldsw + _i * 8192), 16, 0, 0); } while (0)
; #define PG8_LDA(dst, b, h) do { _Pragma("unroll") for (int m = 0; m < 4; ++m) _Pragma("unroll") for (int k = 0; k < 2; ++k) dst[m][k] = *(const LAS bf16x8*)(lds + PG8_SA(b, h) + ((aoff ^ (k * 64)) + m * 2048)); } while (0)
; #define PG8_LDB(dst, b, h) do { _Pragma("unroll") for (int n = 0; n < 2; ++n) _Pragma("unroll") for (int k = 0; k < 2; ++k) dst[n][k] = *(const LAS bf16x8*)(lds + PG8_SB(b, h) + ((boff ^ (k * 64)) + n * 2048)); } while (0)
; #define PG8_MMA(ai, bj, At, Bt) do { __builtin_amdgcn_s_setprio(1); _Pragma("unroll") for (int m = 0; m < 4; ++m) _Pragma("unroll") for (int n = 0; n < 2; ++n) _Pragma("unroll") for (int k = 0; k < 2; ++k) \
;         acc[ai][bj][m][n] = __builtin_amdgcn_mfma_f32_16x16x32_bf16(Bt[n][k], At[m][k], acc[ai][bj][m][n], 0, 0, 0); __builtin_amdgcn_s_setprio(0); } while (0)
; #define PG8_WAIT_V(n) asm volatile("s_waitcnt vmcnt(" #n ")" ::: "memory")
; #define PG8_WAIT_L(n) asm volatile("s_waitcnt lgkmcnt(" #n ")" ::: "memory")
; #define PG8_BAR __builtin_amdgcn_s_barrier()
; #define PG8_SCHED __builtin_amdgcn_sched_barrier(0)
;     ...
;             PG8_WAIT_V(8); PG8_WAIT_L(0); PG8_BAR; if (do1) { PG8_MMA(1, 0, At, B0); PG8_MMA(1, 1, At, B1); } PG8_BAR; PG8_SCHED;
;             PG8_LDB(B0, 1, 0); PG8_LDB(B1, 1, 1); PG8_SCHED; PG8_LDA(At, 1, 0); PG8_STAGE(PG8_SA(0, 1), a2, vs[1]);
;             PG8_WAIT_V(8); PG8_WAIT_L(0); PG8_BAR; if (do0) { PG8_MMA(0, 0, At, B0); PG8_MMA(0, 1, At, B1); } PG8_BAR; PG8_SCHED;
.LBB0_1104:
	s_barrier
	s_add_i32 s64, 0, 0x18000
	v_add_u32_e32 v3, s64, v199
	v_add_u32_e32 v4, s64, v216
	ds_read_b128 v[150:153], v3
	ds_read_b128 v[154:157], v4
	v_add_u32_e32 v3, s48, v199
	s_add_i32 s64, 0, 0x1c000
	v_add_u32_e32 v4, s48, v216
	ds_read_b128 v[158:161], v3
	ds_read_b128 v[162:165], v4
	v_add_u32_e32 v3, s64, v199
	v_add_u32_e32 v4, s64, v216
	ds_read_b128 v[134:137], v3
	ds_read_b128 v[138:141], v4
	v_add_u32_e32 v3, s49, v199
	v_add_u32_e32 v4, s49, v216
	ds_read_b128 v[142:145], v3
	ds_read_b128 v[146:149], v4
	s_mov_b32 m0, s36
	v_lshl_add_u64 v[4:5], s[26:27], 0, v[204:205]
	s_waitcnt lgkmcnt(0)
	ds_read_b128 v[190:193], v226 offset:32768
	ds_read_b128 v[178:181], v226 offset:34816
	ds_read_b128 v[194:197], v227 offset:32768
	ds_read_b128 v[182:185], v227 offset:34816
	ds_read_b128 v[174:177], v226 offset:36864
	ds_read_b128 v[166:169], v226 offset:38912
	ds_read_b128 v[186:189], v227 offset:36864
	ds_read_b128 v[170:173], v227 offset:38912
	global_load_lds_dwordx4 v[4:5], off
	v_lshl_add_u64 v[4:5], s[26:27], 0, v[206:207]
	s_mov_b32 m0, s37
	s_and_b64 vcc, exec, s[6:7]
	global_load_lds_dwordx4 v[4:5], off
	s_waitcnt vmcnt(8)
	s_waitcnt lgkmcnt(0)
	s_barrier
	s_cbranch_vccnz .LBB0_1106
	s_setprio 1
	s_waitcnt lgkmcnt(0)
	v_mfma_f32_16x16x32_bf16 v[66:69], v[150:153], v[190:193], v[66:69]
	v_mfma_f32_16x16x32_bf16 v[62:65], v[158:161], v[190:193], v[62:65]
	v_mfma_f32_16x16x32_bf16 v[50:53], v[150:153], v[178:181], v[50:53]
	v_mfma_f32_16x16x32_bf16 v[46:49], v[158:161], v[178:181], v[46:49]
	v_mfma_f32_16x16x32_bf16 v[34:37], v[150:153], v[174:177], v[34:37]
	v_mfma_f32_16x16x32_bf16 v[30:33], v[158:161], v[174:177], v[30:33]
	v_mfma_f32_16x16x32_bf16 v[18:21], v[150:153], v[166:169], v[18:21]
	v_mfma_f32_16x16x32_bf16 v[14:17], v[158:161], v[166:169], v[14:17]
	v_mfma_f32_16x16x32_bf16 v[66:69], v[154:157], v[194:197], v[66:69]
	v_mfma_f32_16x16x32_bf16 v[62:65], v[162:165], v[194:197], v[62:65]
	v_mfma_f32_16x16x32_bf16 v[50:53], v[154:157], v[182:185], v[50:53]
	v_mfma_f32_16x16x32_bf16 v[46:49], v[162:165], v[182:185], v[46:49]
	v_mfma_f32_16x16x32_bf16 v[34:37], v[154:157], v[186:189], v[34:37]
	v_mfma_f32_16x16x32_bf16 v[30:33], v[162:165], v[186:189], v[30:33]
	v_mfma_f32_16x16x32_bf16 v[18:21], v[154:157], v[170:173], v[18:21]
	v_mfma_f32_16x16x32_bf16 v[14:17], v[162:165], v[170:173], v[14:17]
	v_mfma_f32_16x16x32_bf16 v[58:61], v[134:137], v[190:193], v[58:61]
	v_mfma_f32_16x16x32_bf16 v[54:57], v[142:145], v[190:193], v[54:57]
	v_mfma_f32_16x16x32_bf16 v[42:45], v[134:137], v[178:181], v[42:45]
	v_mfma_f32_16x16x32_bf16 v[38:41], v[142:145], v[178:181], v[38:41]
	v_mfma_f32_16x16x32_bf16 v[26:29], v[134:137], v[174:177], v[26:29]
	v_mfma_f32_16x16x32_bf16 v[22:25], v[142:145], v[174:177], v[22:25]
	v_mfma_f32_16x16x32_bf16 v[10:13], v[134:137], v[166:169], v[10:13]
	v_mfma_f32_16x16x32_bf16 v[4:7], v[142:145], v[166:169], v[6:9]
	v_mfma_f32_16x16x32_bf16 v[58:61], v[138:141], v[194:197], v[58:61]
	v_mfma_f32_16x16x32_bf16 v[54:57], v[146:149], v[194:197], v[54:57]
	v_mfma_f32_16x16x32_bf16 v[42:45], v[138:141], v[182:185], v[42:45]
	v_mfma_f32_16x16x32_bf16 v[38:41], v[146:149], v[182:185], v[38:41]
	v_mfma_f32_16x16x32_bf16 v[26:29], v[138:141], v[186:189], v[26:29]
	v_mfma_f32_16x16x32_bf16 v[22:25], v[146:149], v[186:189], v[22:25]
	v_mfma_f32_16x16x32_bf16 v[10:13], v[138:141], v[170:173], v[10:13]
	v_mfma_f32_16x16x32_bf16 v[6:9], v[146:149], v[170:173], v[4:7]
	s_setprio 0
; #define PG8_STAGE(bufoff, gbase, voff) do { _Pragma("unroll") for (int _i = 0; _i < 2; ++_i) \
;         __builtin_amdgcn_global_load_lds((const unsigned*)((const char*)(gbase) + (voff)[_i]), (LAS unsigned*)(lds + (bufoff) + ldsw + _i * 8192), 16, 0, 0); } while (0)
; #define PG8_LDA(dst, b, h) do { _Pragma("unroll") for (int m = 0; m < 4; ++m) _Pragma("unroll") for (int k = 0; k < 2; ++k) dst[m][k] = *(const LAS bf16x8*)(lds + PG8_SA(b, h) + ((aoff ^ (k * 64)) + m * 2048)); } while (0)
; #define PG8_MMA(ai, bj, At, Bt) do { __builtin_amdgcn_s_setprio(1); _Pragma("unroll") for (int m = 0; m < 4; ++m) _Pragma("unroll") for (int n = 0; n < 2; ++n) _Pragma("unroll") for (int k = 0; k < 2; ++k) \
;         acc[ai][bj][m][n] = __builtin_amdgcn_mfma_f32_16x16x32_bf16(Bt[n][k], At[m][k], acc[ai][bj][m][n], 0, 0, 0); __builtin_amdgcn_s_setprio(0); } while (0)
; #define PG8_WAIT_V(n) asm volatile("s_waitcnt vmcnt(" #n ")" ::: "memory")
; #define PG8_WAIT_L(n) asm volatile("s_waitcnt lgkmcnt(" #n ")" ::: "memory")
; #define PG8_BAR __builtin_amdgcn_s_barrier()
; #define PG8_SCHED __builtin_amdgcn_sched_barrier(0)
;     ...
;             PG8_WAIT_V(8); PG8_WAIT_L(0); PG8_BAR; if (do0) { PG8_MMA(0, 0, At, B0); PG8_MMA(0, 1, At, B1); } PG8_BAR; PG8_SCHED;
;             PG8_LDA(At, 1, 1); PG8_STAGE(PG8_SB(1, 0), b3, voffB); PG8_STAGE(PG8_SB(1, 1), b3 + hstep, voffB); PG8_STAGE(PG8_SA(1, 0), a3, vs[0]);
;             PG8_WAIT_V(8); PG8_WAIT_L(0); PG8_BAR; if (do1) { PG8_MMA(1, 0, At, B0); PG8_MMA(1, 1, At, B1); } PG8_BAR; PG8_SCHED;
.LBB0_1106:
	s_add_u32 s6, s26, 0x4000
	s_addc_u32 s7, s27, 0
	s_add_u32 s26, s24, 0x4000
	s_addc_u32 s27, s25, 0
	s_barrier
	s_mov_b32 m0, s39
	v_lshl_add_u64 v[4:5], s[26:27], 0, v[208:209]
	s_add_u32 s24, s24, 0xb4000
	s_waitcnt lgkmcnt(0)
	ds_read_b128 v[190:193], v226 offset:49152
	ds_read_b128 v[178:181], v226 offset:51200
	ds_read_b128 v[194:197], v227 offset:49152
	ds_read_b128 v[182:185], v227 offset:51200
	ds_read_b128 v[174:177], v226 offset:53248
	ds_read_b128 v[166:169], v226 offset:55296
	ds_read_b128 v[186:189], v227 offset:53248
	ds_read_b128 v[170:173], v227 offset:55296
	global_load_lds_dwordx4 v[4:5], off
	v_lshl_add_u64 v[4:5], s[26:27], 0, v[210:211]
	s_mov_b32 m0, s40
	s_addc_u32 s25, s25, 0
	global_load_lds_dwordx4 v[4:5], off
	v_lshl_add_u64 v[4:5], s[24:25], 0, v[208:209]
	s_mov_b32 m0, s43
	s_and_b64 vcc, exec, s[8:9]
	global_load_lds_dwordx4 v[4:5], off
	v_lshl_add_u64 v[4:5], s[24:25], 0, v[210:211]
	s_mov_b32 m0, s44
	s_nop 0
	global_load_lds_dwordx4 v[4:5], off
	v_lshl_add_u64 v[4:5], s[6:7], 0, v[200:201]
	s_mov_b32 m0, s41
	s_nop 0
	global_load_lds_dwordx4 v[4:5], off
	v_lshl_add_u64 v[4:5], s[6:7], 0, v[202:203]
	s_mov_b32 m0, s42
	s_nop 0
	global_load_lds_dwordx4 v[4:5], off
	s_waitcnt vmcnt(8)
	s_waitcnt lgkmcnt(0)
	s_barrier
	s_cbranch_vccnz .LBB0_1099
	s_setprio 1
	s_waitcnt lgkmcnt(0)
	v_mfma_f32_16x16x32_bf16 v[130:133], v[150:153], v[190:193], v[130:133]
	v_mfma_f32_16x16x32_bf16 v[126:129], v[158:161], v[190:193], v[126:129]
	v_mfma_f32_16x16x32_bf16 v[114:117], v[150:153], v[178:181], v[114:117]
	v_mfma_f32_16x16x32_bf16 v[110:113], v[158:161], v[178:181], v[110:113]
	v_mfma_f32_16x16x32_bf16 v[98:101], v[150:153], v[174:177], v[98:101]
	v_mfma_f32_16x16x32_bf16 v[94:97], v[158:161], v[174:177], v[94:97]
	v_mfma_f32_16x16x32_bf16 v[82:85], v[150:153], v[166:169], v[82:85]
	v_mfma_f32_16x16x32_bf16 v[78:81], v[158:161], v[166:169], v[78:81]
	v_mfma_f32_16x16x32_bf16 v[130:133], v[154:157], v[194:197], v[130:133]
	v_mfma_f32_16x16x32_bf16 v[126:129], v[162:165], v[194:197], v[126:129]
	v_mfma_f32_16x16x32_bf16 v[114:117], v[154:157], v[182:185], v[114:117]
	v_mfma_f32_16x16x32_bf16 v[110:113], v[162:165], v[182:185], v[110:113]
	v_mfma_f32_16x16x32_bf16 v[98:101], v[154:157], v[186:189], v[98:101]
	v_mfma_f32_16x16x32_bf16 v[94:97], v[162:165], v[186:189], v[94:97]
	v_mfma_f32_16x16x32_bf16 v[82:85], v[154:157], v[170:173], v[82:85]
	v_mfma_f32_16x16x32_bf16 v[78:81], v[162:165], v[170:173], v[78:81]
	v_mfma_f32_16x16x32_bf16 v[122:125], v[134:137], v[190:193], v[122:125]
	v_mfma_f32_16x16x32_bf16 v[118:121], v[142:145], v[190:193], v[118:121]
	v_mfma_f32_16x16x32_bf16 v[106:109], v[134:137], v[178:181], v[106:109]
	v_mfma_f32_16x16x32_bf16 v[102:105], v[142:145], v[178:181], v[102:105]
	v_mfma_f32_16x16x32_bf16 v[90:93], v[134:137], v[174:177], v[90:93]
	v_mfma_f32_16x16x32_bf16 v[86:89], v[142:145], v[174:177], v[86:89]
	v_mfma_f32_16x16x32_bf16 v[74:77], v[134:137], v[166:169], v[74:77]
	v_mfma_f32_16x16x32_bf16 v[70:73], v[142:145], v[166:169], v[70:73]
	v_mfma_f32_16x16x32_bf16 v[122:125], v[138:141], v[194:197], v[122:125]
	v_mfma_f32_16x16x32_bf16 v[118:121], v[146:149], v[194:197], v[118:121]
	v_mfma_f32_16x16x32_bf16 v[106:109], v[138:141], v[182:185], v[106:109]
	v_mfma_f32_16x16x32_bf16 v[102:105], v[146:149], v[182:185], v[102:105]
	v_mfma_f32_16x16x32_bf16 v[90:93], v[138:141], v[186:189], v[90:93]
	v_mfma_f32_16x16x32_bf16 v[86:89], v[146:149], v[186:189], v[86:89]
	v_mfma_f32_16x16x32_bf16 v[74:77], v[138:141], v[170:173], v[74:77]
	v_mfma_f32_16x16x32_bf16 v[70:73], v[146:149], v[170:173], v[70:73]
	s_setprio 0
	s_branch .LBB0_1099

; #define PG8_STAGE(bufoff, gbase, voff) do { _Pragma("unroll") for (int _i = 0; _i < 2; ++_i) \
;         __builtin_amdgcn_global_load_lds((const unsigned*)((const char*)(gbase) + (voff)[_i]), (LAS unsigned*)(lds + (bufoff) + ldsw + _i * 8192), 16, 0, 0); } while (0)
; #define PG8_LDA(dst, b, h) do { _Pragma("unroll") for (int m = 0; m < 4; ++m) _Pragma("unroll") for (int k = 0; k < 2; ++k) dst[m][k] = *(const LAS bf16x8*)(lds + PG8_SA(b, h) + ((aoff ^ (k * 64)) + m * 2048)); } while (0)
; #define PG8_LDB(dst, b, h) do { _Pragma("unroll") for (int n = 0; n < 2; ++n) _Pragma("unroll") for (int k = 0; k < 2; ++k) dst[n][k] = *(const LAS bf16x8*)(lds + PG8_SB(b, h) + ((boff ^ (k * 64)) + n * 2048)); } while (0)
; #define PG8_BAR __builtin_amdgcn_s_barrier()
;     ...
;             const bool last = (t == nt - 2);
;             const char* a1 = cA + (size_t)(t + 1) * kstepA;
;             const char* a2 = last ? nA : cA + (size_t)(t + 2) * kstepA; const char* b2 = last ? nB : cB + (size_t)(t + 2) * kstepB;
;             const char* a3 = a2 + kstepA; const char* b3 = b2 + kstepB;
;             unsigned vs[2][2];
;             if constexpr (GATHER) {
;                 if (last && has_next) {
; #pragma unroll
;                     for (int hh = 0; hh < 2; ++hh)
; #pragma unroll
;                         for (int i = 0; i < 2; ++i) voffN[hh][i] = (unsigned)idxl[(ui + 1) * 256 + hh * HALF + sR[i]] * (unsigned)(K * 2) + (unsigned)sC[i] * 2u;
;                 }
; #pragma unroll
;                 for (int hh = 0; hh < 2; ++hh)
; #pragma unroll
;                     for (int i = 0; i < 2; ++i) vs[hh][i] = last ? voffN[hh][i] : voffA[hh][i];
;             } else {
; #pragma unroll
;                 for (int hh = 0; hh < 2; ++hh)
; #pragma unroll
;                     for (int i = 0; i < 2; ++i) vs[hh][i] = voffA[hh][i];
;             }
;             PG8_LDB(B0, 0, 0); PG8_LDB(B1, 0, 1); PG8_SCHED; PG8_LDA(At, 0, 0); PG8_STAGE(PG8_SA(1, 1), a1, voffA[1]);
;             PG8_WAIT_V(8); PG8_WAIT_L(0); PG8_BAR; if (do0) { PG8_MMA(0, 0, At, B0); PG8_MMA(0, 1, At, B1); } PG8_BAR; PG8_SCHED;
;             PG8_LDA(At, 0, 1); PG8_STAGE(PG8_SB(0, 0), b2, voffB); PG8_STAGE(PG8_SB(0, 1), b2 + hstep, voffB); PG8_STAGE(PG8_SA(0, 0), a2, vs[0]);
;             PG8_WAIT_V(8); PG8_WAIT_L(0); PG8_BAR; if (do1) { PG8_MMA(1, 0, At, B0); PG8_MMA(1, 1, At, B1); } PG8_BAR; PG8_SCHED;
.LBB0_1257:
	ds_read_b128 v[156:159], v176
	ds_read_b128 v[160:163], v177
	ds_read_b128 v[164:167], v178
	ds_read_b128 v[192:195], v179
	ds_read_b128 v[200:203], v180
	ds_read_b128 v[204:207], v181
	ds_read_b128 v[208:211], v182
	ds_read_b128 v[212:215], v183
	s_add_u32 s40, s38, 0x80
	s_addc_u32 s41, s39, 0
	s_cmp_eq_u32 s63, 12
	s_cselect_b32 s45, s3, s41
	s_cselect_b32 s44, s11, s40
	s_cselect_b32 s41, s12, s62
	s_cselect_b32 s40, s29, s31
	v_lshl_add_u64 v[168:169], s[38:39], 0, v[150:151]
	s_add_i32 m0, s47, 0xc000
	ds_read_b128 v[216:219], v184
	ds_read_b128 v[220:223], v184 offset:2048
	ds_read_b128 v[224:227], v185
	ds_read_b128 v[228:231], v185 offset:2048
	ds_read_b128 v[232:235], v184 offset:4096
	ds_read_b128 v[236:239], v184 offset:6144
	ds_read_b128 v[240:243], v185 offset:4096
	ds_read_b128 v[244:247], v185 offset:6144
	global_load_lds_dwordx4 v[168:169], off
	v_lshl_add_u64 v[168:169], s[38:39], 0, v[148:149]
	s_add_i32 m0, s47, 0xe000
	s_add_u32 s42, s40, 0x4000
	global_load_lds_dwordx4 v[168:169], off
	s_waitcnt vmcnt(8)
	s_waitcnt lgkmcnt(0)
	s_addc_u32 s43, s41, 0
	s_barrier
	s_setprio 1
	s_waitcnt lgkmcnt(0)
	v_mfma_f32_16x16x32_bf16 v[126:129], v[156:159], v[216:219], v[126:129]
	v_mfma_f32_16x16x32_bf16 v[118:121], v[164:167], v[216:219], v[118:121]
	v_mfma_f32_16x16x32_bf16 v[110:113], v[156:159], v[220:223], v[110:113]
	v_mfma_f32_16x16x32_bf16 v[102:105], v[164:167], v[220:223], v[102:105]
	v_mfma_f32_16x16x32_bf16 v[94:97], v[156:159], v[232:235], v[94:97]
	v_mfma_f32_16x16x32_bf16 v[86:89], v[164:167], v[232:235], v[86:89]
	v_mfma_f32_16x16x32_bf16 v[78:81], v[156:159], v[236:239], v[78:81]
	v_mfma_f32_16x16x32_bf16 v[70:73], v[164:167], v[236:239], v[70:73]
	v_mfma_f32_16x16x32_bf16 v[126:129], v[160:163], v[224:227], v[126:129]
	v_mfma_f32_16x16x32_bf16 v[118:121], v[192:195], v[224:227], v[118:121]
	v_mfma_f32_16x16x32_bf16 v[110:113], v[160:163], v[228:231], v[110:113]
	v_mfma_f32_16x16x32_bf16 v[102:105], v[192:195], v[228:231], v[102:105]
	v_mfma_f32_16x16x32_bf16 v[94:97], v[160:163], v[240:243], v[94:97]
	v_mfma_f32_16x16x32_bf16 v[86:89], v[192:195], v[240:243], v[86:89]
	v_mfma_f32_16x16x32_bf16 v[78:81], v[160:163], v[244:247], v[78:81]
	v_mfma_f32_16x16x32_bf16 v[70:73], v[192:195], v[244:247], v[70:73]
	v_mfma_f32_16x16x32_bf16 v[122:125], v[200:203], v[216:219], v[122:125]
	v_mfma_f32_16x16x32_bf16 v[114:117], v[208:211], v[216:219], v[114:117]
	v_mfma_f32_16x16x32_bf16 v[106:109], v[200:203], v[220:223], v[106:109]
	v_mfma_f32_16x16x32_bf16 v[98:101], v[208:211], v[220:223], v[98:101]
	v_mfma_f32_16x16x32_bf16 v[90:93], v[200:203], v[232:235], v[90:93]
	v_mfma_f32_16x16x32_bf16 v[82:85], v[208:211], v[232:235], v[82:85]
	v_mfma_f32_16x16x32_bf16 v[74:77], v[200:203], v[236:239], v[74:77]
	v_mfma_f32_16x16x32_bf16 v[66:69], v[208:211], v[236:239], v[66:69]
	v_mfma_f32_16x16x32_bf16 v[122:125], v[204:207], v[224:227], v[122:125]
	v_mfma_f32_16x16x32_bf16 v[114:117], v[212:215], v[224:227], v[114:117]
	v_mfma_f32_16x16x32_bf16 v[106:109], v[204:207], v[228:231], v[106:109]
	v_mfma_f32_16x16x32_bf16 v[98:101], v[212:215], v[228:231], v[98:101]
	v_mfma_f32_16x16x32_bf16 v[90:93], v[204:207], v[240:243], v[90:93]
	v_mfma_f32_16x16x32_bf16 v[82:85], v[212:215], v[240:243], v[82:85]
	v_mfma_f32_16x16x32_bf16 v[74:77], v[204:207], v[244:247], v[74:77]
	v_mfma_f32_16x16x32_bf16 v[66:69], v[212:215], v[244:247], v[66:69]
	s_setprio 0
	s_barrier
	s_add_i32 s64, s56, s46
	v_lshl_add_u64 v[168:169], s[40:41], 0, v[130:131]
	s_mov_b32 m0, s64
	ds_read_b128 v[216:219], v184 offset:16384
	ds_read_b128 v[220:223], v184 offset:18432
	ds_read_b128 v[224:227], v185 offset:16384
	ds_read_b128 v[228:231], v185 offset:18432
	ds_read_b128 v[232:235], v184 offset:20480
	ds_read_b128 v[236:239], v184 offset:22528
	ds_read_b128 v[240:243], v185 offset:20480
	ds_read_b128 v[244:247], v185 offset:22528
	global_load_lds_dwordx4 v[168:169], off
	s_add_i32 m0, s64, 0x2000
	s_add_u32 s64, s40, 0x40000
	v_lshl_add_u64 v[168:169], s[40:41], 0, v[132:133]
	s_addc_u32 s65, s41, 0
	s_add_i32 s66, s57, s46
	global_load_lds_dwordx4 v[168:169], off
	v_lshl_add_u64 v[168:169], s[64:65], 0, v[130:131]
	s_mov_b32 m0, s66
	v_lshl_add_u64 v[196:197], s[44:45], 0, v[136:137]
	global_load_lds_dwordx4 v[168:169], off
	v_lshl_add_u64 v[168:169], s[64:65], 0, v[132:133]
	s_add_i32 m0, s66, 0x2000
	s_nop 0
	global_load_lds_dwordx4 v[168:169], off
	v_lshl_add_u64 v[168:169], s[44:45], 0, v[134:135]
	s_mov_b32 m0, s47
	s_nop 0
	global_load_lds_dwordx4 v[168:169], off
	s_mov_b32 m0, s48
	s_nop 0
	global_load_lds_dwordx4 v[196:197], off
	s_waitcnt vmcnt(8)
	s_waitcnt lgkmcnt(0)
	s_barrier
; #define PG8_STAGE(bufoff, gbase, voff) do { _Pragma("unroll") for (int _i = 0; _i < 2; ++_i) \
;         __builtin_amdgcn_global_load_lds((const unsigned*)((const char*)(gbase) + (voff)[_i]), (LAS unsigned*)(lds + (bufoff) + ldsw + _i * 8192), 16, 0, 0); } while (0)
; #define PG8_LDA(dst, b, h) do { _Pragma("unroll") for (int m = 0; m < 4; ++m) _Pragma("unroll") for (int k = 0; k < 2; ++k) dst[m][k] = *(const LAS bf16x8*)(lds + PG8_SA(b, h) + ((aoff ^ (k * 64)) + m * 2048)); } while (0)
; #define PG8_LDB(dst, b, h) do { _Pragma("unroll") for (int n = 0; n < 2; ++n) _Pragma("unroll") for (int k = 0; k < 2; ++k) dst[n][k] = *(const LAS bf16x8*)(lds + PG8_SB(b, h) + ((boff ^ (k * 64)) + n * 2048)); } while (0)
; #define PG8_MMA(ai, bj, At, Bt) do { __builtin_amdgcn_s_setprio(1); _Pragma("unroll") for (int m = 0; m < 4; ++m) _Pragma("unroll") for (int n = 0; n < 2; ++n) _Pragma("unroll") for (int k = 0; k < 2; ++k) \
;         acc[ai][bj][m][n] = __builtin_amdgcn_mfma_f32_16x16x32_bf16(Bt[n][k], At[m][k], acc[ai][bj][m][n], 0, 0, 0); __builtin_amdgcn_s_setprio(0); } while (0)
; #define PG8_WAIT_V(n) asm volatile("s_waitcnt vmcnt(" #n ")" ::: "memory")
; #define PG8_WAIT_L(n) asm volatile("s_waitcnt lgkmcnt(" #n ")" ::: "memory")
; #define PG8_BAR __builtin_amdgcn_s_barrier()
; #define PG8_SCHED __builtin_amdgcn_sched_barrier(0)
;     ...
;             PG8_WAIT_V(8); PG8_WAIT_L(0); PG8_BAR; if (do1) { PG8_MMA(1, 0, At, B0); PG8_MMA(1, 1, At, B1); } PG8_BAR; PG8_SCHED;
;             PG8_LDB(B0, 1, 0); PG8_LDB(B1, 1, 1); PG8_SCHED; PG8_LDA(At, 1, 0); PG8_STAGE(PG8_SA(0, 1), a2, vs[1]);
;             PG8_WAIT_V(8); PG8_WAIT_L(0); PG8_BAR; if (do0) { PG8_MMA(0, 0, At, B0); PG8_MMA(0, 1, At, B1); } PG8_BAR; PG8_SCHED;
	s_setprio 1
	s_waitcnt lgkmcnt(0)
	v_mfma_f32_16x16x32_bf16 v[62:65], v[156:159], v[216:219], v[62:65]
	v_mfma_f32_16x16x32_bf16 v[54:57], v[164:167], v[216:219], v[54:57]
	v_mfma_f32_16x16x32_bf16 v[46:49], v[156:159], v[220:223], v[46:49]
	v_mfma_f32_16x16x32_bf16 v[38:41], v[164:167], v[220:223], v[38:41]
	v_mfma_f32_16x16x32_bf16 v[30:33], v[156:159], v[232:235], v[30:33]
	v_mfma_f32_16x16x32_bf16 v[22:25], v[164:167], v[232:235], v[22:25]
	v_mfma_f32_16x16x32_bf16 v[14:17], v[156:159], v[236:239], v[14:17]
	v_mfma_f32_16x16x32_bf16 v[6:9], v[164:167], v[236:239], v[6:9]
	v_mfma_f32_16x16x32_bf16 v[62:65], v[160:163], v[224:227], v[62:65]
	v_mfma_f32_16x16x32_bf16 v[54:57], v[192:195], v[224:227], v[54:57]
	v_mfma_f32_16x16x32_bf16 v[46:49], v[160:163], v[228:231], v[46:49]
	v_mfma_f32_16x16x32_bf16 v[38:41], v[192:195], v[228:231], v[38:41]
	v_mfma_f32_16x16x32_bf16 v[30:33], v[160:163], v[240:243], v[30:33]
	v_mfma_f32_16x16x32_bf16 v[22:25], v[192:195], v[240:243], v[22:25]
	v_mfma_f32_16x16x32_bf16 v[14:17], v[160:163], v[244:247], v[14:17]
	v_mfma_f32_16x16x32_bf16 v[6:9], v[192:195], v[244:247], v[6:9]
	v_mfma_f32_16x16x32_bf16 v[58:61], v[200:203], v[216:219], v[58:61]
	v_mfma_f32_16x16x32_bf16 v[50:53], v[208:211], v[216:219], v[50:53]
	v_mfma_f32_16x16x32_bf16 v[42:45], v[200:203], v[220:223], v[42:45]
	v_mfma_f32_16x16x32_bf16 v[34:37], v[208:211], v[220:223], v[34:37]
	v_mfma_f32_16x16x32_bf16 v[26:29], v[200:203], v[232:235], v[26:29]
	v_mfma_f32_16x16x32_bf16 v[18:21], v[208:211], v[232:235], v[18:21]
	v_mfma_f32_16x16x32_bf16 v[10:13], v[200:203], v[236:239], v[10:13]
	v_mfma_f32_16x16x32_bf16 v[2:5], v[208:211], v[236:239], v[2:5]
	v_mfma_f32_16x16x32_bf16 v[58:61], v[204:207], v[224:227], v[58:61]
	v_mfma_f32_16x16x32_bf16 v[50:53], v[212:215], v[224:227], v[50:53]
	v_mfma_f32_16x16x32_bf16 v[42:45], v[204:207], v[228:231], v[42:45]
	v_mfma_f32_16x16x32_bf16 v[34:37], v[212:215], v[228:231], v[34:37]
	v_mfma_f32_16x16x32_bf16 v[26:29], v[204:207], v[240:243], v[26:29]
	v_mfma_f32_16x16x32_bf16 v[18:21], v[212:215], v[240:243], v[18:21]
	v_mfma_f32_16x16x32_bf16 v[10:13], v[204:207], v[244:247], v[10:13]
	v_mfma_f32_16x16x32_bf16 v[2:5], v[212:215], v[244:247], v[2:5]
	s_setprio 0
	s_barrier
	s_add_i32 s64, 0, 0x18000
	v_add_u32_e32 v142, s64, v170
	v_add_u32_e32 v160, s64, v174
	s_add_i32 s65, 0, 0x1c000
	ds_read_b128 v[156:159], v142
	ds_read_b128 v[160:163], v160
	ds_read_b128 v[164:167], v186
	ds_read_b128 v[192:195], v187
	v_add_u32_e32 v142, s65, v170
	v_add_u32_e32 v191, s65, v174
	ds_read_b128 v[200:203], v142
	ds_read_b128 v[204:207], v191
	ds_read_b128 v[208:211], v188
	ds_read_b128 v[212:215], v189
	s_mov_b32 m0, s49
	v_lshl_add_u64 v[248:249], s[44:45], 0, v[138:139]
	ds_read_b128 v[216:219], v184 offset:32768
	ds_read_b128 v[220:223], v184 offset:34816
	ds_read_b128 v[224:227], v185 offset:32768
	ds_read_b128 v[228:231], v185 offset:34816
	ds_read_b128 v[232:235], v184 offset:36864
	ds_read_b128 v[236:239], v184 offset:38912
	ds_read_b128 v[240:243], v185 offset:36864
	ds_read_b128 v[244:247], v185 offset:38912
	global_load_lds_dwordx4 v[248:249], off
	v_lshl_add_u64 v[248:249], s[44:45], 0, v[140:141]
	s_mov_b32 m0, s50
	s_nop 0
	global_load_lds_dwordx4 v[248:249], off
	s_waitcnt vmcnt(8)
	s_waitcnt lgkmcnt(0)
	s_barrier
	s_setprio 1
	s_waitcnt lgkmcnt(0)
	v_mfma_f32_16x16x32_bf16 v[126:129], v[156:159], v[216:219], v[126:129]
	v_mfma_f32_16x16x32_bf16 v[118:121], v[164:167], v[216:219], v[118:121]
	v_mfma_f32_16x16x32_bf16 v[110:113], v[156:159], v[220:223], v[110:113]
	v_mfma_f32_16x16x32_bf16 v[102:105], v[164:167], v[220:223], v[102:105]
	v_mfma_f32_16x16x32_bf16 v[94:97], v[156:159], v[232:235], v[94:97]
	v_mfma_f32_16x16x32_bf16 v[86:89], v[164:167], v[232:235], v[86:89]
	v_mfma_f32_16x16x32_bf16 v[78:81], v[156:159], v[236:239], v[78:81]
	v_mfma_f32_16x16x32_bf16 v[70:73], v[164:167], v[236:239], v[70:73]
	v_mfma_f32_16x16x32_bf16 v[126:129], v[160:163], v[224:227], v[126:129]
	v_mfma_f32_16x16x32_bf16 v[118:121], v[192:195], v[224:227], v[118:121]
	v_mfma_f32_16x16x32_bf16 v[110:113], v[160:163], v[228:231], v[110:113]
	v_mfma_f32_16x16x32_bf16 v[102:105], v[192:195], v[228:231], v[102:105]
	v_mfma_f32_16x16x32_bf16 v[94:97], v[160:163], v[240:243], v[94:97]
	v_mfma_f32_16x16x32_bf16 v[86:89], v[192:195], v[240:243], v[86:89]
	v_mfma_f32_16x16x32_bf16 v[78:81], v[160:163], v[244:247], v[78:81]
	v_mfma_f32_16x16x32_bf16 v[70:73], v[192:195], v[244:247], v[70:73]
	v_mfma_f32_16x16x32_bf16 v[122:125], v[200:203], v[216:219], v[122:125]
	v_mfma_f32_16x16x32_bf16 v[114:117], v[208:211], v[216:219], v[114:117]
	v_mfma_f32_16x16x32_bf16 v[106:109], v[200:203], v[220:223], v[106:109]
	v_mfma_f32_16x16x32_bf16 v[98:101], v[208:211], v[220:223], v[98:101]
	v_mfma_f32_16x16x32_bf16 v[90:93], v[200:203], v[232:235], v[90:93]
	v_mfma_f32_16x16x32_bf16 v[82:85], v[208:211], v[232:235], v[82:85]
	v_mfma_f32_16x16x32_bf16 v[74:77], v[200:203], v[236:239], v[74:77]
	v_mfma_f32_16x16x32_bf16 v[66:69], v[208:211], v[236:239], v[66:69]
	v_mfma_f32_16x16x32_bf16 v[122:125], v[204:207], v[224:227], v[122:125]
	v_mfma_f32_16x16x32_bf16 v[114:117], v[212:215], v[224:227], v[114:117]
	v_mfma_f32_16x16x32_bf16 v[106:109], v[204:207], v[228:231], v[106:109]
	v_mfma_f32_16x16x32_bf16 v[98:101], v[212:215], v[228:231], v[98:101]
	v_mfma_f32_16x16x32_bf16 v[90:93], v[204:207], v[240:243], v[90:93]
	v_mfma_f32_16x16x32_bf16 v[82:85], v[212:215], v[240:243], v[82:85]
	v_mfma_f32_16x16x32_bf16 v[74:77], v[204:207], v[244:247], v[74:77]
	v_mfma_f32_16x16x32_bf16 v[66:69], v[212:215], v[244:247], v[66:69]
	s_setprio 0
	s_barrier
; #define PG8_STAGE(bufoff, gbase, voff) do { _Pragma("unroll") for (int _i = 0; _i < 2; ++_i) \
;         __builtin_amdgcn_global_load_lds((const unsigned*)((const char*)(gbase) + (voff)[_i]), (LAS unsigned*)(lds + (bufoff) + ldsw + _i * 8192), 16, 0, 0); } while (0)
; #define PG8_LDA(dst, b, h) do { _Pragma("unroll") for (int m = 0; m < 4; ++m) _Pragma("unroll") for (int k = 0; k < 2; ++k) dst[m][k] = *(const LAS bf16x8*)(lds + PG8_SA(b, h) + ((aoff ^ (k * 64)) + m * 2048)); } while (0)
; #define PG8_MMA(ai, bj, At, Bt) do { __builtin_amdgcn_s_setprio(1); _Pragma("unroll") for (int m = 0; m < 4; ++m) _Pragma("unroll") for (int n = 0; n < 2; ++n) _Pragma("unroll") for (int k = 0; k < 2; ++k) \
;         acc[ai][bj][m][n] = __builtin_amdgcn_mfma_f32_16x16x32_bf16(Bt[n][k], At[m][k], acc[ai][bj][m][n], 0, 0, 0); __builtin_amdgcn_s_setprio(0); } while (0)
; #define PG8_WAIT_V(n) asm volatile("s_waitcnt vmcnt(" #n ")" ::: "memory")
; #define PG8_WAIT_L(n) asm volatile("s_waitcnt lgkmcnt(" #n ")" ::: "memory")
; #define PG8_BAR __builtin_amdgcn_s_barrier()
; #define PG8_SCHED __builtin_amdgcn_sched_barrier(0)
;     ...
;             PG8_LDA(At, 1, 1); PG8_STAGE(PG8_SB(1, 0), b3, voffB); PG8_STAGE(PG8_SB(1, 1), b3 + hstep, voffB); PG8_STAGE(PG8_SA(1, 0), a3, vs[0]);
;             PG8_WAIT_V(8); PG8_WAIT_L(0); PG8_BAR; if (do1) { PG8_MMA(1, 0, At, B0); PG8_MMA(1, 1, At, B1); } PG8_BAR; PG8_SCHED;
;         }
;         if (wr == 0) PG8_BAR;
	s_add_i32 s44, s64, s46
	v_lshl_add_u64 v[248:249], s[42:43], 0, v[130:131]
	s_mov_b32 m0, s44
	ds_read_b128 v[216:219], v184 offset:49152
	ds_read_b128 v[220:223], v184 offset:51200
	ds_read_b128 v[224:227], v185 offset:49152
	ds_read_b128 v[228:231], v185 offset:51200
	ds_read_b128 v[232:235], v184 offset:53248
	ds_read_b128 v[236:239], v184 offset:55296
	ds_read_b128 v[240:243], v185 offset:53248
	ds_read_b128 v[244:247], v185 offset:55296
	global_load_lds_dwordx4 v[248:249], off
	s_add_i32 m0, s44, 0x2000
	s_add_u32 s40, s40, 0x44000
	v_lshl_add_u64 v[248:249], s[42:43], 0, v[132:133]
	s_addc_u32 s41, s41, 0
	s_add_i32 s42, s65, s46
	global_load_lds_dwordx4 v[248:249], off
	v_lshl_add_u64 v[248:249], s[40:41], 0, v[130:131]
	s_mov_b32 m0, s42
	v_lshl_add_u64 v[168:169], v[168:169], 0, s[20:21]
	global_load_lds_dwordx4 v[248:249], off
	v_lshl_add_u64 v[248:249], s[40:41], 0, v[132:133]
	s_add_i32 m0, s42, 0x2000
	s_nop 0
	global_load_lds_dwordx4 v[248:249], off
	s_mov_b32 m0, s52
	s_nop 0
	global_load_lds_dwordx4 v[168:169], off
	v_lshl_add_u64 v[168:169], v[196:197], 0, s[20:21]
	s_mov_b32 m0, s53
	s_nop 0
	global_load_lds_dwordx4 v[168:169], off
	s_waitcnt vmcnt(8)
	s_waitcnt lgkmcnt(0)
	s_barrier
	s_setprio 1
	s_waitcnt lgkmcnt(0)
	v_mfma_f32_16x16x32_bf16 v[62:65], v[156:159], v[216:219], v[62:65]
	v_mfma_f32_16x16x32_bf16 v[54:57], v[164:167], v[216:219], v[54:57]
	v_mfma_f32_16x16x32_bf16 v[46:49], v[156:159], v[220:223], v[46:49]
	v_mfma_f32_16x16x32_bf16 v[38:41], v[164:167], v[220:223], v[38:41]
	v_mfma_f32_16x16x32_bf16 v[30:33], v[156:159], v[232:235], v[30:33]
	v_mfma_f32_16x16x32_bf16 v[22:25], v[164:167], v[232:235], v[22:25]
	v_mfma_f32_16x16x32_bf16 v[14:17], v[156:159], v[236:239], v[14:17]
	v_mfma_f32_16x16x32_bf16 v[6:9], v[164:167], v[236:239], v[6:9]
	v_mfma_f32_16x16x32_bf16 v[62:65], v[160:163], v[224:227], v[62:65]
	v_mfma_f32_16x16x32_bf16 v[54:57], v[192:195], v[224:227], v[54:57]
	v_mfma_f32_16x16x32_bf16 v[46:49], v[160:163], v[228:231], v[46:49]
	v_mfma_f32_16x16x32_bf16 v[38:41], v[192:195], v[228:231], v[38:41]
	v_mfma_f32_16x16x32_bf16 v[30:33], v[160:163], v[240:243], v[30:33]
	v_mfma_f32_16x16x32_bf16 v[22:25], v[192:195], v[240:243], v[22:25]
	v_mfma_f32_16x16x32_bf16 v[14:17], v[160:163], v[244:247], v[14:17]
	v_mfma_f32_16x16x32_bf16 v[6:9], v[192:195], v[244:247], v[6:9]
	v_mfma_f32_16x16x32_bf16 v[58:61], v[200:203], v[216:219], v[58:61]
	v_mfma_f32_16x16x32_bf16 v[50:53], v[208:211], v[216:219], v[50:53]
	v_mfma_f32_16x16x32_bf16 v[42:45], v[200:203], v[220:223], v[42:45]
	v_mfma_f32_16x16x32_bf16 v[34:37], v[208:211], v[220:223], v[34:37]
	v_mfma_f32_16x16x32_bf16 v[26:29], v[200:203], v[232:235], v[26:29]
	v_mfma_f32_16x16x32_bf16 v[18:21], v[208:211], v[232:235], v[18:21]
	v_mfma_f32_16x16x32_bf16 v[10:13], v[200:203], v[236:239], v[10:13]
	v_mfma_f32_16x16x32_bf16 v[2:5], v[208:211], v[236:239], v[2:5]
	v_mfma_f32_16x16x32_bf16 v[58:61], v[204:207], v[224:227], v[58:61]
	v_mfma_f32_16x16x32_bf16 v[50:53], v[212:215], v[224:227], v[50:53]
	v_mfma_f32_16x16x32_bf16 v[42:45], v[204:207], v[228:231], v[42:45]
	v_mfma_f32_16x16x32_bf16 v[34:37], v[212:215], v[228:231], v[34:37]
	v_mfma_f32_16x16x32_bf16 v[26:29], v[204:207], v[240:243], v[26:29]
	v_mfma_f32_16x16x32_bf16 v[18:21], v[212:215], v[240:243], v[18:21]
	v_mfma_f32_16x16x32_bf16 v[10:13], v[204:207], v[244:247], v[10:13]
	v_mfma_f32_16x16x32_bf16 v[2:5], v[212:215], v[244:247], v[2:5]
	s_setprio 0
	s_barrier
	s_add_i32 s63, s63, 2
	s_add_u32 s31, s31, 0x8000
	s_addc_u32 s62, s62, 0
	s_add_u32 s38, s38, 0x100
	s_addc_u32 s39, s39, 0
	s_cmp_gt_u32 s63, 13
	s_cbranch_scc0 .LBB0_1257
	s_and_b64 vcc, exec, s[22:23]
	s_cbranch_vccz .LBB0_1260
	s_barrier

; #define PG8_STAGE(bufoff, gbase, voff) do { _Pragma("unroll") for (int _i = 0; _i < 2; ++_i) \
;         __builtin_amdgcn_global_load_lds((const unsigned*)((const char*)(gbase) + (voff)[_i]), (LAS unsigned*)(lds + (bufoff) + ldsw + _i * 8192), 16, 0, 0); } while (0)
; #define PG8_LDA(dst, b, h) do { _Pragma("unroll") for (int m = 0; m < 4; ++m) _Pragma("unroll") for (int k = 0; k < 2; ++k) dst[m][k] = *(const LAS bf16x8*)(lds + PG8_SA(b, h) + ((aoff ^ (k * 64)) + m * 2048)); } while (0)
; #define PG8_LDB(dst, b, h) do { _Pragma("unroll") for (int n = 0; n < 2; ++n) _Pragma("unroll") for (int k = 0; k < 2; ++k) dst[n][k] = *(const LAS bf16x8*)(lds + PG8_SB(b, h) + ((boff ^ (k * 64)) + n * 2048)); } while (0)
; #define PG8_BAR __builtin_amdgcn_s_barrier()
;     ...
;             const bool last = (t == nt - 2);
;             const char* a1 = cA + (size_t)(t + 1) * kstepA;
;             const char* a2 = last ? nA : cA + (size_t)(t + 2) * kstepA; const char* b2 = last ? nB : cB + (size_t)(t + 2) * kstepB;
;             const char* a3 = a2 + kstepA; const char* b3 = b2 + kstepB;
;             unsigned vs[2][2];
;             if constexpr (GATHER) {
;                 if (last && has_next) {
; #pragma unroll
;                     for (int hh = 0; hh < 2; ++hh)
; #pragma unroll
;                         for (int i = 0; i < 2; ++i) voffN[hh][i] = (unsigned)idxl[(ui + 1) * 256 + hh * HALF + sR[i]] * (unsigned)(K * 2) + (unsigned)sC[i] * 2u;
;                 }
; #pragma unroll
;                 for (int hh = 0; hh < 2; ++hh)
; #pragma unroll
;                     for (int i = 0; i < 2; ++i) vs[hh][i] = last ? voffN[hh][i] : voffA[hh][i];
;             } else {
; #pragma unroll
;                 for (int hh = 0; hh < 2; ++hh)
; #pragma unroll
;                     for (int i = 0; i < 2; ++i) vs[hh][i] = voffA[hh][i];
;             }
;             PG8_LDB(B0, 0, 0); PG8_LDB(B1, 0, 1); PG8_SCHED; PG8_LDA(At, 0, 0); PG8_STAGE(PG8_SA(1, 1), a1, voffA[1]);
;             PG8_WAIT_V(8); PG8_WAIT_L(0); PG8_BAR; if (do0) { PG8_MMA(0, 0, At, B0); PG8_MMA(0, 1, At, B1); } PG8_BAR; PG8_SCHED;
;             PG8_LDA(At, 0, 1); PG8_STAGE(PG8_SB(0, 0), b2, voffB); PG8_STAGE(PG8_SB(0, 1), b2 + hstep, voffB); PG8_STAGE(PG8_SA(0, 0), a2, vs[0]);
;             PG8_WAIT_V(8); PG8_WAIT_L(0); PG8_BAR; if (do1) { PG8_MMA(1, 0, At, B0); PG8_MMA(1, 1, At, B1); } PG8_BAR; PG8_SCHED;
.LBB0_1343:
	v_add_u32_e32 v130, s92, v161
	v_add_u32_e32 v134, s92, v188
	v_add_u32_e32 v138, s93, v161
	v_add_u32_e32 v142, s93, v188
	v_add_u32_e32 v158, s62, v161
	ds_read_b128 v[130:133], v130
	ds_read_b128 v[134:137], v134
	ds_read_b128 v[138:141], v138
	ds_read_b128 v[142:145], v142
	v_add_u32_e32 v184, s62, v188
	ds_read_b128 v[180:183], v158
	ds_read_b128 v[200:203], v184
	v_add_u32_e32 v158, s63, v161
	s_add_u32 s56, s0, 0x4000
	v_add_u32_e32 v184, s63, v188
	ds_read_b128 v[204:207], v158
	ds_read_b128 v[208:211], v184
	s_addc_u32 s57, s1, 0
	s_cmp_eq_u32 s95, 12
	s_cselect_b32 s60, s23, s56
	s_cselect_b32 s61, s3, s57
	s_cselect_b32 s58, s47, s74
	s_cselect_b32 s59, s45, s94
	s_add_u32 s56, s60, 0x4000
	s_addc_u32 s57, s61, 0
	v_lshl_add_u64 v[184:185], s[0:1], 0, v[176:177]
	s_add_i32 m0, s55, 0xc000
	ds_read_b128 v[212:215], v193
	ds_read_b128 v[216:219], v193 offset:2048
	ds_read_b128 v[220:223], v194
	ds_read_b128 v[224:227], v194 offset:2048
	ds_read_b128 v[228:231], v193 offset:4096
	ds_read_b128 v[232:235], v193 offset:6144
	ds_read_b128 v[236:239], v194 offset:4096
	ds_read_b128 v[240:243], v194 offset:6144
	global_load_lds_dwordx4 v[184:185], off
	v_lshl_add_u64 v[184:185], s[0:1], 0, v[178:179]
	s_add_i32 m0, s55, 0xe000
	s_nop 0
	global_load_lds_dwordx4 v[184:185], off
	s_waitcnt vmcnt(8)
	s_waitcnt lgkmcnt(0)
	s_barrier
	s_setprio 1
	s_waitcnt lgkmcnt(0)
	v_mfma_f32_16x16x32_bf16 v[126:129], v[130:133], v[212:215], v[126:129]
	v_mfma_f32_16x16x32_bf16 v[122:125], v[138:141], v[212:215], v[122:125]
	v_mfma_f32_16x16x32_bf16 v[94:97], v[130:133], v[216:219], v[94:97]
	v_mfma_f32_16x16x32_bf16 v[90:93], v[138:141], v[216:219], v[90:93]
	v_mfma_f32_16x16x32_bf16 v[62:65], v[130:133], v[228:231], v[62:65]
	v_mfma_f32_16x16x32_bf16 v[58:61], v[138:141], v[228:231], v[58:61]
	v_mfma_f32_16x16x32_bf16 v[30:33], v[130:133], v[232:235], v[30:33]
	v_mfma_f32_16x16x32_bf16 v[26:29], v[138:141], v[232:235], v[26:29]
	v_mfma_f32_16x16x32_bf16 v[126:129], v[134:137], v[220:223], v[126:129]
	v_mfma_f32_16x16x32_bf16 v[122:125], v[142:145], v[220:223], v[122:125]
	v_mfma_f32_16x16x32_bf16 v[94:97], v[134:137], v[224:227], v[94:97]
	v_mfma_f32_16x16x32_bf16 v[90:93], v[142:145], v[224:227], v[90:93]
	v_mfma_f32_16x16x32_bf16 v[62:65], v[134:137], v[236:239], v[62:65]
	v_mfma_f32_16x16x32_bf16 v[58:61], v[142:145], v[236:239], v[58:61]
	v_mfma_f32_16x16x32_bf16 v[30:33], v[134:137], v[240:243], v[30:33]
	v_mfma_f32_16x16x32_bf16 v[26:29], v[142:145], v[240:243], v[26:29]
	v_mfma_f32_16x16x32_bf16 v[110:113], v[180:183], v[212:215], v[110:113]
	v_mfma_f32_16x16x32_bf16 v[106:109], v[204:207], v[212:215], v[106:109]
	v_mfma_f32_16x16x32_bf16 v[78:81], v[180:183], v[216:219], v[78:81]
	v_mfma_f32_16x16x32_bf16 v[74:77], v[204:207], v[216:219], v[74:77]
	v_mfma_f32_16x16x32_bf16 v[46:49], v[180:183], v[228:231], v[46:49]
	v_mfma_f32_16x16x32_bf16 v[42:45], v[204:207], v[228:231], v[42:45]
	v_mfma_f32_16x16x32_bf16 v[14:17], v[180:183], v[232:235], v[14:17]
	v_mfma_f32_16x16x32_bf16 v[10:13], v[204:207], v[232:235], v[10:13]
	v_mfma_f32_16x16x32_bf16 v[110:113], v[200:203], v[220:223], v[110:113]
	v_mfma_f32_16x16x32_bf16 v[106:109], v[208:211], v[220:223], v[106:109]
	v_mfma_f32_16x16x32_bf16 v[78:81], v[200:203], v[224:227], v[78:81]
	v_mfma_f32_16x16x32_bf16 v[74:77], v[208:211], v[224:227], v[74:77]
	v_mfma_f32_16x16x32_bf16 v[46:49], v[200:203], v[236:239], v[46:49]
	v_mfma_f32_16x16x32_bf16 v[42:45], v[208:211], v[236:239], v[42:45]
	v_mfma_f32_16x16x32_bf16 v[14:17], v[200:203], v[240:243], v[14:17]
	v_mfma_f32_16x16x32_bf16 v[10:13], v[208:211], v[240:243], v[10:13]
	s_setprio 0
	s_barrier
	s_add_i32 vcc_lo, s92, s64
	v_lshl_add_u64 v[184:185], s[58:59], 0, v[146:147]
	s_mov_b32 m0, vcc_lo
	ds_read_b128 v[212:215], v193 offset:16384
	ds_read_b128 v[216:219], v193 offset:18432
	ds_read_b128 v[220:223], v194 offset:16384
	ds_read_b128 v[224:227], v194 offset:18432
	ds_read_b128 v[228:231], v193 offset:20480
	ds_read_b128 v[232:235], v193 offset:22528
	ds_read_b128 v[236:239], v194 offset:20480
	ds_read_b128 v[240:243], v194 offset:22528
	global_load_lds_dwordx4 v[184:185], off
	s_add_i32 m0, vcc_lo, 0x2000
	s_add_u32 vcc_lo, s58, 0x40000
	v_lshl_add_u64 v[196:197], s[58:59], 0, v[148:149]
	s_addc_u32 vcc_hi, s59, 0
	s_add_i32 s18, s62, s64
	global_load_lds_dwordx4 v[196:197], off
	v_lshl_add_u64 v[244:245], vcc, 0, v[146:147]
	s_mov_b32 m0, s18
	s_nop 0
	global_load_lds_dwordx4 v[244:245], off
	v_lshl_add_u64 v[244:245], vcc, 0, v[148:149]
	s_add_i32 m0, s18, 0x2000
	s_nop 0
	global_load_lds_dwordx4 v[244:245], off
	v_lshl_add_u64 v[244:245], s[60:61], 0, v[150:151]
	s_mov_b32 m0, s55
	s_nop 0
	global_load_lds_dwordx4 v[244:245], off
	v_lshl_add_u64 v[244:245], s[60:61], 0, v[152:153]
	s_mov_b32 m0, s65
	s_nop 0
	global_load_lds_dwordx4 v[244:245], off
	s_waitcnt vmcnt(8)
	s_waitcnt lgkmcnt(0)
	s_barrier
; #define PG8_STAGE(bufoff, gbase, voff) do { _Pragma("unroll") for (int _i = 0; _i < 2; ++_i) \
;         __builtin_amdgcn_global_load_lds((const unsigned*)((const char*)(gbase) + (voff)[_i]), (LAS unsigned*)(lds + (bufoff) + ldsw + _i * 8192), 16, 0, 0); } while (0)
; #define PG8_LDA(dst, b, h) do { _Pragma("unroll") for (int m = 0; m < 4; ++m) _Pragma("unroll") for (int k = 0; k < 2; ++k) dst[m][k] = *(const LAS bf16x8*)(lds + PG8_SA(b, h) + ((aoff ^ (k * 64)) + m * 2048)); } while (0)
; #define PG8_LDB(dst, b, h) do { _Pragma("unroll") for (int n = 0; n < 2; ++n) _Pragma("unroll") for (int k = 0; k < 2; ++k) dst[n][k] = *(const LAS bf16x8*)(lds + PG8_SB(b, h) + ((boff ^ (k * 64)) + n * 2048)); } while (0)
; #define PG8_MMA(ai, bj, At, Bt) do { __builtin_amdgcn_s_setprio(1); _Pragma("unroll") for (int m = 0; m < 4; ++m) _Pragma("unroll") for (int n = 0; n < 2; ++n) _Pragma("unroll") for (int k = 0; k < 2; ++k) \
;         acc[ai][bj][m][n] = __builtin_amdgcn_mfma_f32_16x16x32_bf16(Bt[n][k], At[m][k], acc[ai][bj][m][n], 0, 0, 0); __builtin_amdgcn_s_setprio(0); } while (0)
; #define PG8_WAIT_V(n) asm volatile("s_waitcnt vmcnt(" #n ")" ::: "memory")
; #define PG8_WAIT_L(n) asm volatile("s_waitcnt lgkmcnt(" #n ")" ::: "memory")
; #define PG8_BAR __builtin_amdgcn_s_barrier()
; #define PG8_SCHED __builtin_amdgcn_sched_barrier(0)
;     ...
;             PG8_WAIT_V(8); PG8_WAIT_L(0); PG8_BAR; if (do1) { PG8_MMA(1, 0, At, B0); PG8_MMA(1, 1, At, B1); } PG8_BAR; PG8_SCHED;
;             PG8_LDB(B0, 1, 0); PG8_LDB(B1, 1, 1); PG8_SCHED; PG8_LDA(At, 1, 0); PG8_STAGE(PG8_SA(0, 1), a2, vs[1]);
;             PG8_WAIT_V(8); PG8_WAIT_L(0); PG8_BAR; if (do0) { PG8_MMA(0, 0, At, B0); PG8_MMA(0, 1, At, B1); } PG8_BAR; PG8_SCHED;
	s_setprio 1
	s_waitcnt lgkmcnt(0)
	v_mfma_f32_16x16x32_bf16 v[118:121], v[130:133], v[212:215], v[118:121]
	v_mfma_f32_16x16x32_bf16 v[114:117], v[138:141], v[212:215], v[114:117]
	v_mfma_f32_16x16x32_bf16 v[86:89], v[130:133], v[216:219], v[86:89]
	v_mfma_f32_16x16x32_bf16 v[82:85], v[138:141], v[216:219], v[82:85]
	v_mfma_f32_16x16x32_bf16 v[54:57], v[130:133], v[228:231], v[54:57]
	v_mfma_f32_16x16x32_bf16 v[50:53], v[138:141], v[228:231], v[50:53]
	v_mfma_f32_16x16x32_bf16 v[22:25], v[130:133], v[232:235], v[22:25]
	v_mfma_f32_16x16x32_bf16 v[18:21], v[138:141], v[232:235], v[18:21]
	v_mfma_f32_16x16x32_bf16 v[118:121], v[134:137], v[220:223], v[118:121]
	v_mfma_f32_16x16x32_bf16 v[114:117], v[142:145], v[220:223], v[114:117]
	v_mfma_f32_16x16x32_bf16 v[86:89], v[134:137], v[224:227], v[86:89]
	v_mfma_f32_16x16x32_bf16 v[82:85], v[142:145], v[224:227], v[82:85]
	v_mfma_f32_16x16x32_bf16 v[54:57], v[134:137], v[236:239], v[54:57]
	v_mfma_f32_16x16x32_bf16 v[50:53], v[142:145], v[236:239], v[50:53]
	v_mfma_f32_16x16x32_bf16 v[22:25], v[134:137], v[240:243], v[22:25]
	v_mfma_f32_16x16x32_bf16 v[18:21], v[142:145], v[240:243], v[18:21]
	v_mfma_f32_16x16x32_bf16 v[102:105], v[180:183], v[212:215], v[102:105]
	v_mfma_f32_16x16x32_bf16 v[98:101], v[204:207], v[212:215], v[98:101]
	v_mfma_f32_16x16x32_bf16 v[70:73], v[180:183], v[216:219], v[70:73]
	v_mfma_f32_16x16x32_bf16 v[66:69], v[204:207], v[216:219], v[66:69]
	v_mfma_f32_16x16x32_bf16 v[38:41], v[180:183], v[228:231], v[38:41]
	v_mfma_f32_16x16x32_bf16 v[34:37], v[204:207], v[228:231], v[34:37]
	v_mfma_f32_16x16x32_bf16 v[6:9], v[180:183], v[232:235], v[6:9]
	v_mfma_f32_16x16x32_bf16 v[2:5], v[204:207], v[232:235], v[2:5]
	v_mfma_f32_16x16x32_bf16 v[102:105], v[200:203], v[220:223], v[102:105]
	v_mfma_f32_16x16x32_bf16 v[98:101], v[208:211], v[220:223], v[98:101]
	v_mfma_f32_16x16x32_bf16 v[70:73], v[200:203], v[224:227], v[70:73]
	v_mfma_f32_16x16x32_bf16 v[66:69], v[208:211], v[224:227], v[66:69]
	v_mfma_f32_16x16x32_bf16 v[38:41], v[200:203], v[236:239], v[38:41]
	v_mfma_f32_16x16x32_bf16 v[34:37], v[208:211], v[236:239], v[34:37]
	v_mfma_f32_16x16x32_bf16 v[6:9], v[200:203], v[240:243], v[6:9]
	v_mfma_f32_16x16x32_bf16 v[2:5], v[208:211], v[240:243], v[2:5]
	s_setprio 0
	s_barrier
	s_add_i32 s18, 0, 0x18000
	s_add_i32 s19, 0, 0x1c000
	v_add_u32_e32 v130, s18, v161
	v_add_u32_e32 v134, s18, v188
	v_add_u32_e32 v138, s72, v161
	v_add_u32_e32 v142, s72, v188
	v_add_u32_e32 v158, s19, v161
	ds_read_b128 v[130:133], v130
	ds_read_b128 v[134:137], v134
	ds_read_b128 v[138:141], v138
	ds_read_b128 v[142:145], v142
	v_add_u32_e32 v195, s19, v188
	ds_read_b128 v[180:183], v158
	ds_read_b128 v[200:203], v195
	v_add_u32_e32 v158, s73, v161
	v_add_u32_e32 v195, s73, v188
	ds_read_b128 v[204:207], v158
	ds_read_b128 v[208:211], v195
	s_mov_b32 m0, s66
	v_lshl_add_u64 v[244:245], s[60:61], 0, v[154:155]
	ds_read_b128 v[212:215], v193 offset:32768
	ds_read_b128 v[216:219], v193 offset:34816
	ds_read_b128 v[220:223], v194 offset:32768
	ds_read_b128 v[224:227], v194 offset:34816
	ds_read_b128 v[228:231], v193 offset:36864
	ds_read_b128 v[232:235], v193 offset:38912
	ds_read_b128 v[236:239], v194 offset:36864
	ds_read_b128 v[240:243], v194 offset:38912
	global_load_lds_dwordx4 v[244:245], off
	v_lshl_add_u64 v[244:245], s[60:61], 0, v[156:157]
	s_mov_b32 m0, s67
	s_nop 0
	global_load_lds_dwordx4 v[244:245], off
	s_waitcnt vmcnt(8)
	s_waitcnt lgkmcnt(0)
	s_barrier
	s_setprio 1
	s_waitcnt lgkmcnt(0)
	v_mfma_f32_16x16x32_bf16 v[126:129], v[130:133], v[212:215], v[126:129]
	v_mfma_f32_16x16x32_bf16 v[122:125], v[138:141], v[212:215], v[122:125]
	v_mfma_f32_16x16x32_bf16 v[94:97], v[130:133], v[216:219], v[94:97]
	v_mfma_f32_16x16x32_bf16 v[90:93], v[138:141], v[216:219], v[90:93]
	v_mfma_f32_16x16x32_bf16 v[62:65], v[130:133], v[228:231], v[62:65]
	v_mfma_f32_16x16x32_bf16 v[58:61], v[138:141], v[228:231], v[58:61]
	v_mfma_f32_16x16x32_bf16 v[30:33], v[130:133], v[232:235], v[30:33]
	v_mfma_f32_16x16x32_bf16 v[26:29], v[138:141], v[232:235], v[26:29]
	v_mfma_f32_16x16x32_bf16 v[126:129], v[134:137], v[220:223], v[126:129]
	v_mfma_f32_16x16x32_bf16 v[122:125], v[142:145], v[220:223], v[122:125]
	v_mfma_f32_16x16x32_bf16 v[94:97], v[134:137], v[224:227], v[94:97]
	v_mfma_f32_16x16x32_bf16 v[90:93], v[142:145], v[224:227], v[90:93]
	v_mfma_f32_16x16x32_bf16 v[62:65], v[134:137], v[236:239], v[62:65]
	v_mfma_f32_16x16x32_bf16 v[58:61], v[142:145], v[236:239], v[58:61]
	v_mfma_f32_16x16x32_bf16 v[30:33], v[134:137], v[240:243], v[30:33]
	v_mfma_f32_16x16x32_bf16 v[26:29], v[142:145], v[240:243], v[26:29]
	v_mfma_f32_16x16x32_bf16 v[110:113], v[180:183], v[212:215], v[110:113]
	v_mfma_f32_16x16x32_bf16 v[106:109], v[204:207], v[212:215], v[106:109]
	v_mfma_f32_16x16x32_bf16 v[78:81], v[180:183], v[216:219], v[78:81]
	v_mfma_f32_16x16x32_bf16 v[74:77], v[204:207], v[216:219], v[74:77]
	v_mfma_f32_16x16x32_bf16 v[46:49], v[180:183], v[228:231], v[46:49]
	v_mfma_f32_16x16x32_bf16 v[42:45], v[204:207], v[228:231], v[42:45]
	v_mfma_f32_16x16x32_bf16 v[14:17], v[180:183], v[232:235], v[14:17]
	v_mfma_f32_16x16x32_bf16 v[10:13], v[204:207], v[232:235], v[10:13]
	v_mfma_f32_16x16x32_bf16 v[110:113], v[200:203], v[220:223], v[110:113]
	v_mfma_f32_16x16x32_bf16 v[106:109], v[208:211], v[220:223], v[106:109]
	v_mfma_f32_16x16x32_bf16 v[78:81], v[200:203], v[224:227], v[78:81]
	v_mfma_f32_16x16x32_bf16 v[74:77], v[208:211], v[224:227], v[74:77]
	v_mfma_f32_16x16x32_bf16 v[46:49], v[200:203], v[236:239], v[46:49]
	v_mfma_f32_16x16x32_bf16 v[42:45], v[208:211], v[236:239], v[42:45]
	v_mfma_f32_16x16x32_bf16 v[14:17], v[200:203], v[240:243], v[14:17]
	v_mfma_f32_16x16x32_bf16 v[10:13], v[208:211], v[240:243], v[10:13]
	s_setprio 0
	s_barrier
; #define PG8_STAGE(bufoff, gbase, voff) do { _Pragma("unroll") for (int _i = 0; _i < 2; ++_i) \
;         __builtin_amdgcn_global_load_lds((const unsigned*)((const char*)(gbase) + (voff)[_i]), (LAS unsigned*)(lds + (bufoff) + ldsw + _i * 8192), 16, 0, 0); } while (0)
; #define PG8_LDA(dst, b, h) do { _Pragma("unroll") for (int m = 0; m < 4; ++m) _Pragma("unroll") for (int k = 0; k < 2; ++k) dst[m][k] = *(const LAS bf16x8*)(lds + PG8_SA(b, h) + ((aoff ^ (k * 64)) + m * 2048)); } while (0)
; #define PG8_MMA(ai, bj, At, Bt) do { __builtin_amdgcn_s_setprio(1); _Pragma("unroll") for (int m = 0; m < 4; ++m) _Pragma("unroll") for (int n = 0; n < 2; ++n) _Pragma("unroll") for (int k = 0; k < 2; ++k) \
;         acc[ai][bj][m][n] = __builtin_amdgcn_mfma_f32_16x16x32_bf16(Bt[n][k], At[m][k], acc[ai][bj][m][n], 0, 0, 0); __builtin_amdgcn_s_setprio(0); } while (0)
; #define PG8_WAIT_V(n) asm volatile("s_waitcnt vmcnt(" #n ")" ::: "memory")
; #define PG8_WAIT_L(n) asm volatile("s_waitcnt lgkmcnt(" #n ")" ::: "memory")
; #define PG8_BAR __builtin_amdgcn_s_barrier()
; #define PG8_SCHED __builtin_amdgcn_sched_barrier(0)
;     ...
;             PG8_LDA(At, 1, 1); PG8_STAGE(PG8_SB(1, 0), b3, voffB); PG8_STAGE(PG8_SB(1, 1), b3 + hstep, voffB); PG8_STAGE(PG8_SA(1, 0), a3, vs[0]);
;             PG8_WAIT_V(8); PG8_WAIT_L(0); PG8_BAR; if (do1) { PG8_MMA(1, 0, At, B0); PG8_MMA(1, 1, At, B1); } PG8_BAR; PG8_SCHED;
;         }
;         if (wr == 0) PG8_BAR;
	s_add_i32 s18, s18, s64
	v_lshl_add_u64 v[184:185], v[184:185], 0, s[10:11]
	s_mov_b32 m0, s18
	ds_read_b128 v[212:215], v193 offset:49152
	ds_read_b128 v[216:219], v193 offset:51200
	ds_read_b128 v[220:223], v194 offset:49152
	ds_read_b128 v[224:227], v194 offset:51200
	ds_read_b128 v[228:231], v193 offset:53248
	ds_read_b128 v[232:235], v193 offset:55296
	ds_read_b128 v[236:239], v194 offset:53248
	ds_read_b128 v[240:243], v194 offset:55296
	global_load_lds_dwordx4 v[184:185], off
	s_add_i32 m0, s18, 0x2000
	s_add_u32 s58, s58, 0x40080
	v_lshl_add_u64 v[184:185], v[196:197], 0, s[10:11]
	s_addc_u32 s59, s59, 0
	s_add_i32 s18, s19, s64
	global_load_lds_dwordx4 v[184:185], off
	v_lshl_add_u64 v[184:185], s[58:59], 0, v[146:147]
	s_mov_b32 m0, s18
	s_nop 0
	global_load_lds_dwordx4 v[184:185], off
	v_lshl_add_u64 v[184:185], s[58:59], 0, v[148:149]
	s_add_i32 m0, s18, 0x2000
	s_nop 0
	global_load_lds_dwordx4 v[184:185], off
	v_lshl_add_u64 v[184:185], s[56:57], 0, v[150:151]
	s_mov_b32 m0, s70
	s_nop 0
	global_load_lds_dwordx4 v[184:185], off
	v_lshl_add_u64 v[184:185], s[56:57], 0, v[152:153]
	s_mov_b32 m0, s71
	s_nop 0
	global_load_lds_dwordx4 v[184:185], off
	s_waitcnt vmcnt(8)
	s_waitcnt lgkmcnt(0)
	s_barrier
	s_setprio 1
	s_waitcnt lgkmcnt(0)
	v_mfma_f32_16x16x32_bf16 v[118:121], v[130:133], v[212:215], v[118:121]
	v_mfma_f32_16x16x32_bf16 v[114:117], v[138:141], v[212:215], v[114:117]
	v_mfma_f32_16x16x32_bf16 v[86:89], v[130:133], v[216:219], v[86:89]
	v_mfma_f32_16x16x32_bf16 v[82:85], v[138:141], v[216:219], v[82:85]
	v_mfma_f32_16x16x32_bf16 v[54:57], v[130:133], v[228:231], v[54:57]
	v_mfma_f32_16x16x32_bf16 v[50:53], v[138:141], v[228:231], v[50:53]
	v_mfma_f32_16x16x32_bf16 v[22:25], v[130:133], v[232:235], v[22:25]
	v_mfma_f32_16x16x32_bf16 v[18:21], v[138:141], v[232:235], v[18:21]
	v_mfma_f32_16x16x32_bf16 v[118:121], v[134:137], v[220:223], v[118:121]
	v_mfma_f32_16x16x32_bf16 v[114:117], v[142:145], v[220:223], v[114:117]
	v_mfma_f32_16x16x32_bf16 v[86:89], v[134:137], v[224:227], v[86:89]
	v_mfma_f32_16x16x32_bf16 v[82:85], v[142:145], v[224:227], v[82:85]
	v_mfma_f32_16x16x32_bf16 v[54:57], v[134:137], v[236:239], v[54:57]
	v_mfma_f32_16x16x32_bf16 v[50:53], v[142:145], v[236:239], v[50:53]
	v_mfma_f32_16x16x32_bf16 v[22:25], v[134:137], v[240:243], v[22:25]
	v_mfma_f32_16x16x32_bf16 v[18:21], v[142:145], v[240:243], v[18:21]
	v_mfma_f32_16x16x32_bf16 v[102:105], v[180:183], v[212:215], v[102:105]
	v_mfma_f32_16x16x32_bf16 v[98:101], v[204:207], v[212:215], v[98:101]
	v_mfma_f32_16x16x32_bf16 v[70:73], v[180:183], v[216:219], v[70:73]
	v_mfma_f32_16x16x32_bf16 v[66:69], v[204:207], v[216:219], v[66:69]
	v_mfma_f32_16x16x32_bf16 v[38:41], v[180:183], v[228:231], v[38:41]
	v_mfma_f32_16x16x32_bf16 v[34:37], v[204:207], v[228:231], v[34:37]
	v_mfma_f32_16x16x32_bf16 v[6:9], v[180:183], v[232:235], v[6:9]
	v_mfma_f32_16x16x32_bf16 v[2:5], v[204:207], v[232:235], v[2:5]
	v_mfma_f32_16x16x32_bf16 v[102:105], v[200:203], v[220:223], v[102:105]
	v_mfma_f32_16x16x32_bf16 v[98:101], v[208:211], v[220:223], v[98:101]
	v_mfma_f32_16x16x32_bf16 v[70:73], v[200:203], v[224:227], v[70:73]
	v_mfma_f32_16x16x32_bf16 v[66:69], v[208:211], v[224:227], v[66:69]
	v_mfma_f32_16x16x32_bf16 v[38:41], v[200:203], v[236:239], v[38:41]
	v_mfma_f32_16x16x32_bf16 v[34:37], v[208:211], v[236:239], v[34:37]
	v_mfma_f32_16x16x32_bf16 v[6:9], v[200:203], v[240:243], v[6:9]
	v_mfma_f32_16x16x32_bf16 v[2:5], v[208:211], v[240:243], v[2:5]
	s_setprio 0
	s_barrier
	s_add_i32 s95, s95, 2
	s_add_u32 s74, s74, 0x100
	s_addc_u32 s94, s94, 0
	s_add_u32 s0, s0, 0x8000
	s_addc_u32 s1, s1, 0
	s_cmp_gt_u32 s95, 13
	s_cbranch_scc0 .LBB0_1343
	s_and_b64 vcc, exec, s[12:13]
	s_cbranch_vccz .LBB0_1346
	s_barrier

;     __device__ bool next(int i, Unit& u) const { return map((long)i * G + c, u); }
;     __device__ bool next(int i, Unit& u) const { if (!p.next(i, u)) return false; if (u.pn >= 4) u.pn += 2; return true; }
; #define PG8_BAR __builtin_amdgcn_s_barrier()
;     ...
;         const bool has_next = S.next(ui + 1, nxt);
;         const char* nA = has_next ? (const char*)(g.A + (size_t)nxt.z * g.aStrideZ) + (GATHER ? (size_t)0 : (size_t)nxt.pm * tstep) + k0t(nxt) * kstepA : cA;
;         const char* nB = has_next ? (const char*)(g.Bt + (size_t)nxt.z * g.bStrideZ) + (size_t)nxt.pn * tstep + k0t(nxt) * kstepB : cB;
;         const int nt = (SPLITK && cur.kq >= 0) ? (cur.kq < 2 ? 12 : 10) : ntf;
;         const bool shortu = cur.pm >= SHORT_PM, do0 = (HALFM && cur.kq >= 0) ? cur.kq == 0 : (!shortu || wr == 0), do1 = (HALFM && cur.kq >= 0) ? cur.kq == 1 : !shortu;
;         for (int t = 0; t < nt; t += 2) {
;             const bool last = (t == nt - 2);
;             const char* a1 = cA + (size_t)(t + 1) * kstepA;
;             const char* a2 = last ? nA : cA + (size_t)(t + 2) * kstepA; const char* b2 = last ? nB : cB + (size_t)(t + 2) * kstepB;
;             const char* a3 = a2 + kstepA; const char* b3 = b2 + kstepB;
;             unsigned vs[2][2];
;             if constexpr (GATHER) {
;                 if (last && has_next) {
; #pragma unroll
;                     for (int hh = 0; hh < 2; ++hh)
; #pragma unroll
;                         for (int i = 0; i < 2; ++i) voffN[hh][i] = (unsigned)idxl[(ui + 1) * 256 + hh * HALF + sR[i]] * (unsigned)(K * 2) + (unsigned)sC[i] * 2u;
;                 }
; #pragma unroll
;                 for (int hh = 0; hh < 2; ++hh)
; #pragma unroll
;                     for (int i = 0; i < 2; ++i) vs[hh][i] = last ? voffN[hh][i] : voffA[hh][i];
;             } else {
; #pragma unroll
;                 for (int hh = 0; hh < 2; ++hh)
; #pragma unroll
;                     for (int i = 0; i < 2; ++i) vs[hh][i] = voffA[hh][i];
;             }
;             PG8_LDB(B0, 0, 0); PG8_LDB(B1, 0, 1); PG8_SCHED; PG8_LDA(At, 0, 0); PG8_STAGE(PG8_SA(1, 1), a1, voffA[1]);
;             PG8_WAIT_V(8); PG8_WAIT_L(0); PG8_BAR; if (do0) { PG8_MMA(0, 0, At, B0); PG8_MMA(0, 1, At, B1); } PG8_BAR; PG8_SCHED;
;             PG8_LDA(At, 0, 1); PG8_STAGE(PG8_SB(0, 0), b2, voffB); PG8_STAGE(PG8_SB(0, 1), b2 + hstep, voffB); PG8_STAGE(PG8_SA(0, 0), a2, vs[0]);
.LBB0_1498:
	v_add_u32_e32 v130, s70, v153
	v_add_u32_e32 v134, s70, v184
	v_add_u32_e32 v150, s71, v153
	v_add_u32_e32 v176, s71, v184
	ds_read_b128 v[130:133], v130
	ds_read_b128 v[134:137], v134
	ds_read_b128 v[172:175], v150
	ds_read_b128 v[176:179], v176
	v_add_u32_e32 v150, s92, v153
	v_add_u32_e32 v180, s92, v184
	ds_read_b128 v[192:195], v150
	ds_read_b128 v[200:203], v180
	v_add_u32_e32 v150, s93, v153
	s_add_u32 s6, s0, 0x4000
	v_add_u32_e32 v180, s93, v184
	ds_read_b128 v[204:207], v150
	ds_read_b128 v[208:211], v180
	s_addc_u32 s7, s1, 0
	s_cmp_eq_u32 s63, 12
	s_cselect_b32 s58, s9, s6
	s_cselect_b32 s59, s3, s7
	s_cselect_b32 s56, s37, s49
	s_cselect_b32 s57, s23, s62
	s_add_u32 s6, s58, 0x4000
	s_addc_u32 s7, s59, 0
	v_lshl_add_u64 v[180:181], s[0:1], 0, v[168:169]
	s_add_i32 m0, s61, 0xc000
	ds_read_b128 v[212:215], v189
	ds_read_b128 v[216:219], v189 offset:2048
	ds_read_b128 v[220:223], v190
	ds_read_b128 v[224:227], v190 offset:2048
	ds_read_b128 v[228:231], v189 offset:4096
	ds_read_b128 v[232:235], v189 offset:6144
	ds_read_b128 v[236:239], v190 offset:4096
	ds_read_b128 v[240:243], v190 offset:6144
	global_load_lds_dwordx4 v[180:181], off
	v_lshl_add_u64 v[180:181], s[0:1], 0, v[170:171]
	s_add_i32 m0, s61, 0xe000
	s_nop 0
	global_load_lds_dwordx4 v[180:181], off
	s_waitcnt vmcnt(8)
	s_waitcnt lgkmcnt(0)
	s_barrier
	s_setprio 1
	s_waitcnt lgkmcnt(0)
	v_mfma_f32_16x16x32_bf16 v[126:129], v[130:133], v[212:215], v[126:129]
	v_mfma_f32_16x16x32_bf16 v[122:125], v[172:175], v[212:215], v[122:125]
	v_mfma_f32_16x16x32_bf16 v[94:97], v[130:133], v[216:219], v[94:97]
	v_mfma_f32_16x16x32_bf16 v[90:93], v[172:175], v[216:219], v[90:93]
	v_mfma_f32_16x16x32_bf16 v[62:65], v[130:133], v[228:231], v[62:65]
	v_mfma_f32_16x16x32_bf16 v[58:61], v[172:175], v[228:231], v[58:61]
	v_mfma_f32_16x16x32_bf16 v[30:33], v[130:133], v[232:235], v[30:33]
	v_mfma_f32_16x16x32_bf16 v[26:29], v[172:175], v[232:235], v[26:29]
	v_mfma_f32_16x16x32_bf16 v[126:129], v[134:137], v[220:223], v[126:129]
	v_mfma_f32_16x16x32_bf16 v[122:125], v[176:179], v[220:223], v[122:125]
	v_mfma_f32_16x16x32_bf16 v[94:97], v[134:137], v[224:227], v[94:97]
	v_mfma_f32_16x16x32_bf16 v[90:93], v[176:179], v[224:227], v[90:93]
	v_mfma_f32_16x16x32_bf16 v[62:65], v[134:137], v[236:239], v[62:65]
	v_mfma_f32_16x16x32_bf16 v[58:61], v[176:179], v[236:239], v[58:61]
	v_mfma_f32_16x16x32_bf16 v[30:33], v[134:137], v[240:243], v[30:33]
	v_mfma_f32_16x16x32_bf16 v[26:29], v[176:179], v[240:243], v[26:29]
	v_mfma_f32_16x16x32_bf16 v[110:113], v[192:195], v[212:215], v[110:113]
	v_mfma_f32_16x16x32_bf16 v[106:109], v[204:207], v[212:215], v[106:109]
	v_mfma_f32_16x16x32_bf16 v[78:81], v[192:195], v[216:219], v[78:81]
	v_mfma_f32_16x16x32_bf16 v[74:77], v[204:207], v[216:219], v[74:77]
	v_mfma_f32_16x16x32_bf16 v[46:49], v[192:195], v[228:231], v[46:49]
	v_mfma_f32_16x16x32_bf16 v[42:45], v[204:207], v[228:231], v[42:45]
	v_mfma_f32_16x16x32_bf16 v[14:17], v[192:195], v[232:235], v[14:17]
	v_mfma_f32_16x16x32_bf16 v[10:13], v[204:207], v[232:235], v[10:13]
	v_mfma_f32_16x16x32_bf16 v[110:113], v[200:203], v[220:223], v[110:113]
	v_mfma_f32_16x16x32_bf16 v[106:109], v[208:211], v[220:223], v[106:109]
	v_mfma_f32_16x16x32_bf16 v[78:81], v[200:203], v[224:227], v[78:81]
	v_mfma_f32_16x16x32_bf16 v[74:77], v[208:211], v[224:227], v[74:77]
	v_mfma_f32_16x16x32_bf16 v[46:49], v[200:203], v[236:239], v[46:49]
	v_mfma_f32_16x16x32_bf16 v[42:45], v[208:211], v[236:239], v[42:45]
	v_mfma_f32_16x16x32_bf16 v[14:17], v[200:203], v[240:243], v[14:17]
	v_mfma_f32_16x16x32_bf16 v[10:13], v[208:211], v[240:243], v[10:13]
	s_setprio 0
	s_barrier
	s_add_i32 s18, s70, s60
	v_lshl_add_u64 v[180:181], s[56:57], 0, v[138:139]
	s_mov_b32 m0, s18
	ds_read_b128 v[212:215], v189 offset:16384
	ds_read_b128 v[216:219], v189 offset:18432
	ds_read_b128 v[220:223], v190 offset:16384
	ds_read_b128 v[224:227], v190 offset:18432
	ds_read_b128 v[228:231], v189 offset:20480
	ds_read_b128 v[232:235], v189 offset:22528
	ds_read_b128 v[236:239], v190 offset:20480
	ds_read_b128 v[240:243], v190 offset:22528
	global_load_lds_dwordx4 v[180:181], off
	s_add_i32 m0, s18, 0x2000
	s_add_u32 s72, s56, 0x40000
	v_lshl_add_u64 v[196:197], s[56:57], 0, v[140:141]
	s_addc_u32 s73, s57, 0
	s_add_i32 s18, s92, s60
	global_load_lds_dwordx4 v[196:197], off
	v_lshl_add_u64 v[244:245], s[72:73], 0, v[138:139]
	s_mov_b32 m0, s18
	s_nop 0
	global_load_lds_dwordx4 v[244:245], off
	v_lshl_add_u64 v[244:245], s[72:73], 0, v[140:141]
	s_add_i32 m0, s18, 0x2000
	s_nop 0
	global_load_lds_dwordx4 v[244:245], off
	v_lshl_add_u64 v[244:245], s[58:59], 0, v[142:143]
	s_mov_b32 m0, s61
	s_nop 0
	global_load_lds_dwordx4 v[244:245], off
	v_lshl_add_u64 v[244:245], s[58:59], 0, v[144:145]
	s_mov_b32 m0, s64
	s_nop 0
	global_load_lds_dwordx4 v[244:245], off
	s_waitcnt vmcnt(8)
	s_waitcnt lgkmcnt(0)
	s_barrier
; #define PG8_STAGE(bufoff, gbase, voff) do { _Pragma("unroll") for (int _i = 0; _i < 2; ++_i) \
;         __builtin_amdgcn_global_load_lds((const unsigned*)((const char*)(gbase) + (voff)[_i]), (LAS unsigned*)(lds + (bufoff) + ldsw + _i * 8192), 16, 0, 0); } while (0)
; #define PG8_LDA(dst, b, h) do { _Pragma("unroll") for (int m = 0; m < 4; ++m) _Pragma("unroll") for (int k = 0; k < 2; ++k) dst[m][k] = *(const LAS bf16x8*)(lds + PG8_SA(b, h) + ((aoff ^ (k * 64)) + m * 2048)); } while (0)
; #define PG8_LDB(dst, b, h) do { _Pragma("unroll") for (int n = 0; n < 2; ++n) _Pragma("unroll") for (int k = 0; k < 2; ++k) dst[n][k] = *(const LAS bf16x8*)(lds + PG8_SB(b, h) + ((boff ^ (k * 64)) + n * 2048)); } while (0)
; #define PG8_MMA(ai, bj, At, Bt) do { __builtin_amdgcn_s_setprio(1); _Pragma("unroll") for (int m = 0; m < 4; ++m) _Pragma("unroll") for (int n = 0; n < 2; ++n) _Pragma("unroll") for (int k = 0; k < 2; ++k) \
;         acc[ai][bj][m][n] = __builtin_amdgcn_mfma_f32_16x16x32_bf16(Bt[n][k], At[m][k], acc[ai][bj][m][n], 0, 0, 0); __builtin_amdgcn_s_setprio(0); } while (0)
; #define PG8_WAIT_V(n) asm volatile("s_waitcnt vmcnt(" #n ")" ::: "memory")
; #define PG8_WAIT_L(n) asm volatile("s_waitcnt lgkmcnt(" #n ")" ::: "memory")
; #define PG8_BAR __builtin_amdgcn_s_barrier()
; #define PG8_SCHED __builtin_amdgcn_sched_barrier(0)
;     ...
;             PG8_WAIT_V(8); PG8_WAIT_L(0); PG8_BAR; if (do1) { PG8_MMA(1, 0, At, B0); PG8_MMA(1, 1, At, B1); } PG8_BAR; PG8_SCHED;
;             PG8_LDB(B0, 1, 0); PG8_LDB(B1, 1, 1); PG8_SCHED; PG8_LDA(At, 1, 0); PG8_STAGE(PG8_SA(0, 1), a2, vs[1]);
;             PG8_WAIT_V(8); PG8_WAIT_L(0); PG8_BAR; if (do0) { PG8_MMA(0, 0, At, B0); PG8_MMA(0, 1, At, B1); } PG8_BAR; PG8_SCHED;
	s_setprio 1
	s_waitcnt lgkmcnt(0)
	v_mfma_f32_16x16x32_bf16 v[118:121], v[130:133], v[212:215], v[118:121]
	v_mfma_f32_16x16x32_bf16 v[114:117], v[172:175], v[212:215], v[114:117]
	v_mfma_f32_16x16x32_bf16 v[86:89], v[130:133], v[216:219], v[86:89]
	v_mfma_f32_16x16x32_bf16 v[82:85], v[172:175], v[216:219], v[82:85]
	v_mfma_f32_16x16x32_bf16 v[54:57], v[130:133], v[228:231], v[54:57]
	v_mfma_f32_16x16x32_bf16 v[50:53], v[172:175], v[228:231], v[50:53]
	v_mfma_f32_16x16x32_bf16 v[22:25], v[130:133], v[232:235], v[22:25]
	v_mfma_f32_16x16x32_bf16 v[18:21], v[172:175], v[232:235], v[18:21]
	v_mfma_f32_16x16x32_bf16 v[118:121], v[134:137], v[220:223], v[118:121]
	v_mfma_f32_16x16x32_bf16 v[114:117], v[176:179], v[220:223], v[114:117]
	v_mfma_f32_16x16x32_bf16 v[86:89], v[134:137], v[224:227], v[86:89]
	v_mfma_f32_16x16x32_bf16 v[82:85], v[176:179], v[224:227], v[82:85]
	v_mfma_f32_16x16x32_bf16 v[54:57], v[134:137], v[236:239], v[54:57]
	v_mfma_f32_16x16x32_bf16 v[50:53], v[176:179], v[236:239], v[50:53]
	v_mfma_f32_16x16x32_bf16 v[22:25], v[134:137], v[240:243], v[22:25]
	v_mfma_f32_16x16x32_bf16 v[18:21], v[176:179], v[240:243], v[18:21]
	v_mfma_f32_16x16x32_bf16 v[102:105], v[192:195], v[212:215], v[102:105]
	v_mfma_f32_16x16x32_bf16 v[98:101], v[204:207], v[212:215], v[98:101]
	v_mfma_f32_16x16x32_bf16 v[70:73], v[192:195], v[216:219], v[70:73]
	v_mfma_f32_16x16x32_bf16 v[66:69], v[204:207], v[216:219], v[66:69]
	v_mfma_f32_16x16x32_bf16 v[38:41], v[192:195], v[228:231], v[38:41]
	v_mfma_f32_16x16x32_bf16 v[34:37], v[204:207], v[228:231], v[34:37]
	v_mfma_f32_16x16x32_bf16 v[6:9], v[192:195], v[232:235], v[6:9]
	v_mfma_f32_16x16x32_bf16 v[2:5], v[204:207], v[232:235], v[2:5]
	v_mfma_f32_16x16x32_bf16 v[102:105], v[200:203], v[220:223], v[102:105]
	v_mfma_f32_16x16x32_bf16 v[98:101], v[208:211], v[220:223], v[98:101]
	v_mfma_f32_16x16x32_bf16 v[70:73], v[200:203], v[224:227], v[70:73]
	v_mfma_f32_16x16x32_bf16 v[66:69], v[208:211], v[224:227], v[66:69]
	v_mfma_f32_16x16x32_bf16 v[38:41], v[200:203], v[236:239], v[38:41]
	v_mfma_f32_16x16x32_bf16 v[34:37], v[208:211], v[236:239], v[34:37]
	v_mfma_f32_16x16x32_bf16 v[6:9], v[200:203], v[240:243], v[6:9]
	v_mfma_f32_16x16x32_bf16 v[2:5], v[208:211], v[240:243], v[2:5]
	s_setprio 0
	s_barrier
	s_add_i32 s18, 0, 0x18000
	v_add_u32_e32 v130, s18, v153
	v_add_u32_e32 v134, s18, v184
	v_add_u32_e32 v150, s12, v153
	v_add_u32_e32 v176, s12, v184
	s_add_i32 s19, 0, 0x1c000
	ds_read_b128 v[130:133], v130
	ds_read_b128 v[134:137], v134
	ds_read_b128 v[172:175], v150
	ds_read_b128 v[176:179], v176
	v_add_u32_e32 v150, s19, v153
	v_add_u32_e32 v191, s19, v184
	ds_read_b128 v[192:195], v150
	ds_read_b128 v[200:203], v191
	v_add_u32_e32 v150, s13, v153
	v_add_u32_e32 v191, s13, v184
	ds_read_b128 v[204:207], v150
	ds_read_b128 v[208:211], v191
	s_mov_b32 m0, s65
	v_lshl_add_u64 v[244:245], s[58:59], 0, v[146:147]
	ds_read_b128 v[212:215], v189 offset:32768
	ds_read_b128 v[216:219], v189 offset:34816
	ds_read_b128 v[220:223], v190 offset:32768
	ds_read_b128 v[224:227], v190 offset:34816
	ds_read_b128 v[228:231], v189 offset:36864
	ds_read_b128 v[232:235], v189 offset:38912
	ds_read_b128 v[236:239], v190 offset:36864
	ds_read_b128 v[240:243], v190 offset:38912
	global_load_lds_dwordx4 v[244:245], off
	v_lshl_add_u64 v[244:245], s[58:59], 0, v[148:149]
	s_mov_b32 m0, s66
	s_nop 0
	global_load_lds_dwordx4 v[244:245], off
	s_waitcnt vmcnt(8)
	s_waitcnt lgkmcnt(0)
	s_barrier
	s_setprio 1
	s_waitcnt lgkmcnt(0)
	v_mfma_f32_16x16x32_bf16 v[126:129], v[130:133], v[212:215], v[126:129]
	v_mfma_f32_16x16x32_bf16 v[122:125], v[172:175], v[212:215], v[122:125]
	v_mfma_f32_16x16x32_bf16 v[94:97], v[130:133], v[216:219], v[94:97]
	v_mfma_f32_16x16x32_bf16 v[90:93], v[172:175], v[216:219], v[90:93]
	v_mfma_f32_16x16x32_bf16 v[62:65], v[130:133], v[228:231], v[62:65]
	v_mfma_f32_16x16x32_bf16 v[58:61], v[172:175], v[228:231], v[58:61]
	v_mfma_f32_16x16x32_bf16 v[30:33], v[130:133], v[232:235], v[30:33]
	v_mfma_f32_16x16x32_bf16 v[26:29], v[172:175], v[232:235], v[26:29]
	v_mfma_f32_16x16x32_bf16 v[126:129], v[134:137], v[220:223], v[126:129]
	v_mfma_f32_16x16x32_bf16 v[122:125], v[176:179], v[220:223], v[122:125]
	v_mfma_f32_16x16x32_bf16 v[94:97], v[134:137], v[224:227], v[94:97]
	v_mfma_f32_16x16x32_bf16 v[90:93], v[176:179], v[224:227], v[90:93]
	v_mfma_f32_16x16x32_bf16 v[62:65], v[134:137], v[236:239], v[62:65]
	v_mfma_f32_16x16x32_bf16 v[58:61], v[176:179], v[236:239], v[58:61]
	v_mfma_f32_16x16x32_bf16 v[30:33], v[134:137], v[240:243], v[30:33]
	v_mfma_f32_16x16x32_bf16 v[26:29], v[176:179], v[240:243], v[26:29]
	v_mfma_f32_16x16x32_bf16 v[110:113], v[192:195], v[212:215], v[110:113]
	v_mfma_f32_16x16x32_bf16 v[106:109], v[204:207], v[212:215], v[106:109]
	v_mfma_f32_16x16x32_bf16 v[78:81], v[192:195], v[216:219], v[78:81]
	v_mfma_f32_16x16x32_bf16 v[74:77], v[204:207], v[216:219], v[74:77]
	v_mfma_f32_16x16x32_bf16 v[46:49], v[192:195], v[228:231], v[46:49]
	v_mfma_f32_16x16x32_bf16 v[42:45], v[204:207], v[228:231], v[42:45]
	v_mfma_f32_16x16x32_bf16 v[14:17], v[192:195], v[232:235], v[14:17]
	v_mfma_f32_16x16x32_bf16 v[10:13], v[204:207], v[232:235], v[10:13]
	v_mfma_f32_16x16x32_bf16 v[110:113], v[200:203], v[220:223], v[110:113]
	v_mfma_f32_16x16x32_bf16 v[106:109], v[208:211], v[220:223], v[106:109]
	v_mfma_f32_16x16x32_bf16 v[78:81], v[200:203], v[224:227], v[78:81]
	v_mfma_f32_16x16x32_bf16 v[74:77], v[208:211], v[224:227], v[74:77]
	v_mfma_f32_16x16x32_bf16 v[46:49], v[200:203], v[236:239], v[46:49]
	v_mfma_f32_16x16x32_bf16 v[42:45], v[208:211], v[236:239], v[42:45]
	v_mfma_f32_16x16x32_bf16 v[14:17], v[200:203], v[240:243], v[14:17]
	v_mfma_f32_16x16x32_bf16 v[10:13], v[208:211], v[240:243], v[10:13]
	s_setprio 0
	s_barrier
; #define PG8_STAGE(bufoff, gbase, voff) do { _Pragma("unroll") for (int _i = 0; _i < 2; ++_i) \
;         __builtin_amdgcn_global_load_lds((const unsigned*)((const char*)(gbase) + (voff)[_i]), (LAS unsigned*)(lds + (bufoff) + ldsw + _i * 8192), 16, 0, 0); } while (0)
; #define PG8_LDA(dst, b, h) do { _Pragma("unroll") for (int m = 0; m < 4; ++m) _Pragma("unroll") for (int k = 0; k < 2; ++k) dst[m][k] = *(const LAS bf16x8*)(lds + PG8_SA(b, h) + ((aoff ^ (k * 64)) + m * 2048)); } while (0)
; #define PG8_MMA(ai, bj, At, Bt) do { __builtin_amdgcn_s_setprio(1); _Pragma("unroll") for (int m = 0; m < 4; ++m) _Pragma("unroll") for (int n = 0; n < 2; ++n) _Pragma("unroll") for (int k = 0; k < 2; ++k) \
;         acc[ai][bj][m][n] = __builtin_amdgcn_mfma_f32_16x16x32_bf16(Bt[n][k], At[m][k], acc[ai][bj][m][n], 0, 0, 0); __builtin_amdgcn_s_setprio(0); } while (0)
; #define PG8_WAIT_V(n) asm volatile("s_waitcnt vmcnt(" #n ")" ::: "memory")
; #define PG8_WAIT_L(n) asm volatile("s_waitcnt lgkmcnt(" #n ")" ::: "memory")
; #define PG8_BAR __builtin_amdgcn_s_barrier()
; #define PG8_SCHED __builtin_amdgcn_sched_barrier(0)
;     ...
;             PG8_LDA(At, 1, 1); PG8_STAGE(PG8_SB(1, 0), b3, voffB); PG8_STAGE(PG8_SB(1, 1), b3 + hstep, voffB); PG8_STAGE(PG8_SA(1, 0), a3, vs[0]);
;             PG8_WAIT_V(8); PG8_WAIT_L(0); PG8_BAR; if (do1) { PG8_MMA(1, 0, At, B0); PG8_MMA(1, 1, At, B1); } PG8_BAR; PG8_SCHED;
;         }
;         if (wr == 0) PG8_BAR;
	s_add_i32 s18, s18, s60
	v_lshl_add_u64 v[180:181], v[180:181], 0, s[24:25]
	s_mov_b32 m0, s18
	ds_read_b128 v[212:215], v189 offset:49152
	ds_read_b128 v[216:219], v189 offset:51200
	ds_read_b128 v[220:223], v190 offset:49152
	ds_read_b128 v[224:227], v190 offset:51200
	ds_read_b128 v[228:231], v189 offset:53248
	ds_read_b128 v[232:235], v189 offset:55296
	ds_read_b128 v[236:239], v190 offset:53248
	ds_read_b128 v[240:243], v190 offset:55296
	global_load_lds_dwordx4 v[180:181], off
	s_add_i32 m0, s18, 0x2000
	s_add_u32 s56, s56, 0x40080
	v_lshl_add_u64 v[180:181], v[196:197], 0, s[24:25]
	s_addc_u32 s57, s57, 0
	s_add_i32 s18, s19, s60
	global_load_lds_dwordx4 v[180:181], off
	v_lshl_add_u64 v[180:181], s[56:57], 0, v[138:139]
	s_mov_b32 m0, s18
	s_nop 0
	global_load_lds_dwordx4 v[180:181], off
	v_lshl_add_u64 v[180:181], s[56:57], 0, v[140:141]
	s_add_i32 m0, s18, 0x2000
	s_nop 0
	global_load_lds_dwordx4 v[180:181], off
	v_lshl_add_u64 v[180:181], s[6:7], 0, v[142:143]
	s_mov_b32 m0, s68
	s_nop 0
	global_load_lds_dwordx4 v[180:181], off
	v_lshl_add_u64 v[180:181], s[6:7], 0, v[144:145]
	s_mov_b32 m0, s69
	s_nop 0
	global_load_lds_dwordx4 v[180:181], off
	s_waitcnt vmcnt(8)
	s_waitcnt lgkmcnt(0)
	s_barrier
	s_setprio 1
	s_waitcnt lgkmcnt(0)
	v_mfma_f32_16x16x32_bf16 v[118:121], v[130:133], v[212:215], v[118:121]
	v_mfma_f32_16x16x32_bf16 v[114:117], v[172:175], v[212:215], v[114:117]
	v_mfma_f32_16x16x32_bf16 v[86:89], v[130:133], v[216:219], v[86:89]
	v_mfma_f32_16x16x32_bf16 v[82:85], v[172:175], v[216:219], v[82:85]
	v_mfma_f32_16x16x32_bf16 v[54:57], v[130:133], v[228:231], v[54:57]
	v_mfma_f32_16x16x32_bf16 v[50:53], v[172:175], v[228:231], v[50:53]
	v_mfma_f32_16x16x32_bf16 v[22:25], v[130:133], v[232:235], v[22:25]
	v_mfma_f32_16x16x32_bf16 v[18:21], v[172:175], v[232:235], v[18:21]
	v_mfma_f32_16x16x32_bf16 v[118:121], v[134:137], v[220:223], v[118:121]
	v_mfma_f32_16x16x32_bf16 v[114:117], v[176:179], v[220:223], v[114:117]
	v_mfma_f32_16x16x32_bf16 v[86:89], v[134:137], v[224:227], v[86:89]
	v_mfma_f32_16x16x32_bf16 v[82:85], v[176:179], v[224:227], v[82:85]
	v_mfma_f32_16x16x32_bf16 v[54:57], v[134:137], v[236:239], v[54:57]
	v_mfma_f32_16x16x32_bf16 v[50:53], v[176:179], v[236:239], v[50:53]
	v_mfma_f32_16x16x32_bf16 v[22:25], v[134:137], v[240:243], v[22:25]
	v_mfma_f32_16x16x32_bf16 v[18:21], v[176:179], v[240:243], v[18:21]
	v_mfma_f32_16x16x32_bf16 v[102:105], v[192:195], v[212:215], v[102:105]
	v_mfma_f32_16x16x32_bf16 v[98:101], v[204:207], v[212:215], v[98:101]
	v_mfma_f32_16x16x32_bf16 v[70:73], v[192:195], v[216:219], v[70:73]
	v_mfma_f32_16x16x32_bf16 v[66:69], v[204:207], v[216:219], v[66:69]
	v_mfma_f32_16x16x32_bf16 v[38:41], v[192:195], v[228:231], v[38:41]
	v_mfma_f32_16x16x32_bf16 v[34:37], v[204:207], v[228:231], v[34:37]
	v_mfma_f32_16x16x32_bf16 v[6:9], v[192:195], v[232:235], v[6:9]
	v_mfma_f32_16x16x32_bf16 v[2:5], v[204:207], v[232:235], v[2:5]
	v_mfma_f32_16x16x32_bf16 v[102:105], v[200:203], v[220:223], v[102:105]
	v_mfma_f32_16x16x32_bf16 v[98:101], v[208:211], v[220:223], v[98:101]
	v_mfma_f32_16x16x32_bf16 v[70:73], v[200:203], v[224:227], v[70:73]
	v_mfma_f32_16x16x32_bf16 v[66:69], v[208:211], v[224:227], v[66:69]
	v_mfma_f32_16x16x32_bf16 v[38:41], v[200:203], v[236:239], v[38:41]
	v_mfma_f32_16x16x32_bf16 v[34:37], v[208:211], v[236:239], v[34:37]
	v_mfma_f32_16x16x32_bf16 v[6:9], v[200:203], v[240:243], v[6:9]
	v_mfma_f32_16x16x32_bf16 v[2:5], v[208:211], v[240:243], v[2:5]
	s_setprio 0
	s_barrier
	s_add_i32 s63, s63, 2
	s_add_u32 s49, s49, 0x100
	s_addc_u32 s62, s62, 0
	s_add_u32 s0, s0, 0x8000
	s_addc_u32 s1, s1, 0
	s_cmp_gt_u32 s63, 13
	s_cbranch_scc0 .LBB0_1498
	s_and_b64 vcc, exec, s[26:27]
	s_cbranch_vccz .LBB0_1502
	s_barrier
	s_cmp_gt_i32 s8, 7
	s_mov_b64 s[0:1], -1
	s_cbranch_scc1 .LBB0_1503

; #define PG8_STAGE(bufoff, gbase, voff) do { _Pragma("unroll") for (int _i = 0; _i < 2; ++_i) \
;         __builtin_amdgcn_global_load_lds((const unsigned*)((const char*)(gbase) + (voff)[_i]), (LAS unsigned*)(lds + (bufoff) + ldsw + _i * 8192), 16, 0, 0); } while (0)
; #define PG8_LDA(dst, b, h) do { _Pragma("unroll") for (int m = 0; m < 4; ++m) _Pragma("unroll") for (int k = 0; k < 2; ++k) dst[m][k] = *(const LAS bf16x8*)(lds + PG8_SA(b, h) + ((aoff ^ (k * 64)) + m * 2048)); } while (0)
; #define PG8_LDB(dst, b, h) do { _Pragma("unroll") for (int n = 0; n < 2; ++n) _Pragma("unroll") for (int k = 0; k < 2; ++k) dst[n][k] = *(const LAS bf16x8*)(lds + PG8_SB(b, h) + ((boff ^ (k * 64)) + n * 2048)); } while (0)
; #define PG8_WAIT_V(n) asm volatile("s_waitcnt vmcnt(" #n ")" ::: "memory")
; #define PG8_WAIT_L(n) asm volatile("s_waitcnt lgkmcnt(" #n ")" ::: "memory")
;     ...
;             const bool last = (t == nt - 2);
;             const char* a1 = cA + (size_t)(t + 1) * kstepA;
;             const char* a2 = last ? nA : cA + (size_t)(t + 2) * kstepA; const char* b2 = last ? nB : cB + (size_t)(t + 2) * kstepB;
;             const char* a3 = a2 + kstepA; const char* b3 = b2 + kstepB;
;             unsigned vs[2][2];
;             if constexpr (GATHER) {
;                 if (last && has_next) {
; #pragma unroll
;                     for (int hh = 0; hh < 2; ++hh)
; #pragma unroll
;                         for (int i = 0; i < 2; ++i) voffN[hh][i] = (unsigned)idxl[(ui + 1) * 256 + hh * HALF + sR[i]] * (unsigned)(K * 2) + (unsigned)sC[i] * 2u;
;                 }
; #pragma unroll
;                 for (int hh = 0; hh < 2; ++hh)
; #pragma unroll
;                     for (int i = 0; i < 2; ++i) vs[hh][i] = last ? voffN[hh][i] : voffA[hh][i];
;             } else {
; #pragma unroll
;                 for (int hh = 0; hh < 2; ++hh)
; #pragma unroll
;                     for (int i = 0; i < 2; ++i) vs[hh][i] = voffA[hh][i];
;             }
;             PG8_LDB(B0, 0, 0); PG8_LDB(B1, 0, 1); PG8_SCHED; PG8_LDA(At, 0, 0); PG8_STAGE(PG8_SA(1, 1), a1, voffA[1]);
;             PG8_WAIT_V(8); PG8_WAIT_L(0); PG8_BAR; if (do0) { PG8_MMA(0, 0, At, B0); PG8_MMA(0, 1, At, B1); } PG8_BAR; PG8_SCHED;
;             PG8_LDA(At, 0, 1); PG8_STAGE(PG8_SB(0, 0), b2, voffB); PG8_STAGE(PG8_SB(0, 1), b2 + hstep, voffB); PG8_STAGE(PG8_SA(0, 0), a2, vs[0]);
.LBB0_1659:
	ds_read_b128 v[146:149], v218
	ds_read_b128 v[150:153], v219
	ds_read_b128 v[154:157], v220
	ds_read_b128 v[158:161], v221
	ds_read_b128 v[130:133], v222
	ds_read_b128 v[134:137], v223
	ds_read_b128 v[138:141], v224
	ds_read_b128 v[142:145], v225
	s_mov_b32 m0, s54
	v_lshl_add_u64 v[212:213], s[90:91], 0, v[208:209]
	s_waitcnt lgkmcnt(0)
	ds_read_b128 v[186:189], v226
	ds_read_b128 v[174:177], v226 offset:2048
	ds_read_b128 v[190:193], v227
	ds_read_b128 v[178:181], v227 offset:2048
	ds_read_b128 v[170:173], v226 offset:4096
	ds_read_b128 v[162:165], v226 offset:6144
	ds_read_b128 v[182:185], v227 offset:4096
	ds_read_b128 v[166:169], v227 offset:6144
	global_load_lds_dwordx4 v[212:213], off
	v_lshl_add_u64 v[212:213], s[90:91], 0, v[210:211]
	s_mov_b32 m0, s55
	s_and_b64 vcc, exec, s[0:1]
	global_load_lds_dwordx4 v[212:213], off
	s_waitcnt vmcnt(8)
	s_waitcnt lgkmcnt(0)
	s_barrier
	s_cbranch_vccnz .LBB0_1661
	s_setprio 1
	s_waitcnt lgkmcnt(0)
	v_mfma_f32_16x16x32_bf16 v[114:117], v[146:149], v[186:189], v[114:117]
	v_mfma_f32_16x16x32_bf16 v[118:121], v[154:157], v[186:189], v[118:121]
	v_mfma_f32_16x16x32_bf16 v[82:85], v[146:149], v[174:177], v[82:85]
	v_mfma_f32_16x16x32_bf16 v[86:89], v[154:157], v[174:177], v[86:89]
	v_mfma_f32_16x16x32_bf16 v[50:53], v[146:149], v[170:173], v[50:53]
	v_mfma_f32_16x16x32_bf16 v[54:57], v[154:157], v[170:173], v[54:57]
	v_mfma_f32_16x16x32_bf16 v[18:21], v[146:149], v[162:165], v[18:21]
	v_mfma_f32_16x16x32_bf16 v[22:25], v[154:157], v[162:165], v[22:25]
	v_mfma_f32_16x16x32_bf16 v[114:117], v[150:153], v[190:193], v[114:117]
	v_mfma_f32_16x16x32_bf16 v[118:121], v[158:161], v[190:193], v[118:121]
	v_mfma_f32_16x16x32_bf16 v[82:85], v[150:153], v[178:181], v[82:85]
	v_mfma_f32_16x16x32_bf16 v[86:89], v[158:161], v[178:181], v[86:89]
	v_mfma_f32_16x16x32_bf16 v[50:53], v[150:153], v[182:185], v[50:53]
	v_mfma_f32_16x16x32_bf16 v[54:57], v[158:161], v[182:185], v[54:57]
	v_mfma_f32_16x16x32_bf16 v[18:21], v[150:153], v[166:169], v[18:21]
	v_mfma_f32_16x16x32_bf16 v[22:25], v[158:161], v[166:169], v[22:25]
	v_mfma_f32_16x16x32_bf16 v[98:101], v[130:133], v[186:189], v[98:101]
	v_mfma_f32_16x16x32_bf16 v[102:105], v[138:141], v[186:189], v[102:105]
	v_mfma_f32_16x16x32_bf16 v[66:69], v[130:133], v[174:177], v[66:69]
	v_mfma_f32_16x16x32_bf16 v[70:73], v[138:141], v[174:177], v[70:73]
	v_mfma_f32_16x16x32_bf16 v[34:37], v[130:133], v[170:173], v[34:37]
	v_mfma_f32_16x16x32_bf16 v[38:41], v[138:141], v[170:173], v[38:41]
	v_mfma_f32_16x16x32_bf16 v[6:9], v[130:133], v[162:165], v[6:9]
	v_mfma_f32_16x16x32_bf16 v[10:13], v[138:141], v[162:165], v[10:13]
	v_mfma_f32_16x16x32_bf16 v[98:101], v[134:137], v[190:193], v[98:101]
	v_mfma_f32_16x16x32_bf16 v[102:105], v[142:145], v[190:193], v[102:105]
	v_mfma_f32_16x16x32_bf16 v[66:69], v[134:137], v[178:181], v[66:69]
	v_mfma_f32_16x16x32_bf16 v[70:73], v[142:145], v[178:181], v[70:73]
	v_mfma_f32_16x16x32_bf16 v[34:37], v[134:137], v[182:185], v[34:37]
	v_mfma_f32_16x16x32_bf16 v[38:41], v[142:145], v[182:185], v[38:41]
	v_mfma_f32_16x16x32_bf16 v[6:9], v[134:137], v[166:169], v[6:9]
	v_mfma_f32_16x16x32_bf16 v[10:13], v[142:145], v[166:169], v[10:13]
	s_setprio 0
.LBB0_1661:
	s_add_u32 s6, s90, s51
	s_addc_u32 s7, s91, s52
	s_add_u32 s18, s90, s50
	s_addc_u32 s19, s91, s41
	s_cmp_eq_u32 s53, 12
	s_cselect_b32 s27, s13, s7
	s_cselect_b32 s26, s12, s6
	s_cselect_b32 s25, s11, s19
	s_cselect_b32 s24, s10, s18
	s_barrier
	s_mov_b32 m0, s34
	v_lshl_add_u64 v[212:213], s[24:25], 0, v[196:197]
	s_add_u32 s6, s24, 0x40000
	s_waitcnt lgkmcnt(0)
	ds_read_b128 v[186:189], v226 offset:16384
	ds_read_b128 v[174:177], v226 offset:18432
	ds_read_b128 v[190:193], v227 offset:16384
	ds_read_b128 v[178:181], v227 offset:18432
	ds_read_b128 v[170:173], v226 offset:20480
	ds_read_b128 v[162:165], v226 offset:22528
	ds_read_b128 v[182:185], v227 offset:20480
	ds_read_b128 v[166:169], v227 offset:22528
	global_load_lds_dwordx4 v[212:213], off
	v_lshl_add_u64 v[214:215], s[24:25], 0, v[194:195]
	s_mov_b32 m0, s35
	s_addc_u32 s7, s25, 0
	global_load_lds_dwordx4 v[214:215], off
	v_lshl_add_u64 v[228:229], s[6:7], 0, v[196:197]
	s_mov_b32 m0, s36
	s_andn2_b64 vcc, exec, s[2:3]
	global_load_lds_dwordx4 v[228:229], off
	v_lshl_add_u64 v[228:229], s[6:7], 0, v[194:195]
	s_mov_b32 m0, s37
	s_nop 0
	global_load_lds_dwordx4 v[228:229], off
	v_lshl_add_u64 v[228:229], s[26:27], 0, v[200:201]
	s_mov_b32 m0, s31
	s_nop 0
	global_load_lds_dwordx4 v[228:229], off
	v_lshl_add_u64 v[228:229], s[26:27], 0, v[202:203]
	s_mov_b32 m0, s38
	s_nop 0
	global_load_lds_dwordx4 v[228:229], off
	s_waitcnt vmcnt(8)
	s_waitcnt lgkmcnt(0)
	v_cndmask_b32_e64 v228, 0, 1, s[2:3]
	v_cmp_ne_u32_e64 s[6:7], 1, v228
	s_barrier
	s_cbranch_vccnz .LBB0_1663
; #define PG8_STAGE(bufoff, gbase, voff) do { _Pragma("unroll") for (int _i = 0; _i < 2; ++_i) \
;         __builtin_amdgcn_global_load_lds((const unsigned*)((const char*)(gbase) + (voff)[_i]), (LAS unsigned*)(lds + (bufoff) + ldsw + _i * 8192), 16, 0, 0); } while (0)
; #define PG8_LDA(dst, b, h) do { _Pragma("unroll") for (int m = 0; m < 4; ++m) _Pragma("unroll") for (int k = 0; k < 2; ++k) dst[m][k] = *(const LAS bf16x8*)(lds + PG8_SA(b, h) + ((aoff ^ (k * 64)) + m * 2048)); } while (0)
; #define PG8_LDB(dst, b, h) do { _Pragma("unroll") for (int n = 0; n < 2; ++n) _Pragma("unroll") for (int k = 0; k < 2; ++k) dst[n][k] = *(const LAS bf16x8*)(lds + PG8_SB(b, h) + ((boff ^ (k * 64)) + n * 2048)); } while (0)
; #define PG8_MMA(ai, bj, At, Bt) do { __builtin_amdgcn_s_setprio(1); _Pragma("unroll") for (int m = 0; m < 4; ++m) _Pragma("unroll") for (int n = 0; n < 2; ++n) _Pragma("unroll") for (int k = 0; k < 2; ++k) \
;         acc[ai][bj][m][n] = __builtin_amdgcn_mfma_f32_16x16x32_bf16(Bt[n][k], At[m][k], acc[ai][bj][m][n], 0, 0, 0); __builtin_amdgcn_s_setprio(0); } while (0)
; #define PG8_WAIT_V(n) asm volatile("s_waitcnt vmcnt(" #n ")" ::: "memory")
; #define PG8_WAIT_L(n) asm volatile("s_waitcnt lgkmcnt(" #n ")" ::: "memory")
; #define PG8_BAR __builtin_amdgcn_s_barrier()
; #define PG8_SCHED __builtin_amdgcn_sched_barrier(0)
;     ...
;             PG8_WAIT_V(8); PG8_WAIT_L(0); PG8_BAR; if (do1) { PG8_MMA(1, 0, At, B0); PG8_MMA(1, 1, At, B1); } PG8_BAR; PG8_SCHED;
;             PG8_LDB(B0, 1, 0); PG8_LDB(B1, 1, 1); PG8_SCHED; PG8_LDA(At, 1, 0); PG8_STAGE(PG8_SA(0, 1), a2, vs[1]);
;             PG8_WAIT_V(8); PG8_WAIT_L(0); PG8_BAR; if (do0) { PG8_MMA(0, 0, At, B0); PG8_MMA(0, 1, At, B1); } PG8_BAR; PG8_SCHED;
	s_setprio 1
	s_waitcnt lgkmcnt(0)
	v_mfma_f32_16x16x32_bf16 v[126:129], v[146:149], v[186:189], v[126:129]
	v_mfma_f32_16x16x32_bf16 v[122:125], v[154:157], v[186:189], v[122:125]
	v_mfma_f32_16x16x32_bf16 v[94:97], v[146:149], v[174:177], v[94:97]
	v_mfma_f32_16x16x32_bf16 v[90:93], v[154:157], v[174:177], v[90:93]
	v_mfma_f32_16x16x32_bf16 v[62:65], v[146:149], v[170:173], v[62:65]
	v_mfma_f32_16x16x32_bf16 v[58:61], v[154:157], v[170:173], v[58:61]
	v_mfma_f32_16x16x32_bf16 v[30:33], v[146:149], v[162:165], v[30:33]
	v_mfma_f32_16x16x32_bf16 v[26:29], v[154:157], v[162:165], v[26:29]
	v_mfma_f32_16x16x32_bf16 v[126:129], v[150:153], v[190:193], v[126:129]
	v_mfma_f32_16x16x32_bf16 v[122:125], v[158:161], v[190:193], v[122:125]
	v_mfma_f32_16x16x32_bf16 v[94:97], v[150:153], v[178:181], v[94:97]
	v_mfma_f32_16x16x32_bf16 v[90:93], v[158:161], v[178:181], v[90:93]
	v_mfma_f32_16x16x32_bf16 v[62:65], v[150:153], v[182:185], v[62:65]
	v_mfma_f32_16x16x32_bf16 v[58:61], v[158:161], v[182:185], v[58:61]
	v_mfma_f32_16x16x32_bf16 v[30:33], v[150:153], v[166:169], v[30:33]
	v_mfma_f32_16x16x32_bf16 v[26:29], v[158:161], v[166:169], v[26:29]
	v_mfma_f32_16x16x32_bf16 v[110:113], v[130:133], v[186:189], v[110:113]
	v_mfma_f32_16x16x32_bf16 v[106:109], v[138:141], v[186:189], v[106:109]
	v_mfma_f32_16x16x32_bf16 v[78:81], v[130:133], v[174:177], v[78:81]
	v_mfma_f32_16x16x32_bf16 v[74:77], v[138:141], v[174:177], v[74:77]
	v_mfma_f32_16x16x32_bf16 v[46:49], v[130:133], v[170:173], v[46:49]
	v_mfma_f32_16x16x32_bf16 v[42:45], v[138:141], v[170:173], v[42:45]
	v_mfma_f32_16x16x32_bf16 v[14:17], v[130:133], v[162:165], v[14:17]
	v_mfma_f32_16x16x32_bf16 v[2:5], v[138:141], v[162:165], v[2:5]
	v_mfma_f32_16x16x32_bf16 v[110:113], v[134:137], v[190:193], v[110:113]
	v_mfma_f32_16x16x32_bf16 v[106:109], v[142:145], v[190:193], v[106:109]
	v_mfma_f32_16x16x32_bf16 v[78:81], v[134:137], v[178:181], v[78:81]
	v_mfma_f32_16x16x32_bf16 v[74:77], v[142:145], v[178:181], v[74:77]
	v_mfma_f32_16x16x32_bf16 v[46:49], v[134:137], v[182:185], v[46:49]
	v_mfma_f32_16x16x32_bf16 v[42:45], v[142:145], v[182:185], v[42:45]
	v_mfma_f32_16x16x32_bf16 v[14:17], v[134:137], v[166:169], v[14:17]
	v_mfma_f32_16x16x32_bf16 v[2:5], v[142:145], v[166:169], v[2:5]
	s_setprio 0
.LBB0_1663:
	s_barrier
	v_add_u32_e32 v130, s58, v216
	v_add_u32_e32 v131, s58, v217
	ds_read_b128 v[146:149], v130
	ds_read_b128 v[150:153], v131
	v_add_u32_e32 v130, s56, v216
	v_add_u32_e32 v131, s56, v217
	ds_read_b128 v[154:157], v130
	ds_read_b128 v[158:161], v131
	v_add_u32_e32 v130, s59, v216
	v_add_u32_e32 v134, s59, v217
	v_add_u32_e32 v138, s57, v216
	v_add_u32_e32 v142, s57, v217
	ds_read_b128 v[130:133], v130
	ds_read_b128 v[134:137], v134
	ds_read_b128 v[138:141], v138
	ds_read_b128 v[142:145], v142
	s_mov_b32 m0, s39
	v_lshl_add_u64 v[228:229], s[26:27], 0, v[204:205]
	s_waitcnt lgkmcnt(0)
	ds_read_b128 v[186:189], v226 offset:32768
	ds_read_b128 v[174:177], v226 offset:34816
	ds_read_b128 v[190:193], v227 offset:32768
	ds_read_b128 v[178:181], v227 offset:34816
	ds_read_b128 v[170:173], v226 offset:36864
	ds_read_b128 v[162:165], v226 offset:38912
	ds_read_b128 v[182:185], v227 offset:36864
	ds_read_b128 v[166:169], v227 offset:38912
	global_load_lds_dwordx4 v[228:229], off
	v_lshl_add_u64 v[228:229], s[26:27], 0, v[206:207]
	s_mov_b32 m0, s40
	s_and_b64 vcc, exec, s[0:1]
	global_load_lds_dwordx4 v[228:229], off
	s_waitcnt vmcnt(8)
	s_waitcnt lgkmcnt(0)
	s_barrier
	s_cbranch_vccnz .LBB0_1665
	s_setprio 1
	s_waitcnt lgkmcnt(0)
	v_mfma_f32_16x16x32_bf16 v[114:117], v[146:149], v[186:189], v[114:117]
	v_mfma_f32_16x16x32_bf16 v[118:121], v[154:157], v[186:189], v[118:121]
	v_mfma_f32_16x16x32_bf16 v[82:85], v[146:149], v[174:177], v[82:85]
	v_mfma_f32_16x16x32_bf16 v[86:89], v[154:157], v[174:177], v[86:89]
	v_mfma_f32_16x16x32_bf16 v[50:53], v[146:149], v[170:173], v[50:53]
	v_mfma_f32_16x16x32_bf16 v[54:57], v[154:157], v[170:173], v[54:57]
	v_mfma_f32_16x16x32_bf16 v[18:21], v[146:149], v[162:165], v[18:21]
	v_mfma_f32_16x16x32_bf16 v[22:25], v[154:157], v[162:165], v[22:25]
	v_mfma_f32_16x16x32_bf16 v[114:117], v[150:153], v[190:193], v[114:117]
	v_mfma_f32_16x16x32_bf16 v[118:121], v[158:161], v[190:193], v[118:121]
	v_mfma_f32_16x16x32_bf16 v[82:85], v[150:153], v[178:181], v[82:85]
	v_mfma_f32_16x16x32_bf16 v[86:89], v[158:161], v[178:181], v[86:89]
	v_mfma_f32_16x16x32_bf16 v[50:53], v[150:153], v[182:185], v[50:53]
	v_mfma_f32_16x16x32_bf16 v[54:57], v[158:161], v[182:185], v[54:57]
	v_mfma_f32_16x16x32_bf16 v[18:21], v[150:153], v[166:169], v[18:21]
	v_mfma_f32_16x16x32_bf16 v[22:25], v[158:161], v[166:169], v[22:25]
	v_mfma_f32_16x16x32_bf16 v[98:101], v[130:133], v[186:189], v[98:101]
	v_mfma_f32_16x16x32_bf16 v[102:105], v[138:141], v[186:189], v[102:105]
	v_mfma_f32_16x16x32_bf16 v[66:69], v[130:133], v[174:177], v[66:69]
	v_mfma_f32_16x16x32_bf16 v[70:73], v[138:141], v[174:177], v[70:73]
	v_mfma_f32_16x16x32_bf16 v[34:37], v[130:133], v[170:173], v[34:37]
	v_mfma_f32_16x16x32_bf16 v[38:41], v[138:141], v[170:173], v[38:41]
	v_mfma_f32_16x16x32_bf16 v[6:9], v[130:133], v[162:165], v[6:9]
	v_mfma_f32_16x16x32_bf16 v[10:13], v[138:141], v[162:165], v[10:13]
	v_mfma_f32_16x16x32_bf16 v[98:101], v[134:137], v[190:193], v[98:101]
	v_mfma_f32_16x16x32_bf16 v[102:105], v[142:145], v[190:193], v[102:105]
	v_mfma_f32_16x16x32_bf16 v[66:69], v[134:137], v[178:181], v[66:69]
	v_mfma_f32_16x16x32_bf16 v[70:73], v[142:145], v[178:181], v[70:73]
	v_mfma_f32_16x16x32_bf16 v[34:37], v[134:137], v[182:185], v[34:37]
	v_mfma_f32_16x16x32_bf16 v[38:41], v[142:145], v[182:185], v[38:41]
	v_mfma_f32_16x16x32_bf16 v[6:9], v[134:137], v[166:169], v[6:9]
	v_mfma_f32_16x16x32_bf16 v[10:13], v[142:145], v[166:169], v[10:13]
	s_setprio 0
; #define PG8_STAGE(bufoff, gbase, voff) do { _Pragma("unroll") for (int _i = 0; _i < 2; ++_i) \
;         __builtin_amdgcn_global_load_lds((const unsigned*)((const char*)(gbase) + (voff)[_i]), (LAS unsigned*)(lds + (bufoff) + ldsw + _i * 8192), 16, 0, 0); } while (0)
; #define PG8_LDA(dst, b, h) do { _Pragma("unroll") for (int m = 0; m < 4; ++m) _Pragma("unroll") for (int k = 0; k < 2; ++k) dst[m][k] = *(const LAS bf16x8*)(lds + PG8_SA(b, h) + ((aoff ^ (k * 64)) + m * 2048)); } while (0)
; #define PG8_MMA(ai, bj, At, Bt) do { __builtin_amdgcn_s_setprio(1); _Pragma("unroll") for (int m = 0; m < 4; ++m) _Pragma("unroll") for (int n = 0; n < 2; ++n) _Pragma("unroll") for (int k = 0; k < 2; ++k) \
;         acc[ai][bj][m][n] = __builtin_amdgcn_mfma_f32_16x16x32_bf16(Bt[n][k], At[m][k], acc[ai][bj][m][n], 0, 0, 0); __builtin_amdgcn_s_setprio(0); } while (0)
; #define PG8_WAIT_V(n) asm volatile("s_waitcnt vmcnt(" #n ")" ::: "memory")
; #define PG8_WAIT_L(n) asm volatile("s_waitcnt lgkmcnt(" #n ")" ::: "memory")
; #define PG8_BAR __builtin_amdgcn_s_barrier()
; #define PG8_SCHED __builtin_amdgcn_sched_barrier(0)
;     ...
;             PG8_LDA(At, 1, 1); PG8_STAGE(PG8_SB(1, 0), b3, voffB); PG8_STAGE(PG8_SB(1, 1), b3 + hstep, voffB); PG8_STAGE(PG8_SA(1, 0), a3, vs[0]);
;             PG8_WAIT_V(8); PG8_WAIT_L(0); PG8_BAR; if (do1) { PG8_MMA(1, 0, At, B0); PG8_MMA(1, 1, At, B1); } PG8_BAR; PG8_SCHED;
.LBB0_1665:
	s_add_u32 s26, s26, 0x4000
	s_addc_u32 s27, s27, 0
	s_barrier
	s_mov_b32 m0, s44
	v_lshl_add_u64 v[212:213], v[212:213], 0, s[14:15]
	s_add_u32 s24, s24, 0x40080
	s_waitcnt lgkmcnt(0)
	ds_read_b128 v[186:189], v226 offset:49152
	ds_read_b128 v[174:177], v226 offset:51200
	ds_read_b128 v[190:193], v227 offset:49152
	ds_read_b128 v[178:181], v227 offset:51200
	ds_read_b128 v[170:173], v226 offset:53248
	ds_read_b128 v[162:165], v226 offset:55296
	ds_read_b128 v[182:185], v227 offset:53248
	ds_read_b128 v[166:169], v227 offset:55296
	global_load_lds_dwordx4 v[212:213], off
	v_lshl_add_u64 v[212:213], v[214:215], 0, s[14:15]
	s_mov_b32 m0, s45
	s_addc_u32 s25, s25, 0
	global_load_lds_dwordx4 v[212:213], off
	v_lshl_add_u64 v[212:213], s[24:25], 0, v[196:197]
	s_mov_b32 m0, s48
	s_and_b64 vcc, exec, s[6:7]
	global_load_lds_dwordx4 v[212:213], off
	v_lshl_add_u64 v[212:213], s[24:25], 0, v[194:195]
	s_mov_b32 m0, s49
	s_nop 0
	global_load_lds_dwordx4 v[212:213], off
	v_lshl_add_u64 v[212:213], s[26:27], 0, v[200:201]
	s_mov_b32 m0, s46
	s_nop 0
	global_load_lds_dwordx4 v[212:213], off
	v_lshl_add_u64 v[212:213], s[26:27], 0, v[202:203]
	s_mov_b32 m0, s47
	s_nop 0
	global_load_lds_dwordx4 v[212:213], off
	s_waitcnt vmcnt(8)
	s_waitcnt lgkmcnt(0)
	s_barrier
	s_cbranch_vccnz .LBB0_1658
	s_setprio 1
	s_waitcnt lgkmcnt(0)
	v_mfma_f32_16x16x32_bf16 v[126:129], v[146:149], v[186:189], v[126:129]
	v_mfma_f32_16x16x32_bf16 v[122:125], v[154:157], v[186:189], v[122:125]
	v_mfma_f32_16x16x32_bf16 v[94:97], v[146:149], v[174:177], v[94:97]
	v_mfma_f32_16x16x32_bf16 v[90:93], v[154:157], v[174:177], v[90:93]
	v_mfma_f32_16x16x32_bf16 v[62:65], v[146:149], v[170:173], v[62:65]
	v_mfma_f32_16x16x32_bf16 v[58:61], v[154:157], v[170:173], v[58:61]
	v_mfma_f32_16x16x32_bf16 v[30:33], v[146:149], v[162:165], v[30:33]
	v_mfma_f32_16x16x32_bf16 v[26:29], v[154:157], v[162:165], v[26:29]
	v_mfma_f32_16x16x32_bf16 v[126:129], v[150:153], v[190:193], v[126:129]
	v_mfma_f32_16x16x32_bf16 v[122:125], v[158:161], v[190:193], v[122:125]
	v_mfma_f32_16x16x32_bf16 v[94:97], v[150:153], v[178:181], v[94:97]
	v_mfma_f32_16x16x32_bf16 v[90:93], v[158:161], v[178:181], v[90:93]
	v_mfma_f32_16x16x32_bf16 v[62:65], v[150:153], v[182:185], v[62:65]
	v_mfma_f32_16x16x32_bf16 v[58:61], v[158:161], v[182:185], v[58:61]
	v_mfma_f32_16x16x32_bf16 v[30:33], v[150:153], v[166:169], v[30:33]
	v_mfma_f32_16x16x32_bf16 v[26:29], v[158:161], v[166:169], v[26:29]
	v_mfma_f32_16x16x32_bf16 v[110:113], v[130:133], v[186:189], v[110:113]
	v_mfma_f32_16x16x32_bf16 v[106:109], v[138:141], v[186:189], v[106:109]
	v_mfma_f32_16x16x32_bf16 v[78:81], v[130:133], v[174:177], v[78:81]
	v_mfma_f32_16x16x32_bf16 v[74:77], v[138:141], v[174:177], v[74:77]
	v_mfma_f32_16x16x32_bf16 v[46:49], v[130:133], v[170:173], v[46:49]
	v_mfma_f32_16x16x32_bf16 v[42:45], v[138:141], v[170:173], v[42:45]
	v_mfma_f32_16x16x32_bf16 v[14:17], v[130:133], v[162:165], v[14:17]
	v_mfma_f32_16x16x32_bf16 v[2:5], v[138:141], v[162:165], v[2:5]
	v_mfma_f32_16x16x32_bf16 v[110:113], v[134:137], v[190:193], v[110:113]
	v_mfma_f32_16x16x32_bf16 v[106:109], v[142:145], v[190:193], v[106:109]
	v_mfma_f32_16x16x32_bf16 v[78:81], v[134:137], v[178:181], v[78:81]
	v_mfma_f32_16x16x32_bf16 v[74:77], v[142:145], v[178:181], v[74:77]
	v_mfma_f32_16x16x32_bf16 v[46:49], v[134:137], v[182:185], v[46:49]
	v_mfma_f32_16x16x32_bf16 v[42:45], v[142:145], v[182:185], v[42:45]
	v_mfma_f32_16x16x32_bf16 v[14:17], v[134:137], v[166:169], v[14:17]
	v_mfma_f32_16x16x32_bf16 v[2:5], v[142:145], v[166:169], v[2:5]
	s_setprio 0
	s_branch .LBB0_1658

; #define PG8_STAGE(bufoff, gbase, voff) do { _Pragma("unroll") for (int _i = 0; _i < 2; ++_i) \
;         __builtin_amdgcn_global_load_lds((const unsigned*)((const char*)(gbase) + (voff)[_i]), (LAS unsigned*)(lds + (bufoff) + ldsw + _i * 8192), 16, 0, 0); } while (0)
; #define PG8_LDA(dst, b, h) do { _Pragma("unroll") for (int m = 0; m < 4; ++m) _Pragma("unroll") for (int k = 0; k < 2; ++k) dst[m][k] = *(const LAS bf16x8*)(lds + PG8_SA(b, h) + ((aoff ^ (k * 64)) + m * 2048)); } while (0)
; #define PG8_LDB(dst, b, h) do { _Pragma("unroll") for (int n = 0; n < 2; ++n) _Pragma("unroll") for (int k = 0; k < 2; ++k) dst[n][k] = *(const LAS bf16x8*)(lds + PG8_SB(b, h) + ((boff ^ (k * 64)) + n * 2048)); } while (0)
; #define PG8_WAIT_V(n) asm volatile("s_waitcnt vmcnt(" #n ")" ::: "memory")
; #define PG8_WAIT_L(n) asm volatile("s_waitcnt lgkmcnt(" #n ")" ::: "memory")
;     ...
;             const bool last = (t == nt - 2);
;             const char* a1 = cA + (size_t)(t + 1) * kstepA;
;             const char* a2 = last ? nA : cA + (size_t)(t + 2) * kstepA; const char* b2 = last ? nB : cB + (size_t)(t + 2) * kstepB;
;             const char* a3 = a2 + kstepA; const char* b3 = b2 + kstepB;
;             unsigned vs[2][2];
;             if constexpr (GATHER) {
;                 if (last && has_next) {
; #pragma unroll
;                     for (int hh = 0; hh < 2; ++hh)
; #pragma unroll
;                         for (int i = 0; i < 2; ++i) voffN[hh][i] = (unsigned)idxl[(ui + 1) * 256 + hh * HALF + sR[i]] * (unsigned)(K * 2) + (unsigned)sC[i] * 2u;
;                 }
; #pragma unroll
;                 for (int hh = 0; hh < 2; ++hh)
; #pragma unroll
;                     for (int i = 0; i < 2; ++i) vs[hh][i] = last ? voffN[hh][i] : voffA[hh][i];
;             } else {
; #pragma unroll
;                 for (int hh = 0; hh < 2; ++hh)
; #pragma unroll
;                     for (int i = 0; i < 2; ++i) vs[hh][i] = voffA[hh][i];
;             }
;             PG8_LDB(B0, 0, 0); PG8_LDB(B1, 0, 1); PG8_SCHED; PG8_LDA(At, 0, 0); PG8_STAGE(PG8_SA(1, 1), a1, voffA[1]);
;             PG8_WAIT_V(8); PG8_WAIT_L(0); PG8_BAR; if (do0) { PG8_MMA(0, 0, At, B0); PG8_MMA(0, 1, At, B1); } PG8_BAR; PG8_SCHED;
;             PG8_LDA(At, 0, 1); PG8_STAGE(PG8_SB(0, 0), b2, voffB); PG8_STAGE(PG8_SB(0, 1), b2 + hstep, voffB); PG8_STAGE(PG8_SA(0, 0), a2, vs[0]);
.LBB0_1934:
	ds_read_b128 v[74:77], v191
	ds_read_b128 v[78:81], v192
	ds_read_b128 v[102:105], v193
	ds_read_b128 v[106:109], v194
	ds_read_b128 v[168:171], v195
	ds_read_b128 v[172:175], v196
	ds_read_b128 v[176:179], v197
	ds_read_b128 v[180:183], v199
	s_add_u32 s38, s0, 0x80
	s_addc_u32 s39, s1, 0
	s_cmp_eq_u32 s45, 28
	s_cselect_b32 s43, s7, s39
	s_cselect_b32 s42, s8, s38
	s_cselect_b32 s39, s27, s44
	s_cselect_b32 s38, s29, s37
	v_lshl_add_u64 v[184:185], s[0:1], 0, v[162:163]
	s_add_i32 m0, s52, 0xc000
	ds_read_b128 v[210:213], v200
	ds_read_b128 v[214:217], v200 offset:2048
	ds_read_b128 v[218:221], v201
	ds_read_b128 v[222:225], v201 offset:2048
	ds_read_b128 v[226:229], v200 offset:4096
	ds_read_b128 v[230:233], v200 offset:6144
	ds_read_b128 v[234:237], v201 offset:4096
	ds_read_b128 v[238:241], v201 offset:6144
	global_load_lds_dwordx4 v[184:185], off
	v_lshl_add_u64 v[184:185], s[0:1], 0, v[160:161]
	s_add_i32 m0, s52, 0xe000
	s_add_u32 s40, s38, 0x4000
	global_load_lds_dwordx4 v[184:185], off
	s_waitcnt vmcnt(8)
	s_waitcnt lgkmcnt(0)
	s_addc_u32 s41, s39, 0
	s_barrier
	s_setprio 1
	s_waitcnt lgkmcnt(0)
	v_mfma_f32_16x16x32_bf16 v[142:145], v[74:77], v[210:213], v[142:145]
	v_mfma_f32_16x16x32_bf16 v[10:13], v[102:105], v[210:213], v[10:13]
	v_mfma_f32_16x16x32_bf16 v[134:137], v[74:77], v[214:217], v[134:137]
	v_mfma_f32_16x16x32_bf16 v[18:21], v[102:105], v[214:217], v[18:21]
	v_mfma_f32_16x16x32_bf16 v[126:129], v[74:77], v[226:229], v[126:129]
	v_mfma_f32_16x16x32_bf16 v[22:25], v[102:105], v[226:229], v[22:25]
	v_mfma_f32_16x16x32_bf16 v[118:121], v[74:77], v[230:233], v[118:121]
	v_mfma_f32_16x16x32_bf16 v[34:37], v[102:105], v[230:233], v[34:37]
	v_mfma_f32_16x16x32_bf16 v[142:145], v[78:81], v[218:221], v[142:145]
	v_mfma_f32_16x16x32_bf16 v[10:13], v[106:109], v[218:221], v[10:13]
	v_mfma_f32_16x16x32_bf16 v[134:137], v[78:81], v[222:225], v[134:137]
	v_mfma_f32_16x16x32_bf16 v[18:21], v[106:109], v[222:225], v[18:21]
	v_mfma_f32_16x16x32_bf16 v[126:129], v[78:81], v[234:237], v[126:129]
	v_mfma_f32_16x16x32_bf16 v[22:25], v[106:109], v[234:237], v[22:25]
	v_mfma_f32_16x16x32_bf16 v[118:121], v[78:81], v[238:241], v[118:121]
	v_mfma_f32_16x16x32_bf16 v[34:37], v[106:109], v[238:241], v[34:37]
	v_mfma_f32_16x16x32_bf16 v[138:141], v[168:171], v[210:213], v[138:141]
	v_mfma_f32_16x16x32_bf16 v[14:17], v[176:179], v[210:213], v[14:17]
	v_mfma_f32_16x16x32_bf16 v[130:133], v[168:171], v[214:217], v[130:133]
	v_mfma_f32_16x16x32_bf16 v[30:33], v[176:179], v[214:217], v[30:33]
	v_mfma_f32_16x16x32_bf16 v[122:125], v[168:171], v[226:229], v[122:125]
	v_mfma_f32_16x16x32_bf16 v[26:29], v[176:179], v[226:229], v[26:29]
	v_mfma_f32_16x16x32_bf16 v[114:117], v[168:171], v[230:233], v[114:117]
	v_mfma_f32_16x16x32_bf16 v[46:49], v[176:179], v[230:233], v[46:49]
	v_mfma_f32_16x16x32_bf16 v[138:141], v[172:175], v[218:221], v[138:141]
	v_mfma_f32_16x16x32_bf16 v[14:17], v[180:183], v[218:221], v[14:17]
	v_mfma_f32_16x16x32_bf16 v[130:133], v[172:175], v[222:225], v[130:133]
	v_mfma_f32_16x16x32_bf16 v[30:33], v[180:183], v[222:225], v[30:33]
	v_mfma_f32_16x16x32_bf16 v[122:125], v[172:175], v[234:237], v[122:125]
	v_mfma_f32_16x16x32_bf16 v[26:29], v[180:183], v[234:237], v[26:29]
	v_mfma_f32_16x16x32_bf16 v[114:117], v[172:175], v[238:241], v[114:117]
	v_mfma_f32_16x16x32_bf16 v[46:49], v[180:183], v[238:241], v[46:49]
	s_setprio 0
	s_barrier
	s_add_i32 s46, s67, s51
	v_lshl_add_u64 v[184:185], s[38:39], 0, v[146:147]
	s_mov_b32 m0, s46
	ds_read_b128 v[210:213], v200 offset:16384
	ds_read_b128 v[214:217], v200 offset:18432
	ds_read_b128 v[218:221], v201 offset:16384
	ds_read_b128 v[222:225], v201 offset:18432
	ds_read_b128 v[226:229], v200 offset:20480
	ds_read_b128 v[230:233], v200 offset:22528
	ds_read_b128 v[234:237], v201 offset:20480
	ds_read_b128 v[238:241], v201 offset:22528
	global_load_lds_dwordx4 v[184:185], off
	s_add_i32 m0, s46, 0x2000
	s_add_u32 s46, s38, 0x80000
	v_lshl_add_u64 v[184:185], s[38:39], 0, v[148:149]
	s_addc_u32 s47, s39, 0
	s_add_i32 s72, s68, s51
	global_load_lds_dwordx4 v[184:185], off
	v_lshl_add_u64 v[184:185], s[46:47], 0, v[146:147]
	s_mov_b32 m0, s72
	v_lshl_add_u64 v[242:243], s[42:43], 0, v[152:153]
	global_load_lds_dwordx4 v[184:185], off
	v_lshl_add_u64 v[184:185], s[46:47], 0, v[148:149]
	s_add_i32 m0, s72, 0x2000
	s_nop 0
	global_load_lds_dwordx4 v[184:185], off
	v_lshl_add_u64 v[184:185], s[42:43], 0, v[150:151]
	s_mov_b32 m0, s52
	s_nop 0
	global_load_lds_dwordx4 v[184:185], off
	s_mov_b32 m0, s53
	s_nop 0
	global_load_lds_dwordx4 v[242:243], off
	s_waitcnt vmcnt(8)
	s_waitcnt lgkmcnt(0)
	s_barrier
; #define PG8_STAGE(bufoff, gbase, voff) do { _Pragma("unroll") for (int _i = 0; _i < 2; ++_i) \
;         __builtin_amdgcn_global_load_lds((const unsigned*)((const char*)(gbase) + (voff)[_i]), (LAS unsigned*)(lds + (bufoff) + ldsw + _i * 8192), 16, 0, 0); } while (0)
; #define PG8_LDA(dst, b, h) do { _Pragma("unroll") for (int m = 0; m < 4; ++m) _Pragma("unroll") for (int k = 0; k < 2; ++k) dst[m][k] = *(const LAS bf16x8*)(lds + PG8_SA(b, h) + ((aoff ^ (k * 64)) + m * 2048)); } while (0)
; #define PG8_LDB(dst, b, h) do { _Pragma("unroll") for (int n = 0; n < 2; ++n) _Pragma("unroll") for (int k = 0; k < 2; ++k) dst[n][k] = *(const LAS bf16x8*)(lds + PG8_SB(b, h) + ((boff ^ (k * 64)) + n * 2048)); } while (0)
; #define PG8_MMA(ai, bj, At, Bt) do { __builtin_amdgcn_s_setprio(1); _Pragma("unroll") for (int m = 0; m < 4; ++m) _Pragma("unroll") for (int n = 0; n < 2; ++n) _Pragma("unroll") for (int k = 0; k < 2; ++k) \
;         acc[ai][bj][m][n] = __builtin_amdgcn_mfma_f32_16x16x32_bf16(Bt[n][k], At[m][k], acc[ai][bj][m][n], 0, 0, 0); __builtin_amdgcn_s_setprio(0); } while (0)
; #define PG8_WAIT_V(n) asm volatile("s_waitcnt vmcnt(" #n ")" ::: "memory")
; #define PG8_WAIT_L(n) asm volatile("s_waitcnt lgkmcnt(" #n ")" ::: "memory")
; #define PG8_BAR __builtin_amdgcn_s_barrier()
; #define PG8_SCHED __builtin_amdgcn_sched_barrier(0)
;     ...
;             PG8_WAIT_V(8); PG8_WAIT_L(0); PG8_BAR; if (do1) { PG8_MMA(1, 0, At, B0); PG8_MMA(1, 1, At, B1); } PG8_BAR; PG8_SCHED;
;             PG8_LDB(B0, 1, 0); PG8_LDB(B1, 1, 1); PG8_SCHED; PG8_LDA(At, 1, 0); PG8_STAGE(PG8_SA(0, 1), a2, vs[1]);
;             PG8_WAIT_V(8); PG8_WAIT_L(0); PG8_BAR; if (do0) { PG8_MMA(0, 0, At, B0); PG8_MMA(0, 1, At, B1); } PG8_BAR; PG8_SCHED;
	s_setprio 1
	s_waitcnt lgkmcnt(0)
	v_mfma_f32_16x16x32_bf16 v[110:113], v[74:77], v[210:213], v[110:113]
	v_mfma_f32_16x16x32_bf16 v[58:61], v[102:105], v[210:213], v[58:61]
	v_mfma_f32_16x16x32_bf16 v[94:97], v[74:77], v[214:217], v[94:97]
	v_mfma_f32_16x16x32_bf16 v[82:85], v[102:105], v[214:217], v[82:85]
	v_mfma_f32_16x16x32_bf16 v[66:69], v[74:77], v[226:229], v[66:69]
	v_mfma_f32_16x16x32_bf16 v[62:65], v[102:105], v[226:229], v[62:65]
	v_mfma_f32_16x16x32_bf16 v[42:45], v[74:77], v[230:233], v[42:45]
	v_mfma_f32_16x16x32_bf16 v[38:41], v[102:105], v[230:233], v[38:41]
	v_mfma_f32_16x16x32_bf16 v[110:113], v[78:81], v[218:221], v[110:113]
	v_mfma_f32_16x16x32_bf16 v[58:61], v[106:109], v[218:221], v[58:61]
	v_mfma_f32_16x16x32_bf16 v[94:97], v[78:81], v[222:225], v[94:97]
	v_mfma_f32_16x16x32_bf16 v[82:85], v[106:109], v[222:225], v[82:85]
	v_mfma_f32_16x16x32_bf16 v[66:69], v[78:81], v[234:237], v[66:69]
	v_mfma_f32_16x16x32_bf16 v[62:65], v[106:109], v[234:237], v[62:65]
	v_mfma_f32_16x16x32_bf16 v[42:45], v[78:81], v[238:241], v[42:45]
	v_mfma_f32_16x16x32_bf16 v[38:41], v[106:109], v[238:241], v[38:41]
	v_mfma_f32_16x16x32_bf16 v[70:73], v[176:179], v[210:213], v[70:73]
	v_mfma_f32_16x16x32_bf16 v[86:89], v[176:179], v[214:217], v[86:89]
	v_mfma_f32_16x16x32_bf16 v[54:57], v[168:171], v[226:229], v[54:57]
	v_mfma_f32_16x16x32_bf16 v[50:53], v[176:179], v[226:229], v[50:53]
	v_mfma_f32_16x16x32_bf16 v[6:9], v[168:171], v[230:233], v[6:9]
	v_mfma_f32_16x16x32_bf16 v[2:5], v[176:179], v[230:233], v[2:5]
	v_mfma_f32_16x16x32_bf16 v[74:77], v[168:171], v[210:213], v[98:101]
	v_mfma_f32_16x16x32_bf16 v[70:73], v[180:183], v[218:221], v[70:73]
	v_mfma_f32_16x16x32_bf16 v[78:81], v[168:171], v[214:217], v[90:93]
	v_mfma_f32_16x16x32_bf16 v[86:89], v[180:183], v[222:225], v[86:89]
	v_mfma_f32_16x16x32_bf16 v[54:57], v[172:175], v[234:237], v[54:57]
	v_mfma_f32_16x16x32_bf16 v[50:53], v[180:183], v[234:237], v[50:53]
	v_mfma_f32_16x16x32_bf16 v[6:9], v[172:175], v[238:241], v[6:9]
	v_mfma_f32_16x16x32_bf16 v[2:5], v[180:183], v[238:241], v[2:5]
	v_mfma_f32_16x16x32_bf16 v[74:77], v[172:175], v[218:221], v[74:77]
	v_mfma_f32_16x16x32_bf16 v[78:81], v[172:175], v[222:225], v[78:81]
	s_setprio 0
	s_barrier
	s_add_i32 s46, 0, 0x18000
	s_add_i32 s47, 0, 0x1c000
	v_add_u32_e32 v90, s46, v189
	v_add_u32_e32 v98, s46, v190
	v_add_u32_e32 v158, s47, v189
	v_add_u32_e32 v172, s47, v190
	ds_read_b128 v[90:93], v90
	ds_read_b128 v[98:101], v98
	ds_read_b128 v[102:105], v202
	ds_read_b128 v[106:109], v203
	ds_read_b128 v[168:171], v158
	ds_read_b128 v[172:175], v172
	ds_read_b128 v[176:179], v204
	ds_read_b128 v[180:183], v205
	s_mov_b32 m0, s54
	v_lshl_add_u64 v[244:245], s[42:43], 0, v[154:155]
	ds_read_b128 v[210:213], v200 offset:32768
	ds_read_b128 v[214:217], v200 offset:34816
	ds_read_b128 v[218:221], v201 offset:32768
	ds_read_b128 v[222:225], v201 offset:34816
	ds_read_b128 v[226:229], v200 offset:36864
	ds_read_b128 v[230:233], v200 offset:38912
	ds_read_b128 v[234:237], v201 offset:36864
	ds_read_b128 v[238:241], v201 offset:38912
	global_load_lds_dwordx4 v[244:245], off
	v_lshl_add_u64 v[244:245], s[42:43], 0, v[156:157]
	s_mov_b32 m0, s55
	s_nop 0
	global_load_lds_dwordx4 v[244:245], off
	s_waitcnt vmcnt(8)
	s_waitcnt lgkmcnt(0)
	s_barrier
	s_setprio 1
	s_waitcnt lgkmcnt(0)
	v_mfma_f32_16x16x32_bf16 v[142:145], v[90:93], v[210:213], v[142:145]
	v_mfma_f32_16x16x32_bf16 v[10:13], v[102:105], v[210:213], v[10:13]
	v_mfma_f32_16x16x32_bf16 v[134:137], v[90:93], v[214:217], v[134:137]
	v_mfma_f32_16x16x32_bf16 v[18:21], v[102:105], v[214:217], v[18:21]
	v_mfma_f32_16x16x32_bf16 v[126:129], v[90:93], v[226:229], v[126:129]
	v_mfma_f32_16x16x32_bf16 v[22:25], v[102:105], v[226:229], v[22:25]
	v_mfma_f32_16x16x32_bf16 v[118:121], v[90:93], v[230:233], v[118:121]
	v_mfma_f32_16x16x32_bf16 v[34:37], v[102:105], v[230:233], v[34:37]
	v_mfma_f32_16x16x32_bf16 v[142:145], v[98:101], v[218:221], v[142:145]
	v_mfma_f32_16x16x32_bf16 v[10:13], v[106:109], v[218:221], v[10:13]
	v_mfma_f32_16x16x32_bf16 v[134:137], v[98:101], v[222:225], v[134:137]
	v_mfma_f32_16x16x32_bf16 v[18:21], v[106:109], v[222:225], v[18:21]
	v_mfma_f32_16x16x32_bf16 v[126:129], v[98:101], v[234:237], v[126:129]
	v_mfma_f32_16x16x32_bf16 v[22:25], v[106:109], v[234:237], v[22:25]
	v_mfma_f32_16x16x32_bf16 v[118:121], v[98:101], v[238:241], v[118:121]
	v_mfma_f32_16x16x32_bf16 v[34:37], v[106:109], v[238:241], v[34:37]
	v_mfma_f32_16x16x32_bf16 v[138:141], v[168:171], v[210:213], v[138:141]
	v_mfma_f32_16x16x32_bf16 v[14:17], v[176:179], v[210:213], v[14:17]
	v_mfma_f32_16x16x32_bf16 v[130:133], v[168:171], v[214:217], v[130:133]
	v_mfma_f32_16x16x32_bf16 v[30:33], v[176:179], v[214:217], v[30:33]
	v_mfma_f32_16x16x32_bf16 v[122:125], v[168:171], v[226:229], v[122:125]
	v_mfma_f32_16x16x32_bf16 v[26:29], v[176:179], v[226:229], v[26:29]
	v_mfma_f32_16x16x32_bf16 v[114:117], v[168:171], v[230:233], v[114:117]
	v_mfma_f32_16x16x32_bf16 v[46:49], v[176:179], v[230:233], v[46:49]
	v_mfma_f32_16x16x32_bf16 v[138:141], v[172:175], v[218:221], v[138:141]
	v_mfma_f32_16x16x32_bf16 v[14:17], v[180:183], v[218:221], v[14:17]
	v_mfma_f32_16x16x32_bf16 v[130:133], v[172:175], v[222:225], v[130:133]
	v_mfma_f32_16x16x32_bf16 v[30:33], v[180:183], v[222:225], v[30:33]
	v_mfma_f32_16x16x32_bf16 v[122:125], v[172:175], v[234:237], v[122:125]
	v_mfma_f32_16x16x32_bf16 v[26:29], v[180:183], v[234:237], v[26:29]
	v_mfma_f32_16x16x32_bf16 v[114:117], v[172:175], v[238:241], v[114:117]
	v_mfma_f32_16x16x32_bf16 v[46:49], v[180:183], v[238:241], v[46:49]
	s_setprio 0
	s_barrier
; #define PG8_STAGE(bufoff, gbase, voff) do { _Pragma("unroll") for (int _i = 0; _i < 2; ++_i) \
;         __builtin_amdgcn_global_load_lds((const unsigned*)((const char*)(gbase) + (voff)[_i]), (LAS unsigned*)(lds + (bufoff) + ldsw + _i * 8192), 16, 0, 0); } while (0)
; #define PG8_LDA(dst, b, h) do { _Pragma("unroll") for (int m = 0; m < 4; ++m) _Pragma("unroll") for (int k = 0; k < 2; ++k) dst[m][k] = *(const LAS bf16x8*)(lds + PG8_SA(b, h) + ((aoff ^ (k * 64)) + m * 2048)); } while (0)
; #define PG8_MMA(ai, bj, At, Bt) do { __builtin_amdgcn_s_setprio(1); _Pragma("unroll") for (int m = 0; m < 4; ++m) _Pragma("unroll") for (int n = 0; n < 2; ++n) _Pragma("unroll") for (int k = 0; k < 2; ++k) \
;         acc[ai][bj][m][n] = __builtin_amdgcn_mfma_f32_16x16x32_bf16(Bt[n][k], At[m][k], acc[ai][bj][m][n], 0, 0, 0); __builtin_amdgcn_s_setprio(0); } while (0)
; #define PG8_WAIT_V(n) asm volatile("s_waitcnt vmcnt(" #n ")" ::: "memory")
; #define PG8_WAIT_L(n) asm volatile("s_waitcnt lgkmcnt(" #n ")" ::: "memory")
; #define PG8_BAR __builtin_amdgcn_s_barrier()
; #define PG8_SCHED __builtin_amdgcn_sched_barrier(0)
;     ...
;             PG8_LDA(At, 1, 1); PG8_STAGE(PG8_SB(1, 0), b3, voffB); PG8_STAGE(PG8_SB(1, 1), b3 + hstep, voffB); PG8_STAGE(PG8_SA(1, 0), a3, vs[0]);
;             PG8_WAIT_V(8); PG8_WAIT_L(0); PG8_BAR; if (do1) { PG8_MMA(1, 0, At, B0); PG8_MMA(1, 1, At, B1); } PG8_BAR; PG8_SCHED;
;         }
;         if (wr == 0) PG8_BAR;
	s_add_i32 s42, s46, s51
	v_lshl_add_u64 v[244:245], s[40:41], 0, v[146:147]
	s_mov_b32 m0, s42
	ds_read_b128 v[210:213], v200 offset:49152
	ds_read_b128 v[214:217], v200 offset:51200
	ds_read_b128 v[218:221], v201 offset:49152
	ds_read_b128 v[222:225], v201 offset:51200
	ds_read_b128 v[226:229], v200 offset:53248
	ds_read_b128 v[230:233], v200 offset:55296
	ds_read_b128 v[234:237], v201 offset:53248
	ds_read_b128 v[238:241], v201 offset:55296
	global_load_lds_dwordx4 v[244:245], off
	s_add_i32 m0, s42, 0x2000
	s_add_u32 s38, s38, 0x84000
	v_lshl_add_u64 v[244:245], s[40:41], 0, v[148:149]
	s_addc_u32 s39, s39, 0
	s_add_i32 s40, s47, s51
	global_load_lds_dwordx4 v[244:245], off
	v_lshl_add_u64 v[244:245], s[38:39], 0, v[146:147]
	s_mov_b32 m0, s40
	v_lshl_add_u64 v[184:185], v[184:185], 0, s[16:17]
	global_load_lds_dwordx4 v[244:245], off
	v_lshl_add_u64 v[244:245], s[38:39], 0, v[148:149]
	s_add_i32 m0, s40, 0x2000
	s_nop 0
	global_load_lds_dwordx4 v[244:245], off
	s_mov_b32 m0, s57
	s_nop 0
	global_load_lds_dwordx4 v[184:185], off
	v_lshl_add_u64 v[184:185], v[242:243], 0, s[16:17]
	s_mov_b32 m0, s58
	s_nop 0
	global_load_lds_dwordx4 v[184:185], off
	s_waitcnt vmcnt(8)
	s_waitcnt lgkmcnt(0)
	s_barrier
	s_setprio 1
	s_waitcnt lgkmcnt(0)
	v_mfma_f32_16x16x32_bf16 v[110:113], v[90:93], v[210:213], v[110:113]
	v_mfma_f32_16x16x32_bf16 v[58:61], v[102:105], v[210:213], v[58:61]
	v_mfma_f32_16x16x32_bf16 v[94:97], v[90:93], v[214:217], v[94:97]
	v_mfma_f32_16x16x32_bf16 v[82:85], v[102:105], v[214:217], v[82:85]
	v_mfma_f32_16x16x32_bf16 v[66:69], v[90:93], v[226:229], v[66:69]
	v_mfma_f32_16x16x32_bf16 v[62:65], v[102:105], v[226:229], v[62:65]
	v_mfma_f32_16x16x32_bf16 v[42:45], v[90:93], v[230:233], v[42:45]
	v_mfma_f32_16x16x32_bf16 v[38:41], v[102:105], v[230:233], v[38:41]
	v_mfma_f32_16x16x32_bf16 v[110:113], v[98:101], v[218:221], v[110:113]
	v_mfma_f32_16x16x32_bf16 v[58:61], v[106:109], v[218:221], v[58:61]
	v_mfma_f32_16x16x32_bf16 v[94:97], v[98:101], v[222:225], v[94:97]
	v_mfma_f32_16x16x32_bf16 v[82:85], v[106:109], v[222:225], v[82:85]
	v_mfma_f32_16x16x32_bf16 v[66:69], v[98:101], v[234:237], v[66:69]
	v_mfma_f32_16x16x32_bf16 v[62:65], v[106:109], v[234:237], v[62:65]
	v_mfma_f32_16x16x32_bf16 v[42:45], v[98:101], v[238:241], v[42:45]
	v_mfma_f32_16x16x32_bf16 v[38:41], v[106:109], v[238:241], v[38:41]
	v_mfma_f32_16x16x32_bf16 v[74:77], v[168:171], v[210:213], v[74:77]
	v_mfma_f32_16x16x32_bf16 v[98:101], v[172:175], v[218:221], v[74:77]
	v_mfma_f32_16x16x32_bf16 v[74:77], v[168:171], v[214:217], v[78:81]
	v_mfma_f32_16x16x32_bf16 v[70:73], v[176:179], v[210:213], v[70:73]
	v_mfma_f32_16x16x32_bf16 v[90:93], v[172:175], v[222:225], v[74:77]
	v_mfma_f32_16x16x32_bf16 v[74:77], v[176:179], v[214:217], v[86:89]
	v_mfma_f32_16x16x32_bf16 v[54:57], v[168:171], v[226:229], v[54:57]
	v_mfma_f32_16x16x32_bf16 v[50:53], v[176:179], v[226:229], v[50:53]
	v_mfma_f32_16x16x32_bf16 v[6:9], v[168:171], v[230:233], v[6:9]
	v_mfma_f32_16x16x32_bf16 v[2:5], v[176:179], v[230:233], v[2:5]
	v_mfma_f32_16x16x32_bf16 v[70:73], v[180:183], v[218:221], v[70:73]
	v_mfma_f32_16x16x32_bf16 v[86:89], v[180:183], v[222:225], v[74:77]
	v_mfma_f32_16x16x32_bf16 v[54:57], v[172:175], v[234:237], v[54:57]
	v_mfma_f32_16x16x32_bf16 v[50:53], v[180:183], v[234:237], v[50:53]
	v_mfma_f32_16x16x32_bf16 v[6:9], v[172:175], v[238:241], v[6:9]
	v_mfma_f32_16x16x32_bf16 v[2:5], v[180:183], v[238:241], v[2:5]
	s_setprio 0
	s_barrier
	s_add_i32 s45, s45, 2
	s_add_u32 s37, s37, 0x8000
	s_addc_u32 s44, s44, 0
	s_add_u32 s0, s0, 0x100
	s_addc_u32 s1, s1, 0
	s_cmp_gt_u32 s45, 29
	s_cbranch_scc0 .LBB0_1934
	s_and_b64 vcc, exec, s[18:19]
	s_cbranch_vccz .LBB0_1937
	s_barrier

; #define PG8_STAGE(bufoff, gbase, voff) do { _Pragma("unroll") for (int _i = 0; _i < 2; ++_i) \
;         __builtin_amdgcn_global_load_lds((const unsigned*)((const char*)(gbase) + (voff)[_i]), (LAS unsigned*)(lds + (bufoff) + ldsw + _i * 8192), 16, 0, 0); } while (0)
; #define PG8_LDA(dst, b, h) do { _Pragma("unroll") for (int m = 0; m < 4; ++m) _Pragma("unroll") for (int k = 0; k < 2; ++k) dst[m][k] = *(const LAS bf16x8*)(lds + PG8_SA(b, h) + ((aoff ^ (k * 64)) + m * 2048)); } while (0)
; #define PG8_LDB(dst, b, h) do { _Pragma("unroll") for (int n = 0; n < 2; ++n) _Pragma("unroll") for (int k = 0; k < 2; ++k) dst[n][k] = *(const LAS bf16x8*)(lds + PG8_SB(b, h) + ((boff ^ (k * 64)) + n * 2048)); } while (0)
; #define PG8_WAIT_V(n) asm volatile("s_waitcnt vmcnt(" #n ")" ::: "memory")
; #define PG8_WAIT_L(n) asm volatile("s_waitcnt lgkmcnt(" #n ")" ::: "memory")
;     ...
;             const bool last = (t == nt - 2);
;             const char* a1 = cA + (size_t)(t + 1) * kstepA;
;             const char* a2 = last ? nA : cA + (size_t)(t + 2) * kstepA; const char* b2 = last ? nB : cB + (size_t)(t + 2) * kstepB;
;             const char* a3 = a2 + kstepA; const char* b3 = b2 + kstepB;
;             unsigned vs[2][2];
;             if constexpr (GATHER) {
;                 if (last && has_next) {
; #pragma unroll
;                     for (int hh = 0; hh < 2; ++hh)
; #pragma unroll
;                         for (int i = 0; i < 2; ++i) voffN[hh][i] = (unsigned)idxl[(ui + 1) * 256 + hh * HALF + sR[i]] * (unsigned)(K * 2) + (unsigned)sC[i] * 2u;
;                 }
; #pragma unroll
;                 for (int hh = 0; hh < 2; ++hh)
; #pragma unroll
;                     for (int i = 0; i < 2; ++i) vs[hh][i] = last ? voffN[hh][i] : voffA[hh][i];
;             } else {
; #pragma unroll
;                 for (int hh = 0; hh < 2; ++hh)
; #pragma unroll
;                     for (int i = 0; i < 2; ++i) vs[hh][i] = voffA[hh][i];
;             }
;             PG8_LDB(B0, 0, 0); PG8_LDB(B1, 0, 1); PG8_SCHED; PG8_LDA(At, 0, 0); PG8_STAGE(PG8_SA(1, 1), a1, voffA[1]);
;             PG8_WAIT_V(8); PG8_WAIT_L(0); PG8_BAR; if (do0) { PG8_MMA(0, 0, At, B0); PG8_MMA(0, 1, At, B1); } PG8_BAR; PG8_SCHED;
;             PG8_LDA(At, 0, 1); PG8_STAGE(PG8_SB(0, 0), b2, voffB); PG8_STAGE(PG8_SB(0, 1), b2 + hstep, voffB); PG8_STAGE(PG8_SA(0, 0), a2, vs[0]);
.LBB0_2337:
	v_add_u32_e32 v136, s43, v159
	v_add_u32_e32 v145, s43, v160
	ds_read_b128 v[166:169], v136
	ds_read_b128 v[170:173], v145
	v_add_u32_e32 v136, s44, v159
	s_add_u32 s22, s90, s20
	v_add_u32_e32 v145, s44, v160
	ds_read_b128 v[174:177], v136
	ds_read_b128 v[178:181], v145
	v_add_u32_e32 v136, s45, v159
	s_addc_u32 s23, s91, s21
	v_add_u32_e32 v145, s45, v160
	ds_read_b128 v[182:185], v136
	ds_read_b128 v[186:189], v145
	v_add_u32_e32 v136, s46, v159
	s_add_u32 s24, s22, 0x4213700
	v_add_u32_e32 v145, s46, v160
	ds_read_b128 v[190:193], v136
	ds_read_b128 v[194:197], v145
	s_addc_u32 s25, s23, 0
	s_and_b64 s[22:23], s[2:3], exec
	s_cselect_b32 s22, s14, s13
	s_cselect_b32 s27, s83, s25
	s_cselect_b32 s26, s82, s24
	s_cselect_b32 s23, s15, s53
	s_add_u32 s24, s22, 0x4000
	s_addc_u32 s25, s23, 0
	v_cndmask_b32_e64 v136, v152, v146, s[2:3]
	v_cndmask_b32_e64 v232, v153, v147, s[2:3]
	v_cndmask_b32_e64 v145, v148, v164, s[2:3]
	v_cndmask_b32_e64 v149, v150, v165, s[2:3]
	v_lshl_add_u64 v[234:235], v[156:157], 0, s[20:21]
	s_add_i32 m0, s17, 0xc000
	ds_read_b128 v[200:203], v161
	ds_read_b128 v[204:207], v161 offset:2048
	ds_read_b128 v[208:211], v162
	ds_read_b128 v[212:215], v162 offset:2048
	ds_read_b128 v[216:219], v161 offset:4096
	ds_read_b128 v[220:223], v161 offset:6144
	ds_read_b128 v[224:227], v162 offset:4096
	ds_read_b128 v[228:231], v162 offset:6144
	global_load_lds_dwordx4 v[234:235], off
	v_lshl_add_u64 v[234:235], v[154:155], 0, s[20:21]
	s_add_i32 m0, s17, 0xe000
	s_nop 0
	global_load_lds_dwordx4 v[234:235], off
	s_waitcnt vmcnt(8)
	s_waitcnt lgkmcnt(0)
	s_barrier
	s_setprio 1
	s_waitcnt lgkmcnt(0)
	v_mfma_f32_16x16x32_bf16 v[126:129], v[166:169], v[200:203], v[126:129]
	v_mfma_f32_16x16x32_bf16 v[122:125], v[174:177], v[200:203], v[122:125]
	v_mfma_f32_16x16x32_bf16 v[110:113], v[166:169], v[204:207], v[110:113]
	v_mfma_f32_16x16x32_bf16 v[106:109], v[174:177], v[204:207], v[106:109]
	v_mfma_f32_16x16x32_bf16 v[94:97], v[166:169], v[216:219], v[94:97]
	v_mfma_f32_16x16x32_bf16 v[90:93], v[174:177], v[216:219], v[90:93]
	v_mfma_f32_16x16x32_bf16 v[78:81], v[166:169], v[220:223], v[78:81]
	v_mfma_f32_16x16x32_bf16 v[74:77], v[174:177], v[220:223], v[74:77]
	v_mfma_f32_16x16x32_bf16 v[126:129], v[170:173], v[208:211], v[126:129]
	v_mfma_f32_16x16x32_bf16 v[122:125], v[178:181], v[208:211], v[122:125]
	v_mfma_f32_16x16x32_bf16 v[110:113], v[170:173], v[212:215], v[110:113]
	v_mfma_f32_16x16x32_bf16 v[106:109], v[178:181], v[212:215], v[106:109]
	v_mfma_f32_16x16x32_bf16 v[94:97], v[170:173], v[224:227], v[94:97]
	v_mfma_f32_16x16x32_bf16 v[90:93], v[178:181], v[224:227], v[90:93]
	v_mfma_f32_16x16x32_bf16 v[78:81], v[170:173], v[228:231], v[78:81]
	v_mfma_f32_16x16x32_bf16 v[74:77], v[178:181], v[228:231], v[74:77]
	v_mfma_f32_16x16x32_bf16 v[118:121], v[182:185], v[200:203], v[118:121]
	v_mfma_f32_16x16x32_bf16 v[114:117], v[190:193], v[200:203], v[114:117]
	v_mfma_f32_16x16x32_bf16 v[102:105], v[182:185], v[204:207], v[102:105]
	v_mfma_f32_16x16x32_bf16 v[98:101], v[190:193], v[204:207], v[98:101]
	v_mfma_f32_16x16x32_bf16 v[86:89], v[182:185], v[216:219], v[86:89]
	v_mfma_f32_16x16x32_bf16 v[82:85], v[190:193], v[216:219], v[82:85]
	v_mfma_f32_16x16x32_bf16 v[70:73], v[182:185], v[220:223], v[70:73]
	v_mfma_f32_16x16x32_bf16 v[66:69], v[190:193], v[220:223], v[66:69]
	v_mfma_f32_16x16x32_bf16 v[118:121], v[186:189], v[208:211], v[118:121]
	v_mfma_f32_16x16x32_bf16 v[114:117], v[194:197], v[208:211], v[114:117]
	v_mfma_f32_16x16x32_bf16 v[102:105], v[186:189], v[212:215], v[102:105]
	v_mfma_f32_16x16x32_bf16 v[98:101], v[194:197], v[212:215], v[98:101]
	v_mfma_f32_16x16x32_bf16 v[86:89], v[186:189], v[224:227], v[86:89]
	v_mfma_f32_16x16x32_bf16 v[82:85], v[194:197], v[224:227], v[82:85]
	v_mfma_f32_16x16x32_bf16 v[70:73], v[186:189], v[228:231], v[70:73]
	v_mfma_f32_16x16x32_bf16 v[66:69], v[194:197], v[228:231], v[66:69]
	s_setprio 0
	s_barrier
	s_add_i32 s2, s43, s34
	v_lshl_add_u64 v[234:235], s[22:23], 0, v[132:133]
	s_mov_b32 m0, s2
	ds_read_b128 v[200:203], v161 offset:16384
	ds_read_b128 v[204:207], v161 offset:18432
	ds_read_b128 v[208:211], v162 offset:16384
	ds_read_b128 v[212:215], v162 offset:18432
	ds_read_b128 v[216:219], v161 offset:20480
	ds_read_b128 v[220:223], v161 offset:22528
	ds_read_b128 v[224:227], v162 offset:20480
	ds_read_b128 v[228:231], v162 offset:22528
	global_load_lds_dwordx4 v[234:235], off
	s_add_i32 m0, s2, 0x2000
	s_add_u32 s2, s22, 0x40000
	v_lshl_add_u64 v[234:235], s[22:23], 0, v[134:135]
	s_addc_u32 s3, s23, 0
	s_add_i32 s55, s45, s34
	global_load_lds_dwordx4 v[234:235], off
	v_lshl_add_u64 v[234:235], s[2:3], 0, v[132:133]
	s_mov_b32 m0, s55
	v_mov_b32_e32 v233, v137
	global_load_lds_dwordx4 v[234:235], off
	v_lshl_add_u64 v[234:235], s[2:3], 0, v[134:135]
	s_add_i32 m0, s55, 0x2000
	s_nop 0
	global_load_lds_dwordx4 v[234:235], off
	s_mov_b32 m0, s17
	v_lshl_add_u64 v[234:235], s[26:27], 0, v[136:137]
	global_load_lds_dwordx4 v136, s[26:27]
	s_mov_b32 m0, s35
	s_nop 0
	global_load_lds_dwordx4 v232, s[26:27]
	s_waitcnt vmcnt(8)
	s_waitcnt lgkmcnt(0)
	v_lshl_add_u64 v[232:233], s[26:27], 0, v[232:233]
	s_barrier
; #define PG8_STAGE(bufoff, gbase, voff) do { _Pragma("unroll") for (int _i = 0; _i < 2; ++_i) \
;         __builtin_amdgcn_global_load_lds((const unsigned*)((const char*)(gbase) + (voff)[_i]), (LAS unsigned*)(lds + (bufoff) + ldsw + _i * 8192), 16, 0, 0); } while (0)
; #define PG8_LDA(dst, b, h) do { _Pragma("unroll") for (int m = 0; m < 4; ++m) _Pragma("unroll") for (int k = 0; k < 2; ++k) dst[m][k] = *(const LAS bf16x8*)(lds + PG8_SA(b, h) + ((aoff ^ (k * 64)) + m * 2048)); } while (0)
; #define PG8_LDB(dst, b, h) do { _Pragma("unroll") for (int n = 0; n < 2; ++n) _Pragma("unroll") for (int k = 0; k < 2; ++k) dst[n][k] = *(const LAS bf16x8*)(lds + PG8_SB(b, h) + ((boff ^ (k * 64)) + n * 2048)); } while (0)
; #define PG8_MMA(ai, bj, At, Bt) do { __builtin_amdgcn_s_setprio(1); _Pragma("unroll") for (int m = 0; m < 4; ++m) _Pragma("unroll") for (int n = 0; n < 2; ++n) _Pragma("unroll") for (int k = 0; k < 2; ++k) \
;         acc[ai][bj][m][n] = __builtin_amdgcn_mfma_f32_16x16x32_bf16(Bt[n][k], At[m][k], acc[ai][bj][m][n], 0, 0, 0); __builtin_amdgcn_s_setprio(0); } while (0)
; #define PG8_WAIT_V(n) asm volatile("s_waitcnt vmcnt(" #n ")" ::: "memory")
; #define PG8_WAIT_L(n) asm volatile("s_waitcnt lgkmcnt(" #n ")" ::: "memory")
; #define PG8_BAR __builtin_amdgcn_s_barrier()
; #define PG8_SCHED __builtin_amdgcn_sched_barrier(0)
;     ...
;             PG8_WAIT_V(8); PG8_WAIT_L(0); PG8_BAR; if (do1) { PG8_MMA(1, 0, At, B0); PG8_MMA(1, 1, At, B1); } PG8_BAR; PG8_SCHED;
;             PG8_LDB(B0, 1, 0); PG8_LDB(B1, 1, 1); PG8_SCHED; PG8_LDA(At, 1, 0); PG8_STAGE(PG8_SA(0, 1), a2, vs[1]);
;             PG8_WAIT_V(8); PG8_WAIT_L(0); PG8_BAR; if (do0) { PG8_MMA(0, 0, At, B0); PG8_MMA(0, 1, At, B1); } PG8_BAR; PG8_SCHED;
	s_setprio 1
	s_waitcnt lgkmcnt(0)
	v_mfma_f32_16x16x32_bf16 v[62:65], v[166:169], v[200:203], v[62:65]
	v_mfma_f32_16x16x32_bf16 v[58:61], v[174:177], v[200:203], v[58:61]
	v_mfma_f32_16x16x32_bf16 v[46:49], v[166:169], v[204:207], v[46:49]
	v_mfma_f32_16x16x32_bf16 v[42:45], v[174:177], v[204:207], v[42:45]
	v_mfma_f32_16x16x32_bf16 v[30:33], v[166:169], v[216:219], v[30:33]
	v_mfma_f32_16x16x32_bf16 v[26:29], v[174:177], v[216:219], v[26:29]
	v_mfma_f32_16x16x32_bf16 v[14:17], v[166:169], v[220:223], v[14:17]
	v_mfma_f32_16x16x32_bf16 v[10:13], v[174:177], v[220:223], v[10:13]
	v_mfma_f32_16x16x32_bf16 v[62:65], v[170:173], v[208:211], v[62:65]
	v_mfma_f32_16x16x32_bf16 v[58:61], v[178:181], v[208:211], v[58:61]
	v_mfma_f32_16x16x32_bf16 v[46:49], v[170:173], v[212:215], v[46:49]
	v_mfma_f32_16x16x32_bf16 v[42:45], v[178:181], v[212:215], v[42:45]
	v_mfma_f32_16x16x32_bf16 v[30:33], v[170:173], v[224:227], v[30:33]
	v_mfma_f32_16x16x32_bf16 v[26:29], v[178:181], v[224:227], v[26:29]
	v_mfma_f32_16x16x32_bf16 v[14:17], v[170:173], v[228:231], v[14:17]
	v_mfma_f32_16x16x32_bf16 v[10:13], v[178:181], v[228:231], v[10:13]
	v_mfma_f32_16x16x32_bf16 v[54:57], v[182:185], v[200:203], v[54:57]
	v_mfma_f32_16x16x32_bf16 v[50:53], v[190:193], v[200:203], v[50:53]
	v_mfma_f32_16x16x32_bf16 v[38:41], v[182:185], v[204:207], v[38:41]
	v_mfma_f32_16x16x32_bf16 v[34:37], v[190:193], v[204:207], v[34:37]
	v_mfma_f32_16x16x32_bf16 v[22:25], v[182:185], v[216:219], v[22:25]
	v_mfma_f32_16x16x32_bf16 v[18:21], v[190:193], v[216:219], v[18:21]
	v_mfma_f32_16x16x32_bf16 v[6:9], v[182:185], v[220:223], v[6:9]
	v_mfma_f32_16x16x32_bf16 v[2:5], v[190:193], v[220:223], v[2:5]
	v_mfma_f32_16x16x32_bf16 v[54:57], v[186:189], v[208:211], v[54:57]
	v_mfma_f32_16x16x32_bf16 v[50:53], v[194:197], v[208:211], v[50:53]
	v_mfma_f32_16x16x32_bf16 v[38:41], v[186:189], v[212:215], v[38:41]
	v_mfma_f32_16x16x32_bf16 v[34:37], v[194:197], v[212:215], v[34:37]
	v_mfma_f32_16x16x32_bf16 v[22:25], v[186:189], v[224:227], v[22:25]
	v_mfma_f32_16x16x32_bf16 v[18:21], v[194:197], v[224:227], v[18:21]
	v_mfma_f32_16x16x32_bf16 v[6:9], v[186:189], v[228:231], v[6:9]
	v_mfma_f32_16x16x32_bf16 v[2:5], v[194:197], v[228:231], v[2:5]
	s_setprio 0
	s_barrier
	s_add_i32 s2, 0, 0x18000
	v_add_u32_e32 v136, s2, v159
	v_add_u32_e32 v151, s2, v160
	ds_read_b128 v[166:169], v136
	ds_read_b128 v[170:173], v151
	v_add_u32_e32 v136, s47, v159
	s_add_i32 s55, 0, 0x1c000
	v_add_u32_e32 v151, s47, v160
	ds_read_b128 v[174:177], v136
	ds_read_b128 v[178:181], v151
	v_add_u32_e32 v136, s55, v159
	v_add_u32_e32 v151, s55, v160
	ds_read_b128 v[182:185], v136
	ds_read_b128 v[186:189], v151
	v_add_u32_e32 v136, s48, v159
	v_add_u32_e32 v151, s48, v160
	ds_read_b128 v[190:193], v136
	ds_read_b128 v[194:197], v151
	s_mov_b32 m0, s36
	ds_read_b128 v[200:203], v161 offset:32768
	ds_read_b128 v[204:207], v161 offset:34816
	ds_read_b128 v[208:211], v162 offset:32768
	ds_read_b128 v[212:215], v162 offset:34816
	ds_read_b128 v[216:219], v161 offset:36864
	ds_read_b128 v[220:223], v161 offset:38912
	ds_read_b128 v[224:227], v162 offset:36864
	ds_read_b128 v[228:231], v162 offset:38912
	global_load_lds_dwordx4 v145, s[26:27]
	s_mov_b32 m0, s37
	s_nop 0
	global_load_lds_dwordx4 v149, s[26:27]
	s_waitcnt vmcnt(8)
	s_waitcnt lgkmcnt(0)
	s_barrier
	s_setprio 1
	s_waitcnt lgkmcnt(0)
	v_mfma_f32_16x16x32_bf16 v[126:129], v[166:169], v[200:203], v[126:129]
	v_mfma_f32_16x16x32_bf16 v[122:125], v[174:177], v[200:203], v[122:125]
	v_mfma_f32_16x16x32_bf16 v[110:113], v[166:169], v[204:207], v[110:113]
	v_mfma_f32_16x16x32_bf16 v[106:109], v[174:177], v[204:207], v[106:109]
	v_mfma_f32_16x16x32_bf16 v[94:97], v[166:169], v[216:219], v[94:97]
	v_mfma_f32_16x16x32_bf16 v[90:93], v[174:177], v[216:219], v[90:93]
	v_mfma_f32_16x16x32_bf16 v[78:81], v[166:169], v[220:223], v[78:81]
	v_mfma_f32_16x16x32_bf16 v[74:77], v[174:177], v[220:223], v[74:77]
	v_mfma_f32_16x16x32_bf16 v[126:129], v[170:173], v[208:211], v[126:129]
	v_mfma_f32_16x16x32_bf16 v[122:125], v[178:181], v[208:211], v[122:125]
	v_mfma_f32_16x16x32_bf16 v[110:113], v[170:173], v[212:215], v[110:113]
	v_mfma_f32_16x16x32_bf16 v[106:109], v[178:181], v[212:215], v[106:109]
	v_mfma_f32_16x16x32_bf16 v[94:97], v[170:173], v[224:227], v[94:97]
	v_mfma_f32_16x16x32_bf16 v[90:93], v[178:181], v[224:227], v[90:93]
	v_mfma_f32_16x16x32_bf16 v[78:81], v[170:173], v[228:231], v[78:81]
	v_mfma_f32_16x16x32_bf16 v[74:77], v[178:181], v[228:231], v[74:77]
	v_mfma_f32_16x16x32_bf16 v[118:121], v[182:185], v[200:203], v[118:121]
	v_mfma_f32_16x16x32_bf16 v[114:117], v[190:193], v[200:203], v[114:117]
	v_mfma_f32_16x16x32_bf16 v[102:105], v[182:185], v[204:207], v[102:105]
	v_mfma_f32_16x16x32_bf16 v[98:101], v[190:193], v[204:207], v[98:101]
	v_mfma_f32_16x16x32_bf16 v[86:89], v[182:185], v[216:219], v[86:89]
	v_mfma_f32_16x16x32_bf16 v[82:85], v[190:193], v[216:219], v[82:85]
	v_mfma_f32_16x16x32_bf16 v[70:73], v[182:185], v[220:223], v[70:73]
	v_mfma_f32_16x16x32_bf16 v[66:69], v[190:193], v[220:223], v[66:69]
	v_mfma_f32_16x16x32_bf16 v[118:121], v[186:189], v[208:211], v[118:121]
	v_mfma_f32_16x16x32_bf16 v[114:117], v[194:197], v[208:211], v[114:117]
	v_mfma_f32_16x16x32_bf16 v[102:105], v[186:189], v[212:215], v[102:105]
	v_mfma_f32_16x16x32_bf16 v[98:101], v[194:197], v[212:215], v[98:101]
	v_mfma_f32_16x16x32_bf16 v[86:89], v[186:189], v[224:227], v[86:89]
	v_mfma_f32_16x16x32_bf16 v[82:85], v[194:197], v[224:227], v[82:85]
	v_mfma_f32_16x16x32_bf16 v[70:73], v[186:189], v[228:231], v[70:73]
	v_mfma_f32_16x16x32_bf16 v[66:69], v[194:197], v[228:231], v[66:69]
	s_setprio 0
	s_barrier
; #define PG8_STAGE(bufoff, gbase, voff) do { _Pragma("unroll") for (int _i = 0; _i < 2; ++_i) \
;         __builtin_amdgcn_global_load_lds((const unsigned*)((const char*)(gbase) + (voff)[_i]), (LAS unsigned*)(lds + (bufoff) + ldsw + _i * 8192), 16, 0, 0); } while (0)
; #define PG8_LDA(dst, b, h) do { _Pragma("unroll") for (int m = 0; m < 4; ++m) _Pragma("unroll") for (int k = 0; k < 2; ++k) dst[m][k] = *(const LAS bf16x8*)(lds + PG8_SA(b, h) + ((aoff ^ (k * 64)) + m * 2048)); } while (0)
; #define PG8_MMA(ai, bj, At, Bt) do { __builtin_amdgcn_s_setprio(1); _Pragma("unroll") for (int m = 0; m < 4; ++m) _Pragma("unroll") for (int n = 0; n < 2; ++n) _Pragma("unroll") for (int k = 0; k < 2; ++k) \
;         acc[ai][bj][m][n] = __builtin_amdgcn_mfma_f32_16x16x32_bf16(Bt[n][k], At[m][k], acc[ai][bj][m][n], 0, 0, 0); __builtin_amdgcn_s_setprio(0); } while (0)
; #define PG8_WAIT_V(n) asm volatile("s_waitcnt vmcnt(" #n ")" ::: "memory")
; #define PG8_WAIT_L(n) asm volatile("s_waitcnt lgkmcnt(" #n ")" ::: "memory")
; #define PG8_BAR __builtin_amdgcn_s_barrier()
; #define PG8_SCHED __builtin_amdgcn_sched_barrier(0)
;     ...
;             PG8_LDA(At, 1, 1); PG8_STAGE(PG8_SB(1, 0), b3, voffB); PG8_STAGE(PG8_SB(1, 1), b3 + hstep, voffB); PG8_STAGE(PG8_SA(1, 0), a3, vs[0]);
;             PG8_WAIT_V(8); PG8_WAIT_L(0); PG8_BAR; if (do1) { PG8_MMA(1, 0, At, B0); PG8_MMA(1, 1, At, B1); } PG8_BAR; PG8_SCHED;
;         }
	s_add_i32 s2, s2, s34
	v_lshl_add_u64 v[236:237], s[24:25], 0, v[132:133]
	s_mov_b32 m0, s2
	ds_read_b128 v[200:203], v161 offset:49152
	ds_read_b128 v[204:207], v161 offset:51200
	ds_read_b128 v[208:211], v162 offset:49152
	ds_read_b128 v[212:215], v162 offset:51200
	ds_read_b128 v[216:219], v161 offset:53248
	ds_read_b128 v[220:223], v161 offset:55296
	ds_read_b128 v[224:227], v162 offset:53248
	ds_read_b128 v[228:231], v162 offset:55296
	global_load_lds_dwordx4 v[236:237], off
	s_add_i32 m0, s2, 0x2000
	s_add_u32 s2, s22, 0x44000
	v_lshl_add_u64 v[236:237], s[24:25], 0, v[134:135]
	s_addc_u32 s3, s23, 0
	s_add_i32 s22, s55, s34
	global_load_lds_dwordx4 v[236:237], off
	v_lshl_add_u64 v[236:237], s[2:3], 0, v[132:133]
	s_mov_b32 m0, s22
	v_lshl_add_u64 v[234:235], v[234:235], 0, s[10:11]
	global_load_lds_dwordx4 v[236:237], off
	v_lshl_add_u64 v[236:237], s[2:3], 0, v[134:135]
	s_add_i32 m0, s22, 0x2000
	v_lshl_add_u64 v[232:233], v[232:233], 0, s[10:11]
	global_load_lds_dwordx4 v[236:237], off
	s_mov_b32 m0, s41
	s_nop 0
	global_load_lds_dwordx4 v[234:235], off
	s_mov_b32 m0, s42
	s_nop 0
	global_load_lds_dwordx4 v[232:233], off
	s_waitcnt vmcnt(8)
	s_waitcnt lgkmcnt(0)
	s_barrier
	s_setprio 1
	s_waitcnt lgkmcnt(0)
	v_mfma_f32_16x16x32_bf16 v[62:65], v[166:169], v[200:203], v[62:65]
	v_mfma_f32_16x16x32_bf16 v[58:61], v[174:177], v[200:203], v[58:61]
	v_mfma_f32_16x16x32_bf16 v[46:49], v[166:169], v[204:207], v[46:49]
	v_mfma_f32_16x16x32_bf16 v[42:45], v[174:177], v[204:207], v[42:45]
	v_mfma_f32_16x16x32_bf16 v[30:33], v[166:169], v[216:219], v[30:33]
	v_mfma_f32_16x16x32_bf16 v[26:29], v[174:177], v[216:219], v[26:29]
	v_mfma_f32_16x16x32_bf16 v[14:17], v[166:169], v[220:223], v[14:17]
	v_mfma_f32_16x16x32_bf16 v[10:13], v[174:177], v[220:223], v[10:13]
	v_mfma_f32_16x16x32_bf16 v[62:65], v[170:173], v[208:211], v[62:65]
	v_mfma_f32_16x16x32_bf16 v[58:61], v[178:181], v[208:211], v[58:61]
	v_mfma_f32_16x16x32_bf16 v[46:49], v[170:173], v[212:215], v[46:49]
	v_mfma_f32_16x16x32_bf16 v[42:45], v[178:181], v[212:215], v[42:45]
	v_mfma_f32_16x16x32_bf16 v[30:33], v[170:173], v[224:227], v[30:33]
	v_mfma_f32_16x16x32_bf16 v[26:29], v[178:181], v[224:227], v[26:29]
	v_mfma_f32_16x16x32_bf16 v[14:17], v[170:173], v[228:231], v[14:17]
	v_mfma_f32_16x16x32_bf16 v[10:13], v[178:181], v[228:231], v[10:13]
	v_mfma_f32_16x16x32_bf16 v[54:57], v[182:185], v[200:203], v[54:57]
	v_mfma_f32_16x16x32_bf16 v[50:53], v[190:193], v[200:203], v[50:53]
	v_mfma_f32_16x16x32_bf16 v[38:41], v[182:185], v[204:207], v[38:41]
	v_mfma_f32_16x16x32_bf16 v[34:37], v[190:193], v[204:207], v[34:37]
	v_mfma_f32_16x16x32_bf16 v[22:25], v[182:185], v[216:219], v[22:25]
	v_mfma_f32_16x16x32_bf16 v[18:21], v[190:193], v[216:219], v[18:21]
	v_mfma_f32_16x16x32_bf16 v[6:9], v[182:185], v[220:223], v[6:9]
	v_mfma_f32_16x16x32_bf16 v[2:5], v[190:193], v[220:223], v[2:5]
	v_mfma_f32_16x16x32_bf16 v[54:57], v[186:189], v[208:211], v[54:57]
	v_mfma_f32_16x16x32_bf16 v[50:53], v[194:197], v[208:211], v[50:53]
	v_mfma_f32_16x16x32_bf16 v[38:41], v[186:189], v[212:215], v[38:41]
	v_mfma_f32_16x16x32_bf16 v[34:37], v[194:197], v[212:215], v[34:37]
	v_mfma_f32_16x16x32_bf16 v[22:25], v[186:189], v[224:227], v[22:25]
	v_mfma_f32_16x16x32_bf16 v[18:21], v[194:197], v[224:227], v[18:21]
	v_mfma_f32_16x16x32_bf16 v[6:9], v[186:189], v[228:231], v[6:9]
	v_mfma_f32_16x16x32_bf16 v[2:5], v[194:197], v[228:231], v[2:5]
	s_setprio 0
	s_barrier
	s_add_i32 s54, s54, 2
	s_add_u32 s13, s13, 0x8000
	s_addc_u32 s53, s53, 0
	s_add_u32 s20, s20, 0x100
	s_addc_u32 s21, s21, 0
	s_cmp_gt_u32 s54, 13
	s_cbranch_scc1 .LBB0_2340

; #define PG8_STAGE(bufoff, gbase, voff) do { _Pragma("unroll") for (int _i = 0; _i < 2; ++_i) \
;         __builtin_amdgcn_global_load_lds((const unsigned*)((const char*)(gbase) + (voff)[_i]), (LAS unsigned*)(lds + (bufoff) + ldsw + _i * 8192), 16, 0, 0); } while (0)
; #define PG8_LDA(dst, b, h) do { _Pragma("unroll") for (int m = 0; m < 4; ++m) _Pragma("unroll") for (int k = 0; k < 2; ++k) dst[m][k] = *(const LAS bf16x8*)(lds + PG8_SA(b, h) + ((aoff ^ (k * 64)) + m * 2048)); } while (0)
; #define PG8_LDB(dst, b, h) do { _Pragma("unroll") for (int n = 0; n < 2; ++n) _Pragma("unroll") for (int k = 0; k < 2; ++k) dst[n][k] = *(const LAS bf16x8*)(lds + PG8_SB(b, h) + ((boff ^ (k * 64)) + n * 2048)); } while (0)
; #define PG8_WAIT_V(n) asm volatile("s_waitcnt vmcnt(" #n ")" ::: "memory")
; #define PG8_WAIT_L(n) asm volatile("s_waitcnt lgkmcnt(" #n ")" ::: "memory")
;     ...
;             const bool last = (t == nt - 2);
;             const char* a1 = cA + (size_t)(t + 1) * kstepA;
;             const char* a2 = last ? nA : cA + (size_t)(t + 2) * kstepA; const char* b2 = last ? nB : cB + (size_t)(t + 2) * kstepB;
;             const char* a3 = a2 + kstepA; const char* b3 = b2 + kstepB;
;             unsigned vs[2][2];
;             if constexpr (GATHER) {
;                 if (last && has_next) {
; #pragma unroll
;                     for (int hh = 0; hh < 2; ++hh)
; #pragma unroll
;                         for (int i = 0; i < 2; ++i) voffN[hh][i] = (unsigned)idxl[(ui + 1) * 256 + hh * HALF + sR[i]] * (unsigned)(K * 2) + (unsigned)sC[i] * 2u;
;                 }
; #pragma unroll
;                 for (int hh = 0; hh < 2; ++hh)
; #pragma unroll
;                     for (int i = 0; i < 2; ++i) vs[hh][i] = last ? voffN[hh][i] : voffA[hh][i];
;             } else {
; #pragma unroll
;                 for (int hh = 0; hh < 2; ++hh)
; #pragma unroll
;                     for (int i = 0; i < 2; ++i) vs[hh][i] = voffA[hh][i];
;             }
;             PG8_LDB(B0, 0, 0); PG8_LDB(B1, 0, 1); PG8_SCHED; PG8_LDA(At, 0, 0); PG8_STAGE(PG8_SA(1, 1), a1, voffA[1]);
;             PG8_WAIT_V(8); PG8_WAIT_L(0); PG8_BAR; if (do0) { PG8_MMA(0, 0, At, B0); PG8_MMA(0, 1, At, B1); } PG8_BAR; PG8_SCHED;
;             PG8_LDA(At, 0, 1); PG8_STAGE(PG8_SB(0, 0), b2, voffB); PG8_STAGE(PG8_SB(0, 1), b2 + hstep, voffB); PG8_STAGE(PG8_SA(0, 0), a2, vs[0]);
.LBB0_2411:
	ds_read_b128 v[146:149], v153
	ds_read_b128 v[168:171], v154
	ds_read_b128 v[172:175], v155
	ds_read_b128 v[176:179], v156
	ds_read_b128 v[180:183], v157
	ds_read_b128 v[184:187], v158
	ds_read_b128 v[188:191], v159
	ds_read_b128 v[192:195], v160
	s_add_u32 s20, s18, 0x4000
	s_addc_u32 s21, s19, 0
	s_cmp_eq_u32 s56, 40
	s_cselect_b32 s26, s14, s20
	s_cselect_b32 s27, s15, s21
	s_cselect_b32 s22, s16, s54
	s_cselect_b32 s23, s17, s55
	s_add_u32 s20, s26, 0x4000
	s_addc_u32 s21, s27, 0
	v_lshl_add_u64 v[196:197], s[18:19], 0, v[142:143]
	s_add_i32 m0, s34, 0xc000
	ds_read_b128 v[200:203], v161
	ds_read_b128 v[204:207], v161 offset:2048
	ds_read_b128 v[208:211], v162
	ds_read_b128 v[212:215], v162 offset:2048
	ds_read_b128 v[216:219], v161 offset:4096
	ds_read_b128 v[220:223], v161 offset:6144
	ds_read_b128 v[224:227], v162 offset:4096
	ds_read_b128 v[228:231], v162 offset:6144
	global_load_lds_dwordx4 v[196:197], off
	v_lshl_add_u64 v[196:197], s[18:19], 0, v[144:145]
	s_add_i32 m0, s34, 0xe000
	s_add_u32 s24, s22, 0x4000
	global_load_lds_dwordx4 v[196:197], off
	s_waitcnt vmcnt(8)
	s_waitcnt lgkmcnt(0)
	s_addc_u32 s25, s23, 0
	s_barrier
	s_setprio 1
	s_waitcnt lgkmcnt(0)
	v_mfma_f32_16x16x32_bf16 v[126:129], v[146:149], v[200:203], v[126:129]
	v_mfma_f32_16x16x32_bf16 v[122:125], v[172:175], v[200:203], v[122:125]
	v_mfma_f32_16x16x32_bf16 v[114:117], v[146:149], v[204:207], v[114:117]
	v_mfma_f32_16x16x32_bf16 v[106:109], v[172:175], v[204:207], v[106:109]
	v_mfma_f32_16x16x32_bf16 v[98:101], v[146:149], v[216:219], v[98:101]
	v_mfma_f32_16x16x32_bf16 v[90:93], v[172:175], v[216:219], v[90:93]
	v_mfma_f32_16x16x32_bf16 v[82:85], v[146:149], v[220:223], v[82:85]
	v_mfma_f32_16x16x32_bf16 v[74:77], v[172:175], v[220:223], v[74:77]
	v_mfma_f32_16x16x32_bf16 v[126:129], v[168:171], v[208:211], v[126:129]
	v_mfma_f32_16x16x32_bf16 v[122:125], v[176:179], v[208:211], v[122:125]
	v_mfma_f32_16x16x32_bf16 v[114:117], v[168:171], v[212:215], v[114:117]
	v_mfma_f32_16x16x32_bf16 v[106:109], v[176:179], v[212:215], v[106:109]
	v_mfma_f32_16x16x32_bf16 v[98:101], v[168:171], v[224:227], v[98:101]
	v_mfma_f32_16x16x32_bf16 v[90:93], v[176:179], v[224:227], v[90:93]
	v_mfma_f32_16x16x32_bf16 v[82:85], v[168:171], v[228:231], v[82:85]
	v_mfma_f32_16x16x32_bf16 v[74:77], v[176:179], v[228:231], v[74:77]
	v_mfma_f32_16x16x32_bf16 v[118:121], v[180:183], v[200:203], v[118:121]
	v_mfma_f32_16x16x32_bf16 v[110:113], v[188:191], v[200:203], v[110:113]
	v_mfma_f32_16x16x32_bf16 v[102:105], v[180:183], v[204:207], v[102:105]
	v_mfma_f32_16x16x32_bf16 v[94:97], v[188:191], v[204:207], v[94:97]
	v_mfma_f32_16x16x32_bf16 v[86:89], v[180:183], v[216:219], v[86:89]
	v_mfma_f32_16x16x32_bf16 v[78:81], v[188:191], v[216:219], v[78:81]
	v_mfma_f32_16x16x32_bf16 v[70:73], v[180:183], v[220:223], v[70:73]
	v_mfma_f32_16x16x32_bf16 v[66:69], v[188:191], v[220:223], v[66:69]
	v_mfma_f32_16x16x32_bf16 v[118:121], v[184:187], v[208:211], v[118:121]
	v_mfma_f32_16x16x32_bf16 v[110:113], v[192:195], v[208:211], v[110:113]
	v_mfma_f32_16x16x32_bf16 v[102:105], v[184:187], v[212:215], v[102:105]
	v_mfma_f32_16x16x32_bf16 v[94:97], v[192:195], v[212:215], v[94:97]
	v_mfma_f32_16x16x32_bf16 v[86:89], v[184:187], v[224:227], v[86:89]
	v_mfma_f32_16x16x32_bf16 v[78:81], v[192:195], v[224:227], v[78:81]
	v_mfma_f32_16x16x32_bf16 v[70:73], v[184:187], v[228:231], v[70:73]
	v_mfma_f32_16x16x32_bf16 v[66:69], v[192:195], v[228:231], v[66:69]
	s_setprio 0
	s_barrier
	s_add_i32 s57, s42, s30
	v_lshl_add_u64 v[196:197], s[22:23], 0, v[132:133]
	s_mov_b32 m0, s57
	ds_read_b128 v[200:203], v161 offset:16384
	ds_read_b128 v[204:207], v161 offset:18432
	ds_read_b128 v[208:211], v162 offset:16384
	ds_read_b128 v[212:215], v162 offset:18432
	ds_read_b128 v[216:219], v161 offset:20480
	ds_read_b128 v[220:223], v161 offset:22528
	ds_read_b128 v[224:227], v162 offset:20480
	ds_read_b128 v[228:231], v162 offset:22528
	global_load_lds_dwordx4 v[196:197], off
	s_add_i32 m0, s57, 0x2000
	s_add_u32 s58, s22, 0xb0000
	v_lshl_add_u64 v[196:197], s[22:23], 0, v[130:131]
	s_addc_u32 s59, s23, 0
	s_add_i32 s57, s43, s30
	global_load_lds_dwordx4 v[196:197], off
	v_lshl_add_u64 v[196:197], s[58:59], 0, v[132:133]
	s_mov_b32 m0, s57
	s_nop 0
	global_load_lds_dwordx4 v[196:197], off
	v_lshl_add_u64 v[196:197], s[58:59], 0, v[130:131]
	s_add_i32 m0, s57, 0x2000
	s_nop 0
	global_load_lds_dwordx4 v[196:197], off
	v_lshl_add_u64 v[196:197], s[26:27], 0, v[134:135]
	s_mov_b32 m0, s34
	s_nop 0
	global_load_lds_dwordx4 v[196:197], off
	v_lshl_add_u64 v[196:197], s[26:27], 0, v[136:137]
	s_mov_b32 m0, s35
	s_nop 0
	global_load_lds_dwordx4 v[196:197], off
	s_waitcnt vmcnt(8)
	s_waitcnt lgkmcnt(0)
	s_barrier
; #define PG8_STAGE(bufoff, gbase, voff) do { _Pragma("unroll") for (int _i = 0; _i < 2; ++_i) \
;         __builtin_amdgcn_global_load_lds((const unsigned*)((const char*)(gbase) + (voff)[_i]), (LAS unsigned*)(lds + (bufoff) + ldsw + _i * 8192), 16, 0, 0); } while (0)
; #define PG8_LDA(dst, b, h) do { _Pragma("unroll") for (int m = 0; m < 4; ++m) _Pragma("unroll") for (int k = 0; k < 2; ++k) dst[m][k] = *(const LAS bf16x8*)(lds + PG8_SA(b, h) + ((aoff ^ (k * 64)) + m * 2048)); } while (0)
; #define PG8_LDB(dst, b, h) do { _Pragma("unroll") for (int n = 0; n < 2; ++n) _Pragma("unroll") for (int k = 0; k < 2; ++k) dst[n][k] = *(const LAS bf16x8*)(lds + PG8_SB(b, h) + ((boff ^ (k * 64)) + n * 2048)); } while (0)
; #define PG8_MMA(ai, bj, At, Bt) do { __builtin_amdgcn_s_setprio(1); _Pragma("unroll") for (int m = 0; m < 4; ++m) _Pragma("unroll") for (int n = 0; n < 2; ++n) _Pragma("unroll") for (int k = 0; k < 2; ++k) \
;         acc[ai][bj][m][n] = __builtin_amdgcn_mfma_f32_16x16x32_bf16(Bt[n][k], At[m][k], acc[ai][bj][m][n], 0, 0, 0); __builtin_amdgcn_s_setprio(0); } while (0)
; #define PG8_WAIT_V(n) asm volatile("s_waitcnt vmcnt(" #n ")" ::: "memory")
; #define PG8_WAIT_L(n) asm volatile("s_waitcnt lgkmcnt(" #n ")" ::: "memory")
; #define PG8_BAR __builtin_amdgcn_s_barrier()
; #define PG8_SCHED __builtin_amdgcn_sched_barrier(0)
;     ...
;             PG8_WAIT_V(8); PG8_WAIT_L(0); PG8_BAR; if (do1) { PG8_MMA(1, 0, At, B0); PG8_MMA(1, 1, At, B1); } PG8_BAR; PG8_SCHED;
;             PG8_LDB(B0, 1, 0); PG8_LDB(B1, 1, 1); PG8_SCHED; PG8_LDA(At, 1, 0); PG8_STAGE(PG8_SA(0, 1), a2, vs[1]);
;             PG8_WAIT_V(8); PG8_WAIT_L(0); PG8_BAR; if (do0) { PG8_MMA(0, 0, At, B0); PG8_MMA(0, 1, At, B1); } PG8_BAR; PG8_SCHED;
	s_setprio 1
	s_waitcnt lgkmcnt(0)
	v_mfma_f32_16x16x32_bf16 v[62:65], v[146:149], v[200:203], v[62:65]
	v_mfma_f32_16x16x32_bf16 v[58:61], v[172:175], v[200:203], v[58:61]
	v_mfma_f32_16x16x32_bf16 v[46:49], v[146:149], v[204:207], v[46:49]
	v_mfma_f32_16x16x32_bf16 v[42:45], v[172:175], v[204:207], v[42:45]
	v_mfma_f32_16x16x32_bf16 v[30:33], v[146:149], v[216:219], v[30:33]
	v_mfma_f32_16x16x32_bf16 v[26:29], v[172:175], v[216:219], v[26:29]
	v_mfma_f32_16x16x32_bf16 v[14:17], v[146:149], v[220:223], v[14:17]
	v_mfma_f32_16x16x32_bf16 v[10:13], v[172:175], v[220:223], v[10:13]
	v_mfma_f32_16x16x32_bf16 v[62:65], v[168:171], v[208:211], v[62:65]
	v_mfma_f32_16x16x32_bf16 v[58:61], v[176:179], v[208:211], v[58:61]
	v_mfma_f32_16x16x32_bf16 v[46:49], v[168:171], v[212:215], v[46:49]
	v_mfma_f32_16x16x32_bf16 v[42:45], v[176:179], v[212:215], v[42:45]
	v_mfma_f32_16x16x32_bf16 v[30:33], v[168:171], v[224:227], v[30:33]
	v_mfma_f32_16x16x32_bf16 v[26:29], v[176:179], v[224:227], v[26:29]
	v_mfma_f32_16x16x32_bf16 v[14:17], v[168:171], v[228:231], v[14:17]
	v_mfma_f32_16x16x32_bf16 v[10:13], v[176:179], v[228:231], v[10:13]
	v_mfma_f32_16x16x32_bf16 v[54:57], v[180:183], v[200:203], v[54:57]
	v_mfma_f32_16x16x32_bf16 v[50:53], v[188:191], v[200:203], v[50:53]
	v_mfma_f32_16x16x32_bf16 v[38:41], v[180:183], v[204:207], v[38:41]
	v_mfma_f32_16x16x32_bf16 v[34:37], v[188:191], v[204:207], v[34:37]
	v_mfma_f32_16x16x32_bf16 v[22:25], v[180:183], v[216:219], v[22:25]
	v_mfma_f32_16x16x32_bf16 v[18:21], v[188:191], v[216:219], v[18:21]
	v_mfma_f32_16x16x32_bf16 v[6:9], v[180:183], v[220:223], v[6:9]
	v_mfma_f32_16x16x32_bf16 v[2:5], v[188:191], v[220:223], v[2:5]
	v_mfma_f32_16x16x32_bf16 v[54:57], v[184:187], v[208:211], v[54:57]
	v_mfma_f32_16x16x32_bf16 v[50:53], v[192:195], v[208:211], v[50:53]
	v_mfma_f32_16x16x32_bf16 v[38:41], v[184:187], v[212:215], v[38:41]
	v_mfma_f32_16x16x32_bf16 v[34:37], v[192:195], v[212:215], v[34:37]
	v_mfma_f32_16x16x32_bf16 v[22:25], v[184:187], v[224:227], v[22:25]
	v_mfma_f32_16x16x32_bf16 v[18:21], v[192:195], v[224:227], v[18:21]
	v_mfma_f32_16x16x32_bf16 v[6:9], v[184:187], v[228:231], v[6:9]
	v_mfma_f32_16x16x32_bf16 v[2:5], v[192:195], v[228:231], v[2:5]
	s_setprio 0
	s_barrier
	s_add_i32 s57, 0, 0x18000
	v_add_u32_e32 v146, s57, v150
	v_add_u32_e32 v167, s57, v151
	s_add_i32 s58, 0, 0x1c000
	ds_read_b128 v[146:149], v146
	ds_read_b128 v[168:171], v167
	ds_read_b128 v[172:175], v163
	ds_read_b128 v[176:179], v164
	v_add_u32_e32 v167, s58, v150
	v_add_u32_e32 v184, s58, v151
	ds_read_b128 v[180:183], v167
	ds_read_b128 v[184:187], v184
	ds_read_b128 v[188:191], v165
	ds_read_b128 v[192:195], v166
	s_mov_b32 m0, s36
	v_lshl_add_u64 v[196:197], s[26:27], 0, v[138:139]
	ds_read_b128 v[200:203], v161 offset:32768
	ds_read_b128 v[204:207], v161 offset:34816
	ds_read_b128 v[208:211], v162 offset:32768
	ds_read_b128 v[212:215], v162 offset:34816
	ds_read_b128 v[216:219], v161 offset:36864
	ds_read_b128 v[220:223], v161 offset:38912
	ds_read_b128 v[224:227], v162 offset:36864
	ds_read_b128 v[228:231], v162 offset:38912
	global_load_lds_dwordx4 v[196:197], off
	v_lshl_add_u64 v[196:197], s[26:27], 0, v[140:141]
	s_mov_b32 m0, s37
	s_nop 0
	global_load_lds_dwordx4 v[196:197], off
	s_waitcnt vmcnt(8)
	s_waitcnt lgkmcnt(0)
	s_barrier
	s_setprio 1
	s_waitcnt lgkmcnt(0)
	v_mfma_f32_16x16x32_bf16 v[126:129], v[146:149], v[200:203], v[126:129]
	v_mfma_f32_16x16x32_bf16 v[122:125], v[172:175], v[200:203], v[122:125]
	v_mfma_f32_16x16x32_bf16 v[114:117], v[146:149], v[204:207], v[114:117]
	v_mfma_f32_16x16x32_bf16 v[106:109], v[172:175], v[204:207], v[106:109]
	v_mfma_f32_16x16x32_bf16 v[98:101], v[146:149], v[216:219], v[98:101]
	v_mfma_f32_16x16x32_bf16 v[90:93], v[172:175], v[216:219], v[90:93]
	v_mfma_f32_16x16x32_bf16 v[82:85], v[146:149], v[220:223], v[82:85]
	v_mfma_f32_16x16x32_bf16 v[74:77], v[172:175], v[220:223], v[74:77]
	v_mfma_f32_16x16x32_bf16 v[126:129], v[168:171], v[208:211], v[126:129]
	v_mfma_f32_16x16x32_bf16 v[122:125], v[176:179], v[208:211], v[122:125]
	v_mfma_f32_16x16x32_bf16 v[114:117], v[168:171], v[212:215], v[114:117]
	v_mfma_f32_16x16x32_bf16 v[106:109], v[176:179], v[212:215], v[106:109]
	v_mfma_f32_16x16x32_bf16 v[98:101], v[168:171], v[224:227], v[98:101]
	v_mfma_f32_16x16x32_bf16 v[90:93], v[176:179], v[224:227], v[90:93]
	v_mfma_f32_16x16x32_bf16 v[82:85], v[168:171], v[228:231], v[82:85]
	v_mfma_f32_16x16x32_bf16 v[74:77], v[176:179], v[228:231], v[74:77]
	v_mfma_f32_16x16x32_bf16 v[118:121], v[180:183], v[200:203], v[118:121]
	v_mfma_f32_16x16x32_bf16 v[110:113], v[188:191], v[200:203], v[110:113]
	v_mfma_f32_16x16x32_bf16 v[102:105], v[180:183], v[204:207], v[102:105]
	v_mfma_f32_16x16x32_bf16 v[94:97], v[188:191], v[204:207], v[94:97]
	v_mfma_f32_16x16x32_bf16 v[86:89], v[180:183], v[216:219], v[86:89]
	v_mfma_f32_16x16x32_bf16 v[78:81], v[188:191], v[216:219], v[78:81]
	v_mfma_f32_16x16x32_bf16 v[70:73], v[180:183], v[220:223], v[70:73]
	v_mfma_f32_16x16x32_bf16 v[66:69], v[188:191], v[220:223], v[66:69]
	v_mfma_f32_16x16x32_bf16 v[118:121], v[184:187], v[208:211], v[118:121]
	v_mfma_f32_16x16x32_bf16 v[110:113], v[192:195], v[208:211], v[110:113]
	v_mfma_f32_16x16x32_bf16 v[102:105], v[184:187], v[212:215], v[102:105]
	v_mfma_f32_16x16x32_bf16 v[94:97], v[192:195], v[212:215], v[94:97]
	v_mfma_f32_16x16x32_bf16 v[86:89], v[184:187], v[224:227], v[86:89]
	v_mfma_f32_16x16x32_bf16 v[78:81], v[192:195], v[224:227], v[78:81]
	v_mfma_f32_16x16x32_bf16 v[70:73], v[184:187], v[228:231], v[70:73]
	v_mfma_f32_16x16x32_bf16 v[66:69], v[192:195], v[228:231], v[66:69]
	s_setprio 0
	s_barrier
; #define PG8_STAGE(bufoff, gbase, voff) do { _Pragma("unroll") for (int _i = 0; _i < 2; ++_i) \
;         __builtin_amdgcn_global_load_lds((const unsigned*)((const char*)(gbase) + (voff)[_i]), (LAS unsigned*)(lds + (bufoff) + ldsw + _i * 8192), 16, 0, 0); } while (0)
; #define PG8_LDA(dst, b, h) do { _Pragma("unroll") for (int m = 0; m < 4; ++m) _Pragma("unroll") for (int k = 0; k < 2; ++k) dst[m][k] = *(const LAS bf16x8*)(lds + PG8_SA(b, h) + ((aoff ^ (k * 64)) + m * 2048)); } while (0)
; #define PG8_MMA(ai, bj, At, Bt) do { __builtin_amdgcn_s_setprio(1); _Pragma("unroll") for (int m = 0; m < 4; ++m) _Pragma("unroll") for (int n = 0; n < 2; ++n) _Pragma("unroll") for (int k = 0; k < 2; ++k) \
;         acc[ai][bj][m][n] = __builtin_amdgcn_mfma_f32_16x16x32_bf16(Bt[n][k], At[m][k], acc[ai][bj][m][n], 0, 0, 0); __builtin_amdgcn_s_setprio(0); } while (0)
; #define PG8_WAIT_V(n) asm volatile("s_waitcnt vmcnt(" #n ")" ::: "memory")
; #define PG8_WAIT_L(n) asm volatile("s_waitcnt lgkmcnt(" #n ")" ::: "memory")
; #define PG8_BAR __builtin_amdgcn_s_barrier()
; #define PG8_SCHED __builtin_amdgcn_sched_barrier(0)
;     ...
;             PG8_LDA(At, 1, 1); PG8_STAGE(PG8_SB(1, 0), b3, voffB); PG8_STAGE(PG8_SB(1, 1), b3 + hstep, voffB); PG8_STAGE(PG8_SA(1, 0), a3, vs[0]);
;             PG8_WAIT_V(8); PG8_WAIT_L(0); PG8_BAR; if (do1) { PG8_MMA(1, 0, At, B0); PG8_MMA(1, 1, At, B1); } PG8_BAR; PG8_SCHED;
;         }
;         if (wr == 0) PG8_BAR;
	s_add_i32 s26, s57, s30
	v_lshl_add_u64 v[196:197], s[24:25], 0, v[132:133]
	s_mov_b32 m0, s26
	ds_read_b128 v[200:203], v161 offset:49152
	ds_read_b128 v[204:207], v161 offset:51200
	ds_read_b128 v[208:211], v162 offset:49152
	ds_read_b128 v[212:215], v162 offset:51200
	ds_read_b128 v[216:219], v161 offset:53248
	ds_read_b128 v[220:223], v161 offset:55296
	ds_read_b128 v[224:227], v162 offset:53248
	ds_read_b128 v[228:231], v162 offset:55296
	global_load_lds_dwordx4 v[196:197], off
	s_add_i32 m0, s26, 0x2000
	s_add_u32 s22, s22, 0xb4000
	v_lshl_add_u64 v[196:197], s[24:25], 0, v[130:131]
	s_addc_u32 s23, s23, 0
	s_add_i32 s24, s58, s30
	global_load_lds_dwordx4 v[196:197], off
	v_lshl_add_u64 v[196:197], s[22:23], 0, v[132:133]
	s_mov_b32 m0, s24
	s_nop 0
	global_load_lds_dwordx4 v[196:197], off
	v_lshl_add_u64 v[196:197], s[22:23], 0, v[130:131]
	s_add_i32 m0, s24, 0x2000
	s_nop 0
	global_load_lds_dwordx4 v[196:197], off
	v_lshl_add_u64 v[196:197], s[20:21], 0, v[134:135]
	s_mov_b32 m0, s39
	s_nop 0
	global_load_lds_dwordx4 v[196:197], off
	v_lshl_add_u64 v[196:197], s[20:21], 0, v[136:137]
	s_mov_b32 m0, s40
	s_nop 0
	global_load_lds_dwordx4 v[196:197], off
	s_waitcnt vmcnt(8)
	s_waitcnt lgkmcnt(0)
	s_barrier
	s_setprio 1
	s_waitcnt lgkmcnt(0)
	v_mfma_f32_16x16x32_bf16 v[62:65], v[146:149], v[200:203], v[62:65]
	v_mfma_f32_16x16x32_bf16 v[58:61], v[172:175], v[200:203], v[58:61]
	v_mfma_f32_16x16x32_bf16 v[46:49], v[146:149], v[204:207], v[46:49]
	v_mfma_f32_16x16x32_bf16 v[42:45], v[172:175], v[204:207], v[42:45]
	v_mfma_f32_16x16x32_bf16 v[30:33], v[146:149], v[216:219], v[30:33]
	v_mfma_f32_16x16x32_bf16 v[26:29], v[172:175], v[216:219], v[26:29]
	v_mfma_f32_16x16x32_bf16 v[14:17], v[146:149], v[220:223], v[14:17]
	v_mfma_f32_16x16x32_bf16 v[10:13], v[172:175], v[220:223], v[10:13]
	v_mfma_f32_16x16x32_bf16 v[62:65], v[168:171], v[208:211], v[62:65]
	v_mfma_f32_16x16x32_bf16 v[58:61], v[176:179], v[208:211], v[58:61]
	v_mfma_f32_16x16x32_bf16 v[46:49], v[168:171], v[212:215], v[46:49]
	v_mfma_f32_16x16x32_bf16 v[42:45], v[176:179], v[212:215], v[42:45]
	v_mfma_f32_16x16x32_bf16 v[30:33], v[168:171], v[224:227], v[30:33]
	v_mfma_f32_16x16x32_bf16 v[26:29], v[176:179], v[224:227], v[26:29]
	v_mfma_f32_16x16x32_bf16 v[14:17], v[168:171], v[228:231], v[14:17]
	v_mfma_f32_16x16x32_bf16 v[10:13], v[176:179], v[228:231], v[10:13]
	v_mfma_f32_16x16x32_bf16 v[54:57], v[180:183], v[200:203], v[54:57]
	v_mfma_f32_16x16x32_bf16 v[50:53], v[188:191], v[200:203], v[50:53]
	v_mfma_f32_16x16x32_bf16 v[38:41], v[180:183], v[204:207], v[38:41]
	v_mfma_f32_16x16x32_bf16 v[34:37], v[188:191], v[204:207], v[34:37]
	v_mfma_f32_16x16x32_bf16 v[22:25], v[180:183], v[216:219], v[22:25]
	v_mfma_f32_16x16x32_bf16 v[18:21], v[188:191], v[216:219], v[18:21]
	v_mfma_f32_16x16x32_bf16 v[6:9], v[180:183], v[220:223], v[6:9]
	v_mfma_f32_16x16x32_bf16 v[2:5], v[188:191], v[220:223], v[2:5]
	v_mfma_f32_16x16x32_bf16 v[54:57], v[184:187], v[208:211], v[54:57]
	v_mfma_f32_16x16x32_bf16 v[50:53], v[192:195], v[208:211], v[50:53]
	v_mfma_f32_16x16x32_bf16 v[38:41], v[184:187], v[212:215], v[38:41]
	v_mfma_f32_16x16x32_bf16 v[34:37], v[192:195], v[212:215], v[34:37]
	v_mfma_f32_16x16x32_bf16 v[22:25], v[184:187], v[224:227], v[22:25]
	v_mfma_f32_16x16x32_bf16 v[18:21], v[192:195], v[224:227], v[18:21]
	v_mfma_f32_16x16x32_bf16 v[6:9], v[184:187], v[228:231], v[6:9]
	v_mfma_f32_16x16x32_bf16 v[2:5], v[192:195], v[228:231], v[2:5]
	s_setprio 0
	s_barrier
	s_add_i32 s56, s56, 2
	s_add_u32 s18, s18, 0x8000
	s_addc_u32 s19, s19, 0
	s_add_u32 s54, s54, 0x8000
	s_addc_u32 s55, s55, 0
	s_cmp_gt_u32 s56, 41
	s_cbranch_scc0 .LBB0_2411
	s_and_b64 vcc, exec, s[4:5]
	s_cbranch_vccz .LBB0_2414
	s_barrier
